# leading half-workgroup starts its GEMM epilogue during the trailing half's last MFMA block (its pre-epilogue barrier moved into the epilogue)
# speedup vs baseline: 1.0007x; 1.0007x over previous
; #define PG8_STAGE(bufoff, gbase, voff) do { _Pragma("unroll") for (int _i = 0; _i < 2; ++_i) \
;         __builtin_amdgcn_global_load_lds((const unsigned*)((const char*)(gbase) + (voff)[_i]), (PG8_LAS unsigned*)(lds + (bufoff) + ldsw + _i * 8192), 16, 0, 0); } while (0)
; #define PG8_LDA(dst, b, h) do { _Pragma("unroll") for (int m = 0; m < 4; ++m) _Pragma("unroll") for (int k = 0; k < 2; ++k) dst[m][k] = *(const PG8_LAS bf16x8*)(lds + PG8_SA(b, h) + aoff + m * 2048 + k * 1024); } while (0)
; #define PG8_LDB(dst, b, h) do { _Pragma("unroll") for (int n = 0; n < 2; ++n) _Pragma("unroll") for (int k = 0; k < 2; ++k) dst[n][k] = *(const PG8_LAS bf16x8*)(lds + PG8_SB(b, h) + boff + n * 2048 + k * 1024); } while (0)
; #define PG8_WAIT_V(n) asm volatile("s_waitcnt vmcnt(" #n ")" ::: "memory")
; #define PG8_WAIT_L(n) asm volatile("s_waitcnt lgkmcnt(" #n ")" ::: "memory")
; #define PG8_BAR __builtin_amdgcn_s_barrier()
; #define PG8_SCHED __builtin_amdgcn_sched_barrier(0)
; template <class Epi, class Sched, bool ALIGN_EPI = false, bool SP2 = false>
; __device__ __forceinline__ void gemm_phase(PG8_LAS unsigned char* lds, const Gemm g, const Sched& S, const Epi& E) {
;     ...
;             PG8_LDB(B0, 0, 0); PG8_LDB(B1, 0, 1); PG8_SCHED; PG8_LDA(At, 0, 0); PG8_STAGE(PG8_SA(1, 1), a1 + hstep, voffA);
;             PG8_WAIT_V(8); PG8_WAIT_L(0); PG8_BAR; PG8_MMA(0, 0, At, B0); PG8_MMA(0, 1, At, B1); PG8_BAR; PG8_SCHED;
;             PG8_LDA(At, 0, 1); PG8_STAGE(PG8_SB(0, 0), b2, voffB); PG8_STAGE(PG8_SB(0, 1), b2 + hstep, voffB); PG8_STAGE(PG8_SA(0, 0), a2, voffA);
;             PG8_WAIT_V(8); PG8_WAIT_L(0); PG8_BAR; PG8_MMA(1, 0, At, B0); PG8_MMA(1, 1, At, B1); PG8_BAR; PG8_SCHED;
;             PG8_LDB(B0, 1, 0); PG8_LDB(B1, 1, 1); PG8_SCHED; PG8_LDA(At, 1, 0); PG8_STAGE(PG8_SA(0, 1), a2 + hstep, voffA);
;             PG8_WAIT_V(8); PG8_WAIT_L(0); PG8_BAR; PG8_MMA(0, 0, At, B0); PG8_MMA(0, 1, At, B1); PG8_BAR; PG8_SCHED;
;             PG8_LDA(At, 1, 1); PG8_STAGE(PG8_SB(1, 0), b3, voffB); PG8_STAGE(PG8_SB(1, 1), b3 + hstep, voffB); PG8_STAGE(PG8_SA(1, 0), a3, voffA);
;             PG8_WAIT_V(8); PG8_WAIT_L(0); PG8_BAR; PG8_MMA(1, 0, At, B0); PG8_MMA(1, 1, At, B1); PG8_BAR; PG8_SCHED;
.LBB0_747:
	ds_read_b128 v[130:133], v218
	ds_read_b128 v[134:137], v218 offset:1024
	ds_read_b128 v[138:141], v218 offset:2048
	ds_read_b128 v[142:145], v218 offset:3072
	ds_read_b128 v[146:149], v219
	ds_read_b128 v[150:153], v219 offset:1024
	ds_read_b128 v[154:157], v219 offset:2048
	ds_read_b128 v[158:161], v219 offset:3072
	s_add_u32 s30, s28, 0xfff80080
	s_addc_u32 s31, s29, -1
	s_cmp_eq_u32 s62, 28
	s_cselect_b32 s35, s21, s31
	s_cselect_b32 s34, s58, s30
	s_cselect_b32 s31, s19, s61
	s_cselect_b32 s30, s59, s60
	s_add_i32 m0, s27, 0xc000
	ds_read_b128 v[162:165], v220
	ds_read_b128 v[166:169], v220 offset:1024
	ds_read_b128 v[170:173], v220 offset:2048
	ds_read_b128 v[174:177], v220 offset:3072
	ds_read_b128 v[178:181], v220 offset:4096
	ds_read_b128 v[182:185], v220 offset:5120
	ds_read_b128 v[206:209], v220 offset:6144
	ds_read_b128 v[222:225], v220 offset:7168
	global_load_lds_dwordx4 v198, s[28:29]
	s_add_i32 m0, s27, 0xe000
	s_nop 0
	global_load_lds_dwordx4 v200, s[28:29]
	s_waitcnt vmcnt(8)
	s_waitcnt lgkmcnt(0)
	s_barrier
	s_setprio 1
	s_waitcnt lgkmcnt(0)
	v_mfma_f32_16x16x32_bf16 v[126:129], v[130:133], v[162:165], v[126:129]
	v_mfma_f32_16x16x32_bf16 v[122:125], v[138:141], v[162:165], v[122:125]
	v_mfma_f32_16x16x32_bf16 v[118:121], v[130:133], v[170:173], v[118:121]
	v_mfma_f32_16x16x32_bf16 v[110:113], v[138:141], v[170:173], v[110:113]
	v_mfma_f32_16x16x32_bf16 v[94:97], v[130:133], v[178:181], v[94:97]
	v_mfma_f32_16x16x32_bf16 v[90:93], v[138:141], v[178:181], v[90:93]
	v_mfma_f32_16x16x32_bf16 v[82:85], v[130:133], v[206:209], v[82:85]
	v_mfma_f32_16x16x32_bf16 v[74:77], v[138:141], v[206:209], v[74:77]
	v_mfma_f32_16x16x32_bf16 v[126:129], v[134:137], v[166:169], v[126:129]
	v_mfma_f32_16x16x32_bf16 v[122:125], v[142:145], v[166:169], v[122:125]
	v_mfma_f32_16x16x32_bf16 v[118:121], v[134:137], v[174:177], v[118:121]
	v_mfma_f32_16x16x32_bf16 v[110:113], v[142:145], v[174:177], v[110:113]
	v_mfma_f32_16x16x32_bf16 v[94:97], v[134:137], v[182:185], v[94:97]
	v_mfma_f32_16x16x32_bf16 v[90:93], v[142:145], v[182:185], v[90:93]
	v_mfma_f32_16x16x32_bf16 v[82:85], v[134:137], v[222:225], v[82:85]
	v_mfma_f32_16x16x32_bf16 v[74:77], v[142:145], v[222:225], v[74:77]
	s_setprio 0
	s_setprio 1
	v_mfma_f32_16x16x32_bf16 v[114:117], v[146:149], v[162:165], v[114:117]
	v_mfma_f32_16x16x32_bf16 v[106:109], v[154:157], v[162:165], v[106:109]
	v_mfma_f32_16x16x32_bf16 v[102:105], v[146:149], v[170:173], v[102:105]
	v_mfma_f32_16x16x32_bf16 v[98:101], v[154:157], v[170:173], v[98:101]
	v_mfma_f32_16x16x32_bf16 v[86:89], v[146:149], v[178:181], v[86:89]
	v_mfma_f32_16x16x32_bf16 v[78:81], v[154:157], v[178:181], v[78:81]
	v_mfma_f32_16x16x32_bf16 v[70:73], v[146:149], v[206:209], v[70:73]
	v_mfma_f32_16x16x32_bf16 v[66:69], v[154:157], v[206:209], v[66:69]
	v_mfma_f32_16x16x32_bf16 v[114:117], v[150:153], v[166:169], v[114:117]
	v_mfma_f32_16x16x32_bf16 v[106:109], v[158:161], v[166:169], v[106:109]
	v_mfma_f32_16x16x32_bf16 v[102:105], v[150:153], v[174:177], v[102:105]
	v_mfma_f32_16x16x32_bf16 v[98:101], v[158:161], v[174:177], v[98:101]
	v_mfma_f32_16x16x32_bf16 v[86:89], v[150:153], v[182:185], v[86:89]
	v_mfma_f32_16x16x32_bf16 v[78:81], v[158:161], v[182:185], v[78:81]
	v_mfma_f32_16x16x32_bf16 v[70:73], v[150:153], v[222:225], v[70:73]
	v_mfma_f32_16x16x32_bf16 v[66:69], v[158:161], v[222:225], v[66:69]
	s_setprio 0
	s_barrier
	s_add_i32 s63, s48, s38
	s_mov_b32 m0, s63
	ds_read_b128 v[162:165], v220 offset:16384
	ds_read_b128 v[166:169], v220 offset:17408
	ds_read_b128 v[170:173], v220 offset:18432
	ds_read_b128 v[174:177], v220 offset:19456
	ds_read_b128 v[178:181], v220 offset:20480
	ds_read_b128 v[182:185], v220 offset:21504
	ds_read_b128 v[206:209], v220 offset:22528
	ds_read_b128 v[222:225], v220 offset:23552
	global_load_lds_dwordx4 v192, s[30:31]
	s_add_i32 m0, s63, 0x2000
	s_add_u32 s64, s30, 0x80000
	s_addc_u32 s65, s31, 0
	s_add_i32 s63, s49, s38
	global_load_lds_dwordx4 v196, s[30:31]
	s_mov_b32 m0, s63
	s_nop 0
	global_load_lds_dwordx4 v192, s[64:65]
	s_add_i32 m0, s63, 0x2000
	s_nop 0
	global_load_lds_dwordx4 v196, s[64:65]
	s_mov_b32 m0, s27
	s_nop 0
	global_load_lds_dwordx4 v190, s[34:35]
	s_mov_b32 m0, s39
	s_nop 0
	global_load_lds_dwordx4 v194, s[34:35]
	s_waitcnt vmcnt(8)
	s_waitcnt lgkmcnt(0)
	s_barrier
	s_setprio 1
	s_waitcnt lgkmcnt(0)
	v_mfma_f32_16x16x32_bf16 v[62:65], v[130:133], v[162:165], v[62:65]
	v_mfma_f32_16x16x32_bf16 v[58:61], v[138:141], v[162:165], v[58:61]
	v_mfma_f32_16x16x32_bf16 v[50:53], v[130:133], v[170:173], v[50:53]
	v_mfma_f32_16x16x32_bf16 v[42:45], v[138:141], v[170:173], v[42:45]
	v_mfma_f32_16x16x32_bf16 v[34:37], v[130:133], v[178:181], v[34:37]
	v_mfma_f32_16x16x32_bf16 v[26:29], v[138:141], v[178:181], v[26:29]
	v_mfma_f32_16x16x32_bf16 v[18:21], v[130:133], v[206:209], v[18:21]
	v_mfma_f32_16x16x32_bf16 v[10:13], v[138:141], v[206:209], v[10:13]
	v_mfma_f32_16x16x32_bf16 v[62:65], v[134:137], v[166:169], v[62:65]
	v_mfma_f32_16x16x32_bf16 v[58:61], v[142:145], v[166:169], v[58:61]
	v_mfma_f32_16x16x32_bf16 v[50:53], v[134:137], v[174:177], v[50:53]
	v_mfma_f32_16x16x32_bf16 v[42:45], v[142:145], v[174:177], v[42:45]
	v_mfma_f32_16x16x32_bf16 v[34:37], v[134:137], v[182:185], v[34:37]
	v_mfma_f32_16x16x32_bf16 v[26:29], v[142:145], v[182:185], v[26:29]
	v_mfma_f32_16x16x32_bf16 v[18:21], v[134:137], v[222:225], v[18:21]
	v_mfma_f32_16x16x32_bf16 v[10:13], v[142:145], v[222:225], v[10:13]
	s_setprio 0
	s_setprio 1
	v_mfma_f32_16x16x32_bf16 v[54:57], v[146:149], v[162:165], v[54:57]
	v_mfma_f32_16x16x32_bf16 v[46:49], v[154:157], v[162:165], v[46:49]
	v_mfma_f32_16x16x32_bf16 v[38:41], v[146:149], v[170:173], v[38:41]
	v_mfma_f32_16x16x32_bf16 v[30:33], v[154:157], v[170:173], v[30:33]
	v_mfma_f32_16x16x32_bf16 v[22:25], v[146:149], v[178:181], v[22:25]
	v_mfma_f32_16x16x32_bf16 v[14:17], v[154:157], v[178:181], v[14:17]
	v_mfma_f32_16x16x32_bf16 v[6:9], v[146:149], v[206:209], v[6:9]
	v_mfma_f32_16x16x32_bf16 v[2:5], v[154:157], v[206:209], v[2:5]
	v_mfma_f32_16x16x32_bf16 v[54:57], v[150:153], v[166:169], v[54:57]
	v_mfma_f32_16x16x32_bf16 v[46:49], v[158:161], v[166:169], v[46:49]
	v_mfma_f32_16x16x32_bf16 v[38:41], v[150:153], v[174:177], v[38:41]
	v_mfma_f32_16x16x32_bf16 v[30:33], v[158:161], v[174:177], v[30:33]
	v_mfma_f32_16x16x32_bf16 v[22:25], v[150:153], v[182:185], v[22:25]
	v_mfma_f32_16x16x32_bf16 v[14:17], v[158:161], v[182:185], v[14:17]
	v_mfma_f32_16x16x32_bf16 v[6:9], v[150:153], v[222:225], v[6:9]
	v_mfma_f32_16x16x32_bf16 v[2:5], v[158:161], v[222:225], v[2:5]
	s_setprio 0
	s_barrier
; #define PG8_STAGE(bufoff, gbase, voff) do { _Pragma("unroll") for (int _i = 0; _i < 2; ++_i) \
;         __builtin_amdgcn_global_load_lds((const unsigned*)((const char*)(gbase) + (voff)[_i]), (PG8_LAS unsigned*)(lds + (bufoff) + ldsw + _i * 8192), 16, 0, 0); } while (0)
; #define PG8_LDA(dst, b, h) do { _Pragma("unroll") for (int m = 0; m < 4; ++m) _Pragma("unroll") for (int k = 0; k < 2; ++k) dst[m][k] = *(const PG8_LAS bf16x8*)(lds + PG8_SA(b, h) + aoff + m * 2048 + k * 1024); } while (0)
; #define PG8_LDB(dst, b, h) do { _Pragma("unroll") for (int n = 0; n < 2; ++n) _Pragma("unroll") for (int k = 0; k < 2; ++k) dst[n][k] = *(const PG8_LAS bf16x8*)(lds + PG8_SB(b, h) + boff + n * 2048 + k * 1024); } while (0)
; #define PG8_WAIT_V(n) asm volatile("s_waitcnt vmcnt(" #n ")" ::: "memory")
; #define PG8_WAIT_L(n) asm volatile("s_waitcnt lgkmcnt(" #n ")" ::: "memory")
; #define PG8_BAR __builtin_amdgcn_s_barrier()
; #define PG8_SCHED __builtin_amdgcn_sched_barrier(0)
; template <class Epi, class Sched, bool ALIGN_EPI = false, bool SP2 = false>
; __device__ __forceinline__ void gemm_phase(PG8_LAS unsigned char* lds, const Gemm g, const Sched& S, const Epi& E) {
;     ...
;             PG8_LDB(B0, 1, 0); PG8_LDB(B1, 1, 1); PG8_SCHED; PG8_LDA(At, 1, 0); PG8_STAGE(PG8_SA(0, 1), a2 + hstep, voffA);
;             PG8_WAIT_V(8); PG8_WAIT_L(0); PG8_BAR; PG8_MMA(0, 0, At, B0); PG8_MMA(0, 1, At, B1); PG8_BAR; PG8_SCHED;
;             PG8_LDA(At, 1, 1); PG8_STAGE(PG8_SB(1, 0), b3, voffB); PG8_STAGE(PG8_SB(1, 1), b3 + hstep, voffB); PG8_STAGE(PG8_SA(1, 0), a3, voffA);
;             PG8_WAIT_V(8); PG8_WAIT_L(0); PG8_BAR; PG8_MMA(1, 0, At, B0); PG8_MMA(1, 1, At, B1); PG8_BAR; PG8_SCHED;
	s_add_i32 s63, 0, 0x18000
	s_add_i32 s64, 0, 0x1c000
	ds_read_b128 v[130:133], v248
	ds_read_b128 v[134:137], v248 offset:1024
	ds_read_b128 v[138:141], v248 offset:2048
	ds_read_b128 v[142:145], v248 offset:3072
	ds_read_b128 v[146:149], v249
	ds_read_b128 v[150:153], v249 offset:1024
	ds_read_b128 v[154:157], v249 offset:2048
	ds_read_b128 v[158:161], v249 offset:3072
	s_add_u32 s34, s34, 0x80000
	s_addc_u32 s35, s35, 0
	s_mov_b32 m0, s40
	ds_read_b128 v[162:165], v220 offset:32768
	ds_read_b128 v[166:169], v220 offset:33792
	ds_read_b128 v[170:173], v220 offset:34816
	ds_read_b128 v[174:177], v220 offset:35840
	ds_read_b128 v[178:181], v220 offset:36864
	ds_read_b128 v[182:185], v220 offset:37888
	ds_read_b128 v[206:209], v220 offset:38912
	ds_read_b128 v[222:225], v220 offset:39936
	global_load_lds_dwordx4 v190, s[34:35]
	s_mov_b32 m0, s41
	s_nop 0
	global_load_lds_dwordx4 v194, s[34:35]
	s_waitcnt vmcnt(8)
	s_waitcnt lgkmcnt(0)
	s_barrier
	s_setprio 1
	s_waitcnt lgkmcnt(0)
	v_mfma_f32_16x16x32_bf16 v[126:129], v[130:133], v[162:165], v[126:129]
	v_mfma_f32_16x16x32_bf16 v[122:125], v[138:141], v[162:165], v[122:125]
	v_mfma_f32_16x16x32_bf16 v[118:121], v[130:133], v[170:173], v[118:121]
	v_mfma_f32_16x16x32_bf16 v[110:113], v[138:141], v[170:173], v[110:113]
	v_mfma_f32_16x16x32_bf16 v[94:97], v[130:133], v[178:181], v[94:97]
	v_mfma_f32_16x16x32_bf16 v[90:93], v[138:141], v[178:181], v[90:93]
	v_mfma_f32_16x16x32_bf16 v[82:85], v[130:133], v[206:209], v[82:85]
	v_mfma_f32_16x16x32_bf16 v[74:77], v[138:141], v[206:209], v[74:77]
	v_mfma_f32_16x16x32_bf16 v[126:129], v[134:137], v[166:169], v[126:129]
	v_mfma_f32_16x16x32_bf16 v[122:125], v[142:145], v[166:169], v[122:125]
	v_mfma_f32_16x16x32_bf16 v[118:121], v[134:137], v[174:177], v[118:121]
	v_mfma_f32_16x16x32_bf16 v[110:113], v[142:145], v[174:177], v[110:113]
	v_mfma_f32_16x16x32_bf16 v[94:97], v[134:137], v[182:185], v[94:97]
	v_mfma_f32_16x16x32_bf16 v[90:93], v[142:145], v[182:185], v[90:93]
	v_mfma_f32_16x16x32_bf16 v[82:85], v[134:137], v[222:225], v[82:85]
	v_mfma_f32_16x16x32_bf16 v[74:77], v[142:145], v[222:225], v[74:77]
	s_setprio 0
	s_setprio 1
	v_mfma_f32_16x16x32_bf16 v[114:117], v[146:149], v[162:165], v[114:117]
	v_mfma_f32_16x16x32_bf16 v[106:109], v[154:157], v[162:165], v[106:109]
	v_mfma_f32_16x16x32_bf16 v[102:105], v[146:149], v[170:173], v[102:105]
	v_mfma_f32_16x16x32_bf16 v[98:101], v[154:157], v[170:173], v[98:101]
	v_mfma_f32_16x16x32_bf16 v[86:89], v[146:149], v[178:181], v[86:89]
	v_mfma_f32_16x16x32_bf16 v[78:81], v[154:157], v[178:181], v[78:81]
	v_mfma_f32_16x16x32_bf16 v[70:73], v[146:149], v[206:209], v[70:73]
	v_mfma_f32_16x16x32_bf16 v[66:69], v[154:157], v[206:209], v[66:69]
	v_mfma_f32_16x16x32_bf16 v[114:117], v[150:153], v[166:169], v[114:117]
	v_mfma_f32_16x16x32_bf16 v[106:109], v[158:161], v[166:169], v[106:109]
	v_mfma_f32_16x16x32_bf16 v[102:105], v[150:153], v[174:177], v[102:105]
	v_mfma_f32_16x16x32_bf16 v[98:101], v[158:161], v[174:177], v[98:101]
	v_mfma_f32_16x16x32_bf16 v[86:89], v[150:153], v[182:185], v[86:89]
	v_mfma_f32_16x16x32_bf16 v[78:81], v[158:161], v[182:185], v[78:81]
	v_mfma_f32_16x16x32_bf16 v[70:73], v[150:153], v[222:225], v[70:73]
	v_mfma_f32_16x16x32_bf16 v[66:69], v[158:161], v[222:225], v[66:69]
	s_setprio 0
	s_barrier
	s_add_u32 s98, s30, 0x80
	s_addc_u32 s99, s31, 0
	s_add_u32 s100, s34, 0xfff80080
	s_addc_u32 s101, s35, -1
	s_add_i32 s34, s63, s38
	s_mov_b32 m0, s34
	ds_read_b128 v[162:165], v220 offset:49152
	ds_read_b128 v[166:169], v220 offset:50176
	ds_read_b128 v[170:173], v220 offset:51200
	ds_read_b128 v[174:177], v220 offset:52224
	ds_read_b128 v[178:181], v220 offset:53248
	ds_read_b128 v[182:185], v220 offset:54272
	ds_read_b128 v[206:209], v220 offset:55296
	ds_read_b128 v[222:225], v220 offset:56320
	global_load_lds_dwordx4 v192, s[98:99]
	s_add_i32 m0, s34, 0x2000
	s_add_u32 s30, s30, 0x80080
	s_addc_u32 s31, s31, 0
	s_add_i32 s34, s64, s38
	global_load_lds_dwordx4 v196, s[98:99]
	s_mov_b32 m0, s34
	s_nop 0
	global_load_lds_dwordx4 v192, s[30:31]
	s_add_i32 m0, s34, 0x2000
	s_nop 0
	global_load_lds_dwordx4 v196, s[30:31]
	s_mov_b32 m0, s45
	s_nop 0
	global_load_lds_dwordx4 v190, s[100:101]
	s_mov_b32 m0, s46
	s_nop 0
	global_load_lds_dwordx4 v194, s[100:101]
	s_waitcnt vmcnt(8)
	s_waitcnt lgkmcnt(0)
	s_barrier
	s_setprio 1
	s_waitcnt lgkmcnt(0)
	v_mfma_f32_16x16x32_bf16 v[62:65], v[130:133], v[162:165], v[62:65]
	v_mfma_f32_16x16x32_bf16 v[58:61], v[138:141], v[162:165], v[58:61]
	v_mfma_f32_16x16x32_bf16 v[50:53], v[130:133], v[170:173], v[50:53]
	v_mfma_f32_16x16x32_bf16 v[42:45], v[138:141], v[170:173], v[42:45]
	v_mfma_f32_16x16x32_bf16 v[34:37], v[130:133], v[178:181], v[34:37]
	v_mfma_f32_16x16x32_bf16 v[26:29], v[138:141], v[178:181], v[26:29]
	v_mfma_f32_16x16x32_bf16 v[18:21], v[130:133], v[206:209], v[18:21]
	v_mfma_f32_16x16x32_bf16 v[10:13], v[138:141], v[206:209], v[10:13]
	v_mfma_f32_16x16x32_bf16 v[62:65], v[134:137], v[166:169], v[62:65]
	v_mfma_f32_16x16x32_bf16 v[58:61], v[142:145], v[166:169], v[58:61]
	v_mfma_f32_16x16x32_bf16 v[50:53], v[134:137], v[174:177], v[50:53]
	v_mfma_f32_16x16x32_bf16 v[42:45], v[142:145], v[174:177], v[42:45]
	v_mfma_f32_16x16x32_bf16 v[34:37], v[134:137], v[182:185], v[34:37]
	v_mfma_f32_16x16x32_bf16 v[26:29], v[142:145], v[182:185], v[26:29]
	v_mfma_f32_16x16x32_bf16 v[18:21], v[134:137], v[222:225], v[18:21]
	v_mfma_f32_16x16x32_bf16 v[10:13], v[142:145], v[222:225], v[10:13]
	s_setprio 0
	s_setprio 1
	v_mfma_f32_16x16x32_bf16 v[54:57], v[146:149], v[162:165], v[54:57]
	v_mfma_f32_16x16x32_bf16 v[46:49], v[154:157], v[162:165], v[46:49]
	v_mfma_f32_16x16x32_bf16 v[38:41], v[146:149], v[170:173], v[38:41]
	v_mfma_f32_16x16x32_bf16 v[30:33], v[154:157], v[170:173], v[30:33]
	v_mfma_f32_16x16x32_bf16 v[22:25], v[146:149], v[178:181], v[22:25]
	v_mfma_f32_16x16x32_bf16 v[14:17], v[154:157], v[178:181], v[14:17]
	v_mfma_f32_16x16x32_bf16 v[6:9], v[146:149], v[206:209], v[6:9]
	v_mfma_f32_16x16x32_bf16 v[2:5], v[154:157], v[206:209], v[2:5]
	v_mfma_f32_16x16x32_bf16 v[54:57], v[150:153], v[166:169], v[54:57]
	v_mfma_f32_16x16x32_bf16 v[46:49], v[158:161], v[166:169], v[46:49]
	v_mfma_f32_16x16x32_bf16 v[38:41], v[150:153], v[174:177], v[38:41]
	v_mfma_f32_16x16x32_bf16 v[30:33], v[158:161], v[174:177], v[30:33]
	v_mfma_f32_16x16x32_bf16 v[22:25], v[150:153], v[182:185], v[22:25]
	v_mfma_f32_16x16x32_bf16 v[14:17], v[158:161], v[182:185], v[14:17]
	v_mfma_f32_16x16x32_bf16 v[6:9], v[150:153], v[222:225], v[6:9]
	v_mfma_f32_16x16x32_bf16 v[2:5], v[158:161], v[222:225], v[2:5]
	s_setprio 0
	s_barrier
; __device__ __forceinline__ unsigned cvt_pk_bf16(float lo, float hi) { unsigned r; asm volatile("v_cvt_pk_bf16_f32 %0, %1, %2" : "=v"(r) : "v"(lo), "v"(hi)); return r; }
; #define PG8_BAR __builtin_amdgcn_s_barrier()
;     __device__ __forceinline__ void operator()(const f32x4 (&acc)[2][2][4][2], const Unit& u, int wr, int wc, int fr, int fq) const {
;     ...
;             for (int n = 0; n < 2; ++n) gv[bj][n] = *(const f32x4*)(gp + bj * HALF + n * 4);
; #pragma unroll
;         for (int ai = 0; ai < 2; ++ai) {
;             if constexpr (BASE_F32) {
;                 const float* __restrict__ bp = (const float*)base + (size_t)row0 * 2048 + col0;
;                 f32x4 bs[4][2][2];
; #pragma unroll
;                 for (int m = 0; m < 4; ++m)
; #pragma unroll
;                     for (int bj = 0; bj < 2; ++bj)
; #pragma unroll
;                         for (int n = 0; n < 2; ++n) bs[m][bj][n] = *(const f32x4*)(bp + (size_t)(ai * HALF + m * 16) * 2048 + bj * HALF + n * 4);
; #pragma unroll
;                 for (int m = 0; m < 4; ++m)
; #pragma unroll
;                     for (int bj = 0; bj < 2; ++bj) { const f32x4 v0 = bs[m][bj][0] + gv[bj][0] * acc[ai][bj][m][0], v1 = bs[m][bj][1] + gv[bj][1] * acc[ai][bj][m][1];
;                         u32x4 w; w.x = cvt_pk_bf16(v0[0], v0[1]); w.y = cvt_pk_bf16(v0[2], v0[3]); w.z = cvt_pk_bf16(v1[0], v1[1]); w.w = cvt_pk_bf16(v1[2], v1[3]);
;                         *(u32x4*)(op + (size_t)(ai * HALF + m * 16) * 2048 + bj * HALF) = w; }
; template <class Epi, class Sched, bool ALIGN_EPI = false, bool SP2 = false>
; __device__ __forceinline__ void gemm_phase(PG8_LAS unsigned char* lds, const Gemm g, const Sched& S, const Epi& E) {
;     ...
;         if constexpr (ALIGN_EPI) { if (wr == 0) PG8_BAR; }
	s_add_i32 s62, s62, 2
	s_add_u32 s28, s28, 0x100
	s_addc_u32 s29, s29, 0
	s_add_u32 s60, s60, 0x100
	s_addc_u32 s61, s61, 0
	s_cmp_gt_u32 s62, 29
	s_cbranch_scc0 .LBB0_747
	s_ashr_i32 s19, s26, 3
	v_lshl_or_b32 v148, s57, 8, v217
	s_mul_hi_i32 s21, s19, 0xc000
	s_mul_i32 s19, s19, 0xc000
	s_add_u32 s28, s43, s19
	v_ashrrev_i32_e32 v149, 31, v148
	v_lshl_add_u32 v146, s26, 8, v189
	s_addc_u32 s29, s44, s21
	v_lshlrev_b64 v[130:131], 2, v[148:149]
	v_lshl_add_u64 v[132:133], s[28:29], 0, v[130:131]
	v_ashrrev_i32_e32 v147, 31, v146
	v_readlane_b32 s28, v247, 10
	v_lshlrev_b64 v[134:135], 13, v[146:147]
	v_readlane_b32 s29, v247, 11
	s_mov_b32 s19, 0x40000
	v_lshlrev_b64 v[146:147], 12, v[146:147]
	v_lshl_add_u64 v[134:135], s[28:29], 0, v[134:135]
	v_lshl_add_u64 v[208:209], v[134:135], 0, v[130:131]
	global_load_dwordx4 v[222:225], v[208:209], off
	global_load_dwordx4 v[142:145], v[132:133], off
	global_load_dwordx4 v[138:141], v[132:133], off offset:16
	global_load_dwordx4 v[226:229], v[208:209], off offset:16
	global_load_dwordx4 v[230:233], v[208:209], off offset:512
	global_load_dwordx4 v[134:137], v[132:133], off offset:512
	s_nop 0
	global_load_dwordx4 v[130:133], v[132:133], off offset:528
	s_nop 0
	global_load_dwordx4 v[234:237], v[208:209], off offset:528
	v_add_co_u32_e32 v150, vcc, s50, v208
	s_mov_b64 s[28:29], 0x20000
	s_nop 0
	v_addc_co_u32_e32 v151, vcc, 0, v209, vcc
	v_lshl_add_u64 v[152:153], v[208:209], 0, s[28:29]
	s_mov_b64 s[28:29], 0x20200
	global_load_dwordx4 v[238:241], v[150:151], off
	global_load_dwordx4 v[242:245], v[152:153], off offset:16
	v_lshl_add_u64 v[152:153], v[208:209], 0, s[28:29]
	global_load_dwordx4 v[182:185], v[150:151], off offset:512
	global_load_dwordx4 v[178:181], v[152:153], off offset:16
	v_add_co_u32_e32 v150, vcc, s19, v208
	s_mov_b64 s[28:29], 0x40000
	s_nop 0
	v_addc_co_u32_e32 v151, vcc, 0, v209, vcc
	global_load_dwordx4 v[174:177], v[150:151], off
	v_lshl_add_u64 v[152:153], v[208:209], 0, s[28:29]
	global_load_dwordx4 v[170:173], v[152:153], off offset:16
	s_mov_b64 s[28:29], 0x40200
	s_mov_b32 s19, 0x60000
	v_lshl_add_u64 v[152:153], v[208:209], 0, s[28:29]
	global_load_dwordx4 v[166:169], v[150:151], off offset:512
	global_load_dwordx4 v[162:165], v[152:153], off offset:16
	v_add_co_u32_e32 v150, vcc, s19, v208
	s_mov_b64 s[28:29], 0x60000
	s_nop 0
	v_addc_co_u32_e32 v151, vcc, 0, v209, vcc
	global_load_dwordx4 v[158:161], v[150:151], off
	v_lshl_add_u64 v[152:153], v[208:209], 0, s[28:29]
	global_load_dwordx4 v[154:157], v[152:153], off offset:16
	s_mov_b64 s[28:29], 0x60200
	v_lshl_add_u64 v[146:147], s[66:67], 0, v[146:147]
	v_lshl_add_u64 v[206:207], v[148:149], 1, v[146:147]
	v_lshl_add_u64 v[146:147], v[208:209], 0, s[28:29]
	global_load_dwordx4 v[146:149], v[146:147], off offset:16
	s_mov_b32 s19, 0x10000
	global_load_dwordx4 v[150:153], v[150:151], off offset:512
	s_mov_b64 s[28:29], 0x100000
	s_and_b64 vcc, exec, s[8:9]
	s_cbranch_vccz .LBB0_750
	s_barrier
.LBB0_750:
	s_waitcnt vmcnt(0)
	v_pk_fma_f32 v[128:129], v[128:129], v[144:145], v[224:225]
	v_pk_fma_f32 v[126:127], v[126:127], v[142:143], v[222:223]
	v_pk_fma_f32 v[124:125], v[124:125], v[140:141], v[228:229]
	v_pk_fma_f32 v[122:123], v[122:123], v[138:139], v[226:227]
	v_pk_fma_f32 v[116:117], v[116:117], v[136:137], v[232:233]
	v_pk_fma_f32 v[114:115], v[114:115], v[134:135], v[230:231]
	v_pk_fma_f32 v[222:223], v[108:109], v[132:133], v[236:237]
	v_pk_fma_f32 v[224:225], v[106:107], v[130:131], v[234:235]
	v_cvt_pk_bf16_f32 v106, v126, v127
	v_cvt_pk_bf16_f32 v107, v128, v129
	v_cvt_pk_bf16_f32 v108, v122, v123
	v_cvt_pk_bf16_f32 v109, v124, v125
	global_store_dwordx4 v[206:207], v[106:109], off
	v_lshl_add_u64 v[126:127], v[208:209], 0, s[16:17]
	v_pk_fma_f32 v[120:121], v[120:121], v[144:145], v[240:241]
	v_cvt_pk_bf16_f32 v106, v114, v115
	v_cvt_pk_bf16_f32 v107, v116, v117
	v_cvt_pk_bf16_f32 v108, v224, v225
	v_cvt_pk_bf16_f32 v109, v222, v223
	global_store_dwordx4 v[206:207], v[106:109], off offset:256
	v_pk_fma_f32 v[118:119], v[118:119], v[142:143], v[238:239]
	v_pk_fma_f32 v[112:113], v[112:113], v[140:141], v[244:245]
	v_pk_fma_f32 v[108:109], v[110:111], v[138:139], v[242:243]
	v_add_co_u32_e32 v110, vcc, s19, v206
	v_cvt_pk_bf16_f32 v106, v118, v119
	v_cvt_pk_bf16_f32 v107, v120, v121
	v_cvt_pk_bf16_f32 v108, v108, v109
	v_cvt_pk_bf16_f32 v109, v112, v113
	s_nop 1
	v_addc_co_u32_e32 v111, vcc, 0, v207, vcc
	global_store_dwordx4 v[110:111], v[106:109], off
	v_pk_fma_f32 v[104:105], v[104:105], v[136:137], v[184:185]
	v_pk_fma_f32 v[102:103], v[102:103], v[134:135], v[182:183]
	v_pk_fma_f32 v[106:107], v[100:101], v[132:133], v[180:181]
	v_pk_fma_f32 v[100:101], v[98:99], v[130:131], v[178:179]
	v_cvt_pk_bf16_f32 v98, v102, v103
	v_cvt_pk_bf16_f32 v99, v104, v105
	v_pk_fma_f32 v[94:95], v[94:95], v[142:143], v[174:175]
	v_cvt_pk_bf16_f32 v100, v100, v101
	v_cvt_pk_bf16_f32 v101, v106, v107
	global_store_dwordx4 v[110:111], v[98:101], off offset:256
	v_pk_fma_f32 v[96:97], v[96:97], v[144:145], v[176:177]
	v_pk_fma_f32 v[88:89], v[88:89], v[136:137], v[168:169]
	v_pk_fma_f32 v[98:99], v[92:93], v[140:141], v[172:173]
	v_pk_fma_f32 v[92:93], v[90:91], v[138:139], v[170:171]
	v_cvt_pk_bf16_f32 v90, v94, v95
	v_add_co_u32_e32 v94, vcc, s50, v206
	v_cvt_pk_bf16_f32 v91, v96, v97
	v_cvt_pk_bf16_f32 v92, v92, v93
	v_cvt_pk_bf16_f32 v93, v98, v99
	v_pk_fma_f32 v[86:87], v[86:87], v[134:135], v[166:167]
	s_nop 0
	v_addc_co_u32_e32 v95, vcc, 0, v207, vcc
	global_store_dwordx4 v[94:95], v[90:93], off
	s_mov_b32 s19, 0x30000
	v_pk_fma_f32 v[72:73], v[72:73], v[136:137], v[152:153]
	v_pk_fma_f32 v[90:91], v[80:81], v[132:133], v[164:165]
; __device__ __forceinline__ unsigned cvt_pk_bf16(float lo, float hi) { unsigned r; asm volatile("v_cvt_pk_bf16_f32 %0, %1, %2" : "=v"(r) : "v"(lo), "v"(hi)); return r; }
; #define PG8_BAR __builtin_amdgcn_s_barrier()
;     __device__ __forceinline__ void operator()(const f32x4 (&acc)[2][2][4][2], const Unit& u, int wr, int wc, int fr, int fq) const {
;     ...
;         for (int ai = 0; ai < 2; ++ai) {
;             if constexpr (BASE_F32) {
;                 const float* __restrict__ bp = (const float*)base + (size_t)row0 * 2048 + col0;
;                 f32x4 bs[4][2][2];
; #pragma unroll
;                 for (int m = 0; m < 4; ++m)
; #pragma unroll
;                     for (int bj = 0; bj < 2; ++bj)
; #pragma unroll
;                         for (int n = 0; n < 2; ++n) bs[m][bj][n] = *(const f32x4*)(bp + (size_t)(ai * HALF + m * 16) * 2048 + bj * HALF + n * 4);
; #pragma unroll
;                 for (int m = 0; m < 4; ++m)
; #pragma unroll
;                     for (int bj = 0; bj < 2; ++bj) { const f32x4 v0 = bs[m][bj][0] + gv[bj][0] * acc[ai][bj][m][0], v1 = bs[m][bj][1] + gv[bj][1] * acc[ai][bj][m][1];
;                         u32x4 w; w.x = cvt_pk_bf16(v0[0], v0[1]); w.y = cvt_pk_bf16(v0[2], v0[3]); w.z = cvt_pk_bf16(v1[0], v1[1]); w.w = cvt_pk_bf16(v1[2], v1[3]);
;                         *(u32x4*)(op + (size_t)(ai * HALF + m * 16) * 2048 + bj * HALF) = w; }
; template <class Epi, class Sched, bool ALIGN_EPI = false, bool SP2 = false>
; __device__ __forceinline__ void gemm_phase(PG8_LAS unsigned char* lds, const Gemm g, const Sched& S, const Epi& E) {
;     ...
;         if (!has_next) break;
; #pragma unroll
;         for (int a = 0; a < 2; ++a)
; #pragma unroll
;             for (int b = 0; b < 2; ++b)
; #pragma unroll
;                 for (int m = 0; m < 4; ++m)
; #pragma unroll
;                     for (int n = 0; n < 2; ++n) acc[a][b][m][n] = (f32x4){0.f, 0.f, 0.f, 0.f};
;         cur = nxt; cA = nA; cB = nB; ++ui;
;         if constexpr (ALIGN_EPI) { if (wr == 1) PG8_BAR; }
	v_pk_fma_f32 v[80:81], v[78:79], v[130:131], v[162:163]
	v_cvt_pk_bf16_f32 v78, v86, v87
	v_cvt_pk_bf16_f32 v79, v88, v89
	v_pk_fma_f32 v[70:71], v[70:71], v[134:135], v[150:151]
	v_cvt_pk_bf16_f32 v80, v80, v81
	v_cvt_pk_bf16_f32 v81, v90, v91
	global_store_dwordx4 v[94:95], v[78:81], off offset:256
	v_lshl_add_u64 v[102:103], v[208:209], 0, s[10:11]
	v_lshl_add_u64 v[110:111], v[208:209], 0, s[12:13]
	v_pk_fma_f32 v[78:79], v[84:85], v[144:145], v[160:161]
	v_pk_fma_f32 v[80:81], v[82:83], v[142:143], v[158:159]
	v_pk_fma_f32 v[82:83], v[76:77], v[140:141], v[156:157]
	v_pk_fma_f32 v[76:77], v[74:75], v[138:139], v[154:155]
	v_cvt_pk_bf16_f32 v74, v80, v81
	v_cvt_pk_bf16_f32 v75, v78, v79
	v_add_co_u32_e32 v78, vcc, s19, v206
	v_cvt_pk_bf16_f32 v76, v76, v77
	v_cvt_pk_bf16_f32 v77, v82, v83
	s_mov_b32 s19, 0x100000
	s_nop 0
	v_addc_co_u32_e32 v79, vcc, 0, v207, vcc
	global_store_dwordx4 v[78:79], v[74:77], off
	v_lshl_add_u64 v[118:119], v[208:209], 0, s[14:15]
	s_nop 0
	v_pk_fma_f32 v[74:75], v[68:69], v[132:133], v[148:149]
	v_pk_fma_f32 v[68:69], v[66:67], v[130:131], v[146:147]
	v_cvt_pk_bf16_f32 v66, v70, v71
	v_cvt_pk_bf16_f32 v67, v72, v73
	v_lshl_add_u64 v[70:71], v[208:209], 0, s[28:29]
	v_cvt_pk_bf16_f32 v68, v68, v69
	v_cvt_pk_bf16_f32 v69, v74, v75
	global_store_dwordx4 v[78:79], v[66:69], off offset:256
	v_add_co_u32_e32 v74, vcc, s19, v208
	global_load_dwordx4 v[70:73], v[70:71], off offset:16
	s_nop 0
	v_addc_co_u32_e32 v75, vcc, 0, v209, vcc
	global_load_dwordx4 v[66:69], v[74:75], off
	s_mov_b64 s[28:29], 0x100200
	s_mov_b32 s19, 0x120000
	v_lshl_add_u64 v[78:79], v[208:209], 0, s[28:29]
	v_add_co_u32_e32 v90, vcc, s19, v208
	global_load_dwordx4 v[74:77], v[74:75], off offset:512
	s_nop 0
	global_load_dwordx4 v[78:81], v[78:79], off offset:16
	s_mov_b64 s[28:29], 0x120000
	v_addc_co_u32_e32 v91, vcc, 0, v209, vcc
	global_load_dwordx4 v[82:85], v[90:91], off
	v_lshl_add_u64 v[86:87], v[208:209], 0, s[28:29]
	global_load_dwordx4 v[86:89], v[86:87], off offset:16
	s_mov_b64 s[28:29], 0x120200
	v_lshl_add_u64 v[94:95], v[208:209], 0, s[28:29]
	v_add_co_u32_e32 v106, vcc, s51, v208
	global_load_dwordx4 v[90:93], v[90:91], off offset:512
	s_nop 0
	v_addc_co_u32_e32 v107, vcc, 0, v209, vcc
	global_load_dwordx4 v[94:97], v[94:95], off offset:16
	v_add_co_u32_e32 v122, vcc, s52, v208
	global_load_dwordx4 v[98:101], v[106:107], off
	s_nop 0
	global_load_dwordx4 v[102:105], v[102:103], off offset:16
	s_nop 0
	global_load_dwordx4 v[106:109], v[106:107], off offset:512
	v_addc_co_u32_e32 v123, vcc, 0, v209, vcc
	global_load_dwordx4 v[110:113], v[110:111], off offset:16
	s_waitcnt vmcnt(10)
	v_pk_fma_f32 v[62:63], v[62:63], v[142:143], v[66:67]
	global_load_dwordx4 v[114:117], v[122:123], off
	v_pk_fma_f32 v[66:67], v[60:61], v[140:141], v[72:73]
	global_load_dwordx4 v[118:121], v[118:119], off offset:16
	s_nop 0
	global_load_dwordx4 v[122:125], v[122:123], off offset:512
	s_nop 0
	global_load_dwordx4 v[126:129], v[126:127], off offset:16
	v_pk_fma_f32 v[60:61], v[58:59], v[138:139], v[70:71]
	v_cvt_pk_bf16_f32 v58, v62, v63
	v_add_co_u32_e32 v62, vcc, s53, v206
	v_pk_fma_f32 v[64:65], v[64:65], v[144:145], v[68:69]
	s_nop 0
	v_addc_co_u32_e32 v63, vcc, 0, v207, vcc
	v_cvt_pk_bf16_f32 v59, v64, v65
	v_cvt_pk_bf16_f32 v60, v60, v61
	v_cvt_pk_bf16_f32 v61, v66, v67
	global_store_dwordx4 v[62:63], v[58:61], off
	s_waitcnt vmcnt(14)
	v_pk_fma_f32 v[56:57], v[56:57], v[136:137], v[76:77]
	v_pk_fma_f32 v[54:55], v[54:55], v[134:135], v[74:75]
	s_waitcnt vmcnt(13)
	v_pk_fma_f32 v[58:59], v[48:49], v[132:133], v[80:81]
	v_pk_fma_f32 v[48:49], v[46:47], v[130:131], v[78:79]
	v_cvt_pk_bf16_f32 v46, v54, v55
	v_cvt_pk_bf16_f32 v47, v56, v57
	s_waitcnt vmcnt(10)
	v_pk_fma_f32 v[40:41], v[40:41], v[136:137], v[92:93]
	v_cvt_pk_bf16_f32 v48, v48, v49
	v_cvt_pk_bf16_f32 v49, v58, v59
	global_store_dwordx4 v[62:63], v[46:49], off offset:256
	v_pk_fma_f32 v[38:39], v[38:39], v[134:135], v[90:91]
	s_waitcnt vmcnt(7)
	v_pk_fma_f32 v[24:25], v[24:25], v[136:137], v[108:109]
	v_pk_fma_f32 v[46:47], v[52:53], v[144:145], v[84:85]
	v_pk_fma_f32 v[48:49], v[50:51], v[142:143], v[82:83]
	v_pk_fma_f32 v[50:51], v[44:45], v[140:141], v[88:89]
	v_pk_fma_f32 v[44:45], v[42:43], v[138:139], v[86:87]
	v_cvt_pk_bf16_f32 v42, v48, v49
	v_cvt_pk_bf16_f32 v43, v46, v47
	v_add_co_u32_e32 v46, vcc, s54, v206
	v_cvt_pk_bf16_f32 v44, v44, v45
	v_cvt_pk_bf16_f32 v45, v50, v51
	v_pk_fma_f32 v[22:23], v[22:23], v[134:135], v[106:107]
	s_nop 0
	v_addc_co_u32_e32 v47, vcc, 0, v207, vcc
	global_store_dwordx4 v[46:47], v[42:45], off
	s_waitcnt vmcnt(4)
	v_pk_fma_f32 v[8:9], v[8:9], v[136:137], v[124:125]
	v_pk_fma_f32 v[42:43], v[32:33], v[132:133], v[96:97]
	v_pk_fma_f32 v[32:33], v[30:31], v[130:131], v[94:95]
	v_cvt_pk_bf16_f32 v30, v38, v39
	v_cvt_pk_bf16_f32 v31, v40, v41
	v_pk_fma_f32 v[6:7], v[6:7], v[134:135], v[122:123]
	v_cvt_pk_bf16_f32 v32, v32, v33
	v_cvt_pk_bf16_f32 v33, v42, v43
	global_store_dwordx4 v[46:47], v[30:33], off offset:256
	s_nop 1
	v_pk_fma_f32 v[30:31], v[36:37], v[144:145], v[100:101]
	v_pk_fma_f32 v[32:33], v[34:35], v[142:143], v[98:99]
	v_pk_fma_f32 v[34:35], v[28:29], v[140:141], v[104:105]
	v_pk_fma_f32 v[28:29], v[26:27], v[138:139], v[102:103]
	v_cvt_pk_bf16_f32 v26, v32, v33
	v_cvt_pk_bf16_f32 v27, v30, v31
	v_add_co_u32_e32 v30, vcc, s55, v206
	v_cvt_pk_bf16_f32 v28, v28, v29
	v_cvt_pk_bf16_f32 v29, v34, v35
	s_nop 1
	v_addc_co_u32_e32 v31, vcc, 0, v207, vcc
	global_store_dwordx4 v[30:31], v[26:29], off
	s_nop 1
	v_pk_fma_f32 v[26:27], v[16:17], v[132:133], v[112:113]
	v_pk_fma_f32 v[16:17], v[14:15], v[130:131], v[110:111]
	v_cvt_pk_bf16_f32 v14, v22, v23
	v_cvt_pk_bf16_f32 v15, v24, v25
	s_nop 0
	v_cvt_pk_bf16_f32 v16, v16, v17
	v_cvt_pk_bf16_f32 v17, v26, v27
	global_store_dwordx4 v[30:31], v[14:17], off offset:256
	s_nop 1
	v_pk_fma_f32 v[14:15], v[20:21], v[144:145], v[116:117]
	v_pk_fma_f32 v[16:17], v[18:19], v[142:143], v[114:115]
	v_pk_fma_f32 v[18:19], v[12:13], v[140:141], v[120:121]
	v_pk_fma_f32 v[12:13], v[10:11], v[138:139], v[118:119]
	v_cvt_pk_bf16_f32 v10, v16, v17
	v_cvt_pk_bf16_f32 v11, v14, v15
	v_add_co_u32_e32 v14, vcc, s56, v206
	v_cvt_pk_bf16_f32 v12, v12, v13
	v_cvt_pk_bf16_f32 v13, v18, v19
	s_nop 1
	v_addc_co_u32_e32 v15, vcc, 0, v207, vcc
	global_store_dwordx4 v[14:15], v[10:13], off
	s_andn2_b64 vcc, exec, s[2:3]
	s_mov_b64 s[2:3], -1
	s_waitcnt vmcnt(7)
	v_pk_fma_f32 v[10:11], v[4:5], v[132:133], v[128:129]
	v_pk_fma_f32 v[4:5], v[2:3], v[130:131], v[126:127]
	v_cvt_pk_bf16_f32 v2, v6, v7
	v_cvt_pk_bf16_f32 v3, v8, v9
	s_nop 0
	v_cvt_pk_bf16_f32 v4, v4, v5
	v_cvt_pk_bf16_f32 v5, v10, v11
	global_store_dwordx4 v[14:15], v[2:5], off offset:256
	s_cbranch_vccnz .LBB0_739
	s_andn2_b64 vcc, exec, s[4:5]
	s_cbranch_vccnz .LBB0_738
	s_barrier
	s_branch .LBB0_738

; #define PG8_STAGE(bufoff, gbase, voff) do { _Pragma("unroll") for (int _i = 0; _i < 2; ++_i) \
;         __builtin_amdgcn_global_load_lds((const unsigned*)((const char*)(gbase) + (voff)[_i]), (PG8_LAS unsigned*)(lds + (bufoff) + ldsw + _i * 8192), 16, 0, 0); } while (0)
; #define PG8_LDA(dst, b, h) do { _Pragma("unroll") for (int m = 0; m < 4; ++m) _Pragma("unroll") for (int k = 0; k < 2; ++k) dst[m][k] = *(const PG8_LAS bf16x8*)(lds + PG8_SA(b, h) + aoff + m * 2048 + k * 1024); } while (0)
; #define PG8_LDB(dst, b, h) do { _Pragma("unroll") for (int n = 0; n < 2; ++n) _Pragma("unroll") for (int k = 0; k < 2; ++k) dst[n][k] = *(const PG8_LAS bf16x8*)(lds + PG8_SB(b, h) + boff + n * 2048 + k * 1024); } while (0)
; #define PG8_WAIT_V(n) asm volatile("s_waitcnt vmcnt(" #n ")" ::: "memory")
; #define PG8_WAIT_L(n) asm volatile("s_waitcnt lgkmcnt(" #n ")" ::: "memory")
; #define PG8_BAR __builtin_amdgcn_s_barrier()
; #define PG8_SCHED __builtin_amdgcn_sched_barrier(0)
; template <class Epi, class Sched, bool ALIGN_EPI = false, bool SP2 = false>
; __device__ __forceinline__ void gemm_phase(PG8_LAS unsigned char* lds, const Gemm g, const Sched& S, const Epi& E) {
;     ...
;             PG8_LDB(B0, 0, 0); PG8_LDB(B1, 0, 1); PG8_SCHED; PG8_LDA(At, 0, 0); PG8_STAGE(PG8_SA(1, 1), a1 + hstep, voffA);
;             PG8_WAIT_V(8); PG8_WAIT_L(0); PG8_BAR; PG8_MMA(0, 0, At, B0); PG8_MMA(0, 1, At, B1); PG8_BAR; PG8_SCHED;
;             PG8_LDA(At, 0, 1); PG8_STAGE(PG8_SB(0, 0), b2, voffB); PG8_STAGE(PG8_SB(0, 1), b2 + hstep, voffB); PG8_STAGE(PG8_SA(0, 0), a2, voffA);
;             PG8_WAIT_V(8); PG8_WAIT_L(0); PG8_BAR; PG8_MMA(1, 0, At, B0); PG8_MMA(1, 1, At, B1); PG8_BAR; PG8_SCHED;
;             PG8_LDB(B0, 1, 0); PG8_LDB(B1, 1, 1); PG8_SCHED; PG8_LDA(At, 1, 0); PG8_STAGE(PG8_SA(0, 1), a2 + hstep, voffA);
;             PG8_WAIT_V(8); PG8_WAIT_L(0); PG8_BAR; PG8_MMA(0, 0, At, B0); PG8_MMA(0, 1, At, B1); PG8_BAR; PG8_SCHED;
;             PG8_LDA(At, 1, 1); PG8_STAGE(PG8_SB(1, 0), b3, voffB); PG8_STAGE(PG8_SB(1, 1), b3 + hstep, voffB); PG8_STAGE(PG8_SA(1, 0), a3, voffA);
;             PG8_WAIT_V(8); PG8_WAIT_L(0); PG8_BAR; PG8_MMA(1, 0, At, B0); PG8_MMA(1, 1, At, B1); PG8_BAR; PG8_SCHED;
.LBB0_872:
	ds_read_b128 v[146:149], v153
	ds_read_b128 v[156:159], v153 offset:1024
	ds_read_b128 v[160:163], v153 offset:2048
	ds_read_b128 v[164:167], v153 offset:3072
	ds_read_b128 v[168:171], v154
	ds_read_b128 v[172:175], v154 offset:1024
	ds_read_b128 v[176:179], v154 offset:2048
	ds_read_b128 v[180:183], v154 offset:3072
	s_add_u32 s24, s22, 0xfff80080
	s_addc_u32 s25, s23, -1
	s_cmp_eq_u32 s48, 28
	s_cselect_b32 s27, s15, s25
	s_cselect_b32 s26, s44, s24
	s_cselect_b32 s25, s13, s47
	s_cselect_b32 s24, s45, s46
	s_add_i32 m0, s21, 0xc000
	ds_read_b128 v[190:193], v155
	ds_read_b128 v[194:197], v155 offset:1024
	ds_read_b128 v[198:201], v155 offset:2048
	ds_read_b128 v[202:205], v155 offset:3072
	ds_read_b128 v[206:209], v155 offset:4096
	ds_read_b128 v[216:219], v155 offset:5120
	ds_read_b128 v[220:223], v155 offset:6144
	ds_read_b128 v[224:227], v155 offset:7168
	global_load_lds_dwordx4 v138, s[22:23]
	s_add_i32 m0, s21, 0xe000
	s_nop 0
	global_load_lds_dwordx4 v140, s[22:23]
	s_waitcnt vmcnt(8)
	s_waitcnt lgkmcnt(0)
	s_barrier
	s_setprio 1
	s_waitcnt lgkmcnt(0)
	v_mfma_f32_16x16x32_bf16 v[126:129], v[146:149], v[190:193], v[126:129]
	v_mfma_f32_16x16x32_bf16 v[122:125], v[160:163], v[190:193], v[122:125]
	v_mfma_f32_16x16x32_bf16 v[110:113], v[146:149], v[198:201], v[110:113]
	v_mfma_f32_16x16x32_bf16 v[106:109], v[160:163], v[198:201], v[106:109]
	v_mfma_f32_16x16x32_bf16 v[94:97], v[146:149], v[206:209], v[94:97]
	v_mfma_f32_16x16x32_bf16 v[90:93], v[160:163], v[206:209], v[90:93]
	v_mfma_f32_16x16x32_bf16 v[78:81], v[146:149], v[220:223], v[78:81]
	v_mfma_f32_16x16x32_bf16 v[74:77], v[160:163], v[220:223], v[74:77]
	v_mfma_f32_16x16x32_bf16 v[126:129], v[156:159], v[194:197], v[126:129]
	v_mfma_f32_16x16x32_bf16 v[122:125], v[164:167], v[194:197], v[122:125]
	v_mfma_f32_16x16x32_bf16 v[110:113], v[156:159], v[202:205], v[110:113]
	v_mfma_f32_16x16x32_bf16 v[106:109], v[164:167], v[202:205], v[106:109]
	v_mfma_f32_16x16x32_bf16 v[94:97], v[156:159], v[216:219], v[94:97]
	v_mfma_f32_16x16x32_bf16 v[90:93], v[164:167], v[216:219], v[90:93]
	v_mfma_f32_16x16x32_bf16 v[78:81], v[156:159], v[224:227], v[78:81]
	v_mfma_f32_16x16x32_bf16 v[74:77], v[164:167], v[224:227], v[74:77]
	s_setprio 0
	s_setprio 1
	v_mfma_f32_16x16x32_bf16 v[118:121], v[168:171], v[190:193], v[118:121]
	v_mfma_f32_16x16x32_bf16 v[114:117], v[176:179], v[190:193], v[114:117]
	v_mfma_f32_16x16x32_bf16 v[102:105], v[168:171], v[198:201], v[102:105]
	v_mfma_f32_16x16x32_bf16 v[98:101], v[176:179], v[198:201], v[98:101]
	v_mfma_f32_16x16x32_bf16 v[86:89], v[168:171], v[206:209], v[86:89]
	v_mfma_f32_16x16x32_bf16 v[82:85], v[176:179], v[206:209], v[82:85]
	v_mfma_f32_16x16x32_bf16 v[70:73], v[168:171], v[220:223], v[70:73]
	v_mfma_f32_16x16x32_bf16 v[66:69], v[176:179], v[220:223], v[66:69]
	v_mfma_f32_16x16x32_bf16 v[118:121], v[172:175], v[194:197], v[118:121]
	v_mfma_f32_16x16x32_bf16 v[114:117], v[180:183], v[194:197], v[114:117]
	v_mfma_f32_16x16x32_bf16 v[102:105], v[172:175], v[202:205], v[102:105]
	v_mfma_f32_16x16x32_bf16 v[98:101], v[180:183], v[202:205], v[98:101]
	v_mfma_f32_16x16x32_bf16 v[86:89], v[172:175], v[216:219], v[86:89]
	v_mfma_f32_16x16x32_bf16 v[82:85], v[180:183], v[216:219], v[82:85]
	v_mfma_f32_16x16x32_bf16 v[70:73], v[172:175], v[224:227], v[70:73]
	v_mfma_f32_16x16x32_bf16 v[66:69], v[180:183], v[224:227], v[66:69]
	s_setprio 0
	s_barrier
	s_add_i32 s49, s40, s29
	s_mov_b32 m0, s49
	ds_read_b128 v[190:193], v155 offset:16384
	ds_read_b128 v[194:197], v155 offset:17408
	ds_read_b128 v[198:201], v155 offset:18432
	ds_read_b128 v[202:205], v155 offset:19456
	ds_read_b128 v[206:209], v155 offset:20480
	ds_read_b128 v[216:219], v155 offset:21504
	ds_read_b128 v[220:223], v155 offset:22528
	ds_read_b128 v[224:227], v155 offset:23552
	global_load_lds_dwordx4 v134, s[24:25]
	s_add_i32 m0, s49, 0x2000
	s_add_u32 s50, s24, 0x80000
	s_addc_u32 s51, s25, 0
	s_add_i32 s49, s41, s29
	global_load_lds_dwordx4 v130, s[24:25]
	s_mov_b32 m0, s49
	s_nop 0
	global_load_lds_dwordx4 v134, s[50:51]
	s_add_i32 m0, s49, 0x2000
	s_nop 0
	global_load_lds_dwordx4 v130, s[50:51]
	s_mov_b32 m0, s21
	s_nop 0
	global_load_lds_dwordx4 v136, s[26:27]
	s_mov_b32 m0, s33
	s_nop 0
	global_load_lds_dwordx4 v132, s[26:27]
	s_waitcnt vmcnt(8)
	s_waitcnt lgkmcnt(0)
	s_barrier
	s_setprio 1
	s_waitcnt lgkmcnt(0)
	v_mfma_f32_16x16x32_bf16 v[62:65], v[146:149], v[190:193], v[62:65]
	v_mfma_f32_16x16x32_bf16 v[58:61], v[160:163], v[190:193], v[58:61]
	v_mfma_f32_16x16x32_bf16 v[46:49], v[146:149], v[198:201], v[46:49]
	v_mfma_f32_16x16x32_bf16 v[42:45], v[160:163], v[198:201], v[42:45]
	v_mfma_f32_16x16x32_bf16 v[30:33], v[146:149], v[206:209], v[30:33]
	v_mfma_f32_16x16x32_bf16 v[26:29], v[160:163], v[206:209], v[26:29]
	v_mfma_f32_16x16x32_bf16 v[14:17], v[146:149], v[220:223], v[14:17]
	v_mfma_f32_16x16x32_bf16 v[10:13], v[160:163], v[220:223], v[10:13]
	v_mfma_f32_16x16x32_bf16 v[62:65], v[156:159], v[194:197], v[62:65]
	v_mfma_f32_16x16x32_bf16 v[58:61], v[164:167], v[194:197], v[58:61]
	v_mfma_f32_16x16x32_bf16 v[46:49], v[156:159], v[202:205], v[46:49]
	v_mfma_f32_16x16x32_bf16 v[42:45], v[164:167], v[202:205], v[42:45]
	v_mfma_f32_16x16x32_bf16 v[30:33], v[156:159], v[216:219], v[30:33]
	v_mfma_f32_16x16x32_bf16 v[26:29], v[164:167], v[216:219], v[26:29]
	v_mfma_f32_16x16x32_bf16 v[14:17], v[156:159], v[224:227], v[14:17]
	v_mfma_f32_16x16x32_bf16 v[10:13], v[164:167], v[224:227], v[10:13]
	s_setprio 0
	s_setprio 1
	v_mfma_f32_16x16x32_bf16 v[54:57], v[168:171], v[190:193], v[54:57]
	v_mfma_f32_16x16x32_bf16 v[50:53], v[176:179], v[190:193], v[50:53]
	v_mfma_f32_16x16x32_bf16 v[38:41], v[168:171], v[198:201], v[38:41]
	v_mfma_f32_16x16x32_bf16 v[34:37], v[176:179], v[198:201], v[34:37]
	v_mfma_f32_16x16x32_bf16 v[22:25], v[168:171], v[206:209], v[22:25]
	v_mfma_f32_16x16x32_bf16 v[18:21], v[176:179], v[206:209], v[18:21]
	v_mfma_f32_16x16x32_bf16 v[6:9], v[168:171], v[220:223], v[6:9]
	v_mfma_f32_16x16x32_bf16 v[2:5], v[176:179], v[220:223], v[2:5]
	v_mfma_f32_16x16x32_bf16 v[54:57], v[172:175], v[194:197], v[54:57]
	v_mfma_f32_16x16x32_bf16 v[50:53], v[180:183], v[194:197], v[50:53]
	v_mfma_f32_16x16x32_bf16 v[38:41], v[172:175], v[202:205], v[38:41]
	v_mfma_f32_16x16x32_bf16 v[34:37], v[180:183], v[202:205], v[34:37]
	v_mfma_f32_16x16x32_bf16 v[22:25], v[172:175], v[216:219], v[22:25]
	v_mfma_f32_16x16x32_bf16 v[18:21], v[180:183], v[216:219], v[18:21]
	v_mfma_f32_16x16x32_bf16 v[6:9], v[172:175], v[224:227], v[6:9]
	v_mfma_f32_16x16x32_bf16 v[2:5], v[180:183], v[224:227], v[2:5]
	s_setprio 0
	s_barrier
; #define PG8_STAGE(bufoff, gbase, voff) do { _Pragma("unroll") for (int _i = 0; _i < 2; ++_i) \
;         __builtin_amdgcn_global_load_lds((const unsigned*)((const char*)(gbase) + (voff)[_i]), (PG8_LAS unsigned*)(lds + (bufoff) + ldsw + _i * 8192), 16, 0, 0); } while (0)
; #define PG8_LDA(dst, b, h) do { _Pragma("unroll") for (int m = 0; m < 4; ++m) _Pragma("unroll") for (int k = 0; k < 2; ++k) dst[m][k] = *(const PG8_LAS bf16x8*)(lds + PG8_SA(b, h) + aoff + m * 2048 + k * 1024); } while (0)
; #define PG8_LDB(dst, b, h) do { _Pragma("unroll") for (int n = 0; n < 2; ++n) _Pragma("unroll") for (int k = 0; k < 2; ++k) dst[n][k] = *(const PG8_LAS bf16x8*)(lds + PG8_SB(b, h) + boff + n * 2048 + k * 1024); } while (0)
; #define PG8_WAIT_V(n) asm volatile("s_waitcnt vmcnt(" #n ")" ::: "memory")
; #define PG8_WAIT_L(n) asm volatile("s_waitcnt lgkmcnt(" #n ")" ::: "memory")
; #define PG8_BAR __builtin_amdgcn_s_barrier()
; #define PG8_SCHED __builtin_amdgcn_sched_barrier(0)
; template <class Epi, class Sched, bool ALIGN_EPI = false, bool SP2 = false>
; __device__ __forceinline__ void gemm_phase(PG8_LAS unsigned char* lds, const Gemm g, const Sched& S, const Epi& E) {
;     ...
;             PG8_LDB(B0, 1, 0); PG8_LDB(B1, 1, 1); PG8_SCHED; PG8_LDA(At, 1, 0); PG8_STAGE(PG8_SA(0, 1), a2 + hstep, voffA);
;             PG8_WAIT_V(8); PG8_WAIT_L(0); PG8_BAR; PG8_MMA(0, 0, At, B0); PG8_MMA(0, 1, At, B1); PG8_BAR; PG8_SCHED;
;             PG8_LDA(At, 1, 1); PG8_STAGE(PG8_SB(1, 0), b3, voffB); PG8_STAGE(PG8_SB(1, 1), b3 + hstep, voffB); PG8_STAGE(PG8_SA(1, 0), a3, voffA);
;             PG8_WAIT_V(8); PG8_WAIT_L(0); PG8_BAR; PG8_MMA(1, 0, At, B0); PG8_MMA(1, 1, At, B1); PG8_BAR; PG8_SCHED;
	s_add_i32 s49, 0, 0x18000
	s_add_i32 s50, 0, 0x1c000
	ds_read_b128 v[146:149], v248
	ds_read_b128 v[156:159], v248 offset:1024
	ds_read_b128 v[160:163], v248 offset:2048
	ds_read_b128 v[164:167], v248 offset:3072
	ds_read_b128 v[168:171], v249
	ds_read_b128 v[172:175], v249 offset:1024
	ds_read_b128 v[176:179], v249 offset:2048
	ds_read_b128 v[180:183], v249 offset:3072
	s_add_u32 s26, s26, 0x80000
	s_addc_u32 s27, s27, 0
	s_mov_b32 m0, s34
	ds_read_b128 v[190:193], v155 offset:32768
	ds_read_b128 v[194:197], v155 offset:33792
	ds_read_b128 v[198:201], v155 offset:34816
	ds_read_b128 v[202:205], v155 offset:35840
	ds_read_b128 v[206:209], v155 offset:36864
	ds_read_b128 v[216:219], v155 offset:37888
	ds_read_b128 v[220:223], v155 offset:38912
	ds_read_b128 v[224:227], v155 offset:39936
	global_load_lds_dwordx4 v136, s[26:27]
	s_mov_b32 m0, s35
	s_nop 0
	global_load_lds_dwordx4 v132, s[26:27]
	s_waitcnt vmcnt(8)
	s_waitcnt lgkmcnt(0)
	s_barrier
	s_setprio 1
	s_waitcnt lgkmcnt(0)
	v_mfma_f32_16x16x32_bf16 v[126:129], v[146:149], v[190:193], v[126:129]
	v_mfma_f32_16x16x32_bf16 v[122:125], v[160:163], v[190:193], v[122:125]
	v_mfma_f32_16x16x32_bf16 v[110:113], v[146:149], v[198:201], v[110:113]
	v_mfma_f32_16x16x32_bf16 v[106:109], v[160:163], v[198:201], v[106:109]
	v_mfma_f32_16x16x32_bf16 v[94:97], v[146:149], v[206:209], v[94:97]
	v_mfma_f32_16x16x32_bf16 v[90:93], v[160:163], v[206:209], v[90:93]
	v_mfma_f32_16x16x32_bf16 v[78:81], v[146:149], v[220:223], v[78:81]
	v_mfma_f32_16x16x32_bf16 v[74:77], v[160:163], v[220:223], v[74:77]
	v_mfma_f32_16x16x32_bf16 v[126:129], v[156:159], v[194:197], v[126:129]
	v_mfma_f32_16x16x32_bf16 v[122:125], v[164:167], v[194:197], v[122:125]
	v_mfma_f32_16x16x32_bf16 v[110:113], v[156:159], v[202:205], v[110:113]
	v_mfma_f32_16x16x32_bf16 v[106:109], v[164:167], v[202:205], v[106:109]
	v_mfma_f32_16x16x32_bf16 v[94:97], v[156:159], v[216:219], v[94:97]
	v_mfma_f32_16x16x32_bf16 v[90:93], v[164:167], v[216:219], v[90:93]
	v_mfma_f32_16x16x32_bf16 v[78:81], v[156:159], v[224:227], v[78:81]
	v_mfma_f32_16x16x32_bf16 v[74:77], v[164:167], v[224:227], v[74:77]
	s_setprio 0
	s_setprio 1
	v_mfma_f32_16x16x32_bf16 v[118:121], v[168:171], v[190:193], v[118:121]
	v_mfma_f32_16x16x32_bf16 v[114:117], v[176:179], v[190:193], v[114:117]
	v_mfma_f32_16x16x32_bf16 v[102:105], v[168:171], v[198:201], v[102:105]
	v_mfma_f32_16x16x32_bf16 v[98:101], v[176:179], v[198:201], v[98:101]
	v_mfma_f32_16x16x32_bf16 v[86:89], v[168:171], v[206:209], v[86:89]
	v_mfma_f32_16x16x32_bf16 v[82:85], v[176:179], v[206:209], v[82:85]
	v_mfma_f32_16x16x32_bf16 v[70:73], v[168:171], v[220:223], v[70:73]
	v_mfma_f32_16x16x32_bf16 v[66:69], v[176:179], v[220:223], v[66:69]
	v_mfma_f32_16x16x32_bf16 v[118:121], v[172:175], v[194:197], v[118:121]
	v_mfma_f32_16x16x32_bf16 v[114:117], v[180:183], v[194:197], v[114:117]
	v_mfma_f32_16x16x32_bf16 v[102:105], v[172:175], v[202:205], v[102:105]
	v_mfma_f32_16x16x32_bf16 v[98:101], v[180:183], v[202:205], v[98:101]
	v_mfma_f32_16x16x32_bf16 v[86:89], v[172:175], v[216:219], v[86:89]
	v_mfma_f32_16x16x32_bf16 v[82:85], v[180:183], v[216:219], v[82:85]
	v_mfma_f32_16x16x32_bf16 v[70:73], v[172:175], v[224:227], v[70:73]
	v_mfma_f32_16x16x32_bf16 v[66:69], v[180:183], v[224:227], v[66:69]
	s_setprio 0
	s_barrier
	s_add_u32 s98, s24, 0x80
	s_addc_u32 s99, s25, 0
	s_add_u32 s100, s26, 0xfff80080
	s_addc_u32 s101, s27, -1
	s_add_i32 s26, s49, s29
	s_mov_b32 m0, s26
	ds_read_b128 v[190:193], v155 offset:49152
	ds_read_b128 v[194:197], v155 offset:50176
	ds_read_b128 v[198:201], v155 offset:51200
	ds_read_b128 v[202:205], v155 offset:52224
	ds_read_b128 v[206:209], v155 offset:53248
	ds_read_b128 v[216:219], v155 offset:54272
	ds_read_b128 v[220:223], v155 offset:55296
	ds_read_b128 v[224:227], v155 offset:56320
	global_load_lds_dwordx4 v134, s[98:99]
	s_add_i32 m0, s26, 0x2000
	s_add_u32 s24, s24, 0x80080
	s_addc_u32 s25, s25, 0
	s_add_i32 s26, s50, s29
	global_load_lds_dwordx4 v130, s[98:99]
	s_mov_b32 m0, s26
	s_nop 0
	global_load_lds_dwordx4 v134, s[24:25]
	s_add_i32 m0, s26, 0x2000
	s_nop 0
	global_load_lds_dwordx4 v130, s[24:25]
	s_mov_b32 m0, s37
	s_nop 0
	global_load_lds_dwordx4 v136, s[100:101]
	s_mov_b32 m0, s38
	s_nop 0
	global_load_lds_dwordx4 v132, s[100:101]
	s_waitcnt vmcnt(8)
	s_waitcnt lgkmcnt(0)
	s_barrier
	s_setprio 1
	s_waitcnt lgkmcnt(0)
	v_mfma_f32_16x16x32_bf16 v[62:65], v[146:149], v[190:193], v[62:65]
	v_mfma_f32_16x16x32_bf16 v[58:61], v[160:163], v[190:193], v[58:61]
	v_mfma_f32_16x16x32_bf16 v[46:49], v[146:149], v[198:201], v[46:49]
	v_mfma_f32_16x16x32_bf16 v[42:45], v[160:163], v[198:201], v[42:45]
	v_mfma_f32_16x16x32_bf16 v[30:33], v[146:149], v[206:209], v[30:33]
	v_mfma_f32_16x16x32_bf16 v[26:29], v[160:163], v[206:209], v[26:29]
	v_mfma_f32_16x16x32_bf16 v[14:17], v[146:149], v[220:223], v[14:17]
	v_mfma_f32_16x16x32_bf16 v[10:13], v[160:163], v[220:223], v[10:13]
	v_mfma_f32_16x16x32_bf16 v[62:65], v[156:159], v[194:197], v[62:65]
	v_mfma_f32_16x16x32_bf16 v[58:61], v[164:167], v[194:197], v[58:61]
	v_mfma_f32_16x16x32_bf16 v[46:49], v[156:159], v[202:205], v[46:49]
	v_mfma_f32_16x16x32_bf16 v[42:45], v[164:167], v[202:205], v[42:45]
	v_mfma_f32_16x16x32_bf16 v[30:33], v[156:159], v[216:219], v[30:33]
	v_mfma_f32_16x16x32_bf16 v[26:29], v[164:167], v[216:219], v[26:29]
	v_mfma_f32_16x16x32_bf16 v[14:17], v[156:159], v[224:227], v[14:17]
	v_mfma_f32_16x16x32_bf16 v[10:13], v[164:167], v[224:227], v[10:13]
	s_setprio 0
	s_setprio 1
	v_mfma_f32_16x16x32_bf16 v[54:57], v[168:171], v[190:193], v[54:57]
	v_mfma_f32_16x16x32_bf16 v[50:53], v[176:179], v[190:193], v[50:53]
	v_mfma_f32_16x16x32_bf16 v[38:41], v[168:171], v[198:201], v[38:41]
	v_mfma_f32_16x16x32_bf16 v[34:37], v[176:179], v[198:201], v[34:37]
	v_mfma_f32_16x16x32_bf16 v[22:25], v[168:171], v[206:209], v[22:25]
	v_mfma_f32_16x16x32_bf16 v[18:21], v[176:179], v[206:209], v[18:21]
	v_mfma_f32_16x16x32_bf16 v[6:9], v[168:171], v[220:223], v[6:9]
	v_mfma_f32_16x16x32_bf16 v[2:5], v[176:179], v[220:223], v[2:5]
	v_mfma_f32_16x16x32_bf16 v[54:57], v[172:175], v[194:197], v[54:57]
	v_mfma_f32_16x16x32_bf16 v[50:53], v[180:183], v[194:197], v[50:53]
	v_mfma_f32_16x16x32_bf16 v[38:41], v[172:175], v[202:205], v[38:41]
	v_mfma_f32_16x16x32_bf16 v[34:37], v[180:183], v[202:205], v[34:37]
	v_mfma_f32_16x16x32_bf16 v[22:25], v[172:175], v[216:219], v[22:25]
	v_mfma_f32_16x16x32_bf16 v[18:21], v[180:183], v[216:219], v[18:21]
	v_mfma_f32_16x16x32_bf16 v[6:9], v[172:175], v[224:227], v[6:9]
	v_mfma_f32_16x16x32_bf16 v[2:5], v[180:183], v[224:227], v[2:5]
	s_setprio 0
	s_barrier
; __device__ __forceinline__ unsigned cvt_pk_bf16(float lo, float hi) { unsigned r; asm volatile("v_cvt_pk_bf16_f32 %0, %1, %2" : "=v"(r) : "v"(lo), "v"(hi)); return r; }
; #define PG8_BAR __builtin_amdgcn_s_barrier()
;     __device__ __forceinline__ void operator()(const f32x4 (&acc)[2][2][4][2], const Unit& u, int wr, int wc, int fr, int fq) const {
;         const int row0 = u.pm * BM + wr * 64 + fr, col0 = (u.pn % nN) * HALF + wc * 32 + 8 * fq;
; #pragma unroll
;         for (int ai = 0; ai < 2; ++ai)
; #pragma unroll
;             for (int m = 0; m < 4; ++m) { bf16_t* rowp = O + (size_t)(row0 + ai * HALF + m * 16) * ldc + col0;
;                 const f32x4 g0 = acc[ai][0][m][0], g1 = acc[ai][0][m][1], u0 = acc[ai][1][m][0], u1 = acc[ai][1][m][1];
;                 const f32x4 h0 = silu_mul4(g0, u0), h1 = silu_mul4(g1, u1);
;                 u32x4 w; w.x = cvt_pk_bf16(h0[0], h0[1]); w.y = cvt_pk_bf16(h0[2], h0[3]); w.z = cvt_pk_bf16(h1[0], h1[1]); w.w = cvt_pk_bf16(h1[2], h1[3]);
;                 *(u32x4*)(rowp) = w; }
; template <class Epi, class Sched, bool ALIGN_EPI = false, bool SP2 = false>
; __device__ __forceinline__ void gemm_phase(PG8_LAS unsigned char* lds, const Gemm g, const Sched& S, const Epi& E) {
;     ...
;         if constexpr (ALIGN_EPI) { if (wr == 0) PG8_BAR; }
	s_add_i32 s48, s48, 2
	s_add_u32 s22, s22, 0x100
	s_addc_u32 s23, s23, 0
	s_add_u32 s46, s46, 0x100
	s_addc_u32 s47, s47, 0
	s_cmp_gt_u32 s48, 29
	s_cbranch_scc0 .LBB0_872
	v_pk_mul_f32 v[160:161], v[128:129], s[10:11] op_sel_hi:[1,0]
	v_pk_mul_f32 v[162:163], v[126:127], s[10:11] op_sel_hi:[1,0]
	v_exp_f32_e32 v160, v160
	v_exp_f32_e32 v162, v162
	v_exp_f32_e32 v161, v161
	v_exp_f32_e32 v163, v163
	v_pk_mul_f32 v[164:165], v[124:125], s[10:11] op_sel_hi:[1,0]
	v_pk_mul_f32 v[166:167], v[122:123], s[10:11] op_sel_hi:[1,0]
	v_pk_add_f32 v[160:161], v[160:161], 1.0 op_sel_hi:[1,0]
	v_pk_add_f32 v[162:163], v[162:163], 1.0 op_sel_hi:[1,0]
	v_rcp_f32_e32 v160, v160
	v_rcp_f32_e32 v162, v162
	v_rcp_f32_e32 v163, v163
	v_rcp_f32_e32 v161, v161
	v_exp_f32_e32 v166, v166
	v_exp_f32_e32 v164, v164
	v_exp_f32_e32 v165, v165
	v_exp_f32_e32 v167, v167
	s_mul_hi_i32 s13, s43, 0x2e8ba2e9
	s_lshr_b32 s15, s13, 31
	s_lshr_b32 s13, s13, 3
	v_pk_mul_f32 v[128:129], v[128:129], v[160:161]
	v_pk_mul_f32 v[126:127], v[126:127], v[162:163]
	v_pk_add_f32 v[160:161], v[164:165], 1.0 op_sel_hi:[1,0]
	v_pk_add_f32 v[162:163], v[166:167], 1.0 op_sel_hi:[1,0]
	s_add_i32 s13, s13, s15
	v_rcp_f32_e32 v162, v162
	v_rcp_f32_e32 v160, v160
	v_rcp_f32_e32 v161, v161
	v_rcp_f32_e32 v163, v163
	s_mul_i32 s13, s13, 44
	s_sub_i32 s13, s43, s13
	v_readlane_b32 s22, v247, 13
	v_lshl_or_b32 v148, s13, 7, v152
	v_readlane_b32 s23, v247, 14
	v_lshl_add_u32 v156, s20, 8, v150
	v_ashrrev_i32_e32 v149, 31, v148
	v_mov_b64_e32 v[146:147], s[22:23]
	v_pk_mul_f32 v[124:125], v[124:125], v[160:161]
	v_pk_mul_f32 v[122:123], v[122:123], v[162:163]
	v_mad_i64_i32 v[158:159], s[22:23], v156, s42, v[146:147]
	v_lshlrev_b64 v[148:149], 1, v[148:149]
	v_pk_mul_f32 v[124:125], v[124:125], v[116:117]
	v_pk_mul_f32 v[116:117], v[122:123], v[114:115]
	v_lshl_add_u64 v[158:159], v[158:159], 0, v[148:149]
	v_pk_mul_f32 v[120:121], v[128:129], v[120:121]
	v_pk_mul_f32 v[118:119], v[126:127], v[118:119]
	v_pk_mul_f32 v[122:123], v[106:107], s[10:11] op_sel_hi:[1,0]
	v_cvt_pk_bf16_f32 v114, v118, v119
	v_cvt_pk_bf16_f32 v115, v120, v121
	v_cvt_pk_bf16_f32 v116, v116, v117
	v_cvt_pk_bf16_f32 v117, v124, v125
	global_store_dwordx4 v[158:159], v[114:117], off
	v_pk_mul_f32 v[120:121], v[108:109], s[10:11] op_sel_hi:[1,0]
	v_exp_f32_e32 v122, v122
	v_pk_mul_f32 v[114:115], v[112:113], s[10:11] op_sel_hi:[1,0]
	v_pk_mul_f32 v[116:117], v[110:111], s[10:11] op_sel_hi:[1,0]
	v_exp_f32_e32 v114, v114
	v_exp_f32_e32 v116, v116
	v_exp_f32_e32 v117, v117
	v_exp_f32_e32 v115, v115
	v_exp_f32_e32 v120, v120
	v_exp_f32_e32 v121, v121
	v_pk_add_f32 v[116:117], v[116:117], 1.0 op_sel_hi:[1,0]
	v_pk_add_f32 v[114:115], v[114:115], 1.0 op_sel_hi:[1,0]
	v_rcp_f32_e32 v116, v116
	v_rcp_f32_e32 v117, v117
	v_rcp_f32_e32 v114, v114
	v_rcp_f32_e32 v115, v115
	v_exp_f32_e32 v123, v123
	v_pk_mul_f32 v[110:111], v[110:111], v[116:117]
	v_or_b32_e32 v118, 16, v156
	v_pk_mul_f32 v[112:113], v[112:113], v[114:115]
	v_pk_add_f32 v[114:115], v[120:121], 1.0 op_sel_hi:[1,0]
	v_pk_add_f32 v[116:117], v[122:123], 1.0 op_sel_hi:[1,0]
	v_rcp_f32_e32 v114, v114
	v_rcp_f32_e32 v116, v116
	v_rcp_f32_e32 v115, v115
	v_rcp_f32_e32 v117, v117
	v_mad_i64_i32 v[118:119], s[22:23], v118, s42, v[146:147]
	v_pk_mul_f32 v[108:109], v[108:109], v[114:115]
	v_pk_mul_f32 v[106:107], v[106:107], v[116:117]
	v_pk_mul_f32 v[108:109], v[108:109], v[100:101]
	v_pk_mul_f32 v[100:101], v[106:107], v[98:99]
	v_lshl_add_u64 v[118:119], v[118:119], 0, v[148:149]
	v_pk_mul_f32 v[104:105], v[112:113], v[104:105]
	v_pk_mul_f32 v[102:103], v[110:111], v[102:103]
	v_pk_mul_f32 v[106:107], v[90:91], s[10:11] op_sel_hi:[1,0]
	v_cvt_pk_bf16_f32 v98, v102, v103
	v_cvt_pk_bf16_f32 v99, v104, v105
	v_cvt_pk_bf16_f32 v100, v100, v101
	v_cvt_pk_bf16_f32 v101, v108, v109
	global_store_dwordx4 v[118:119], v[98:101], off
	s_and_b64 vcc, exec, s[8:9]
	s_cbranch_vccz .LBB0_875
	s_barrier
.LBB0_875:
	v_pk_mul_f32 v[104:105], v[92:93], s[10:11] op_sel_hi:[1,0]
	v_exp_f32_e32 v106, v106
	v_pk_mul_f32 v[98:99], v[96:97], s[10:11] op_sel_hi:[1,0]
	v_pk_mul_f32 v[100:101], v[94:95], s[10:11] op_sel_hi:[1,0]
	v_exp_f32_e32 v98, v98
	v_exp_f32_e32 v100, v100
	v_exp_f32_e32 v101, v101
	v_exp_f32_e32 v99, v99
	v_exp_f32_e32 v104, v104
	v_exp_f32_e32 v105, v105
	v_pk_add_f32 v[100:101], v[100:101], 1.0 op_sel_hi:[1,0]
	v_pk_add_f32 v[98:99], v[98:99], 1.0 op_sel_hi:[1,0]
	v_rcp_f32_e32 v100, v100
	v_rcp_f32_e32 v101, v101
	v_rcp_f32_e32 v98, v98
	v_rcp_f32_e32 v99, v99
	v_exp_f32_e32 v107, v107
	v_pk_mul_f32 v[94:95], v[94:95], v[100:101]
	v_or_b32_e32 v102, 32, v156
	v_pk_mul_f32 v[96:97], v[96:97], v[98:99]
	v_pk_add_f32 v[98:99], v[104:105], 1.0 op_sel_hi:[1,0]
	v_pk_add_f32 v[100:101], v[106:107], 1.0 op_sel_hi:[1,0]
	v_rcp_f32_e32 v98, v98
	v_rcp_f32_e32 v100, v100
	v_rcp_f32_e32 v99, v99
	v_rcp_f32_e32 v101, v101
	v_mad_i64_i32 v[102:103], s[22:23], v102, s42, v[146:147]
	v_pk_mul_f32 v[92:93], v[92:93], v[98:99]
	v_pk_mul_f32 v[90:91], v[90:91], v[100:101]
	v_pk_mul_f32 v[92:93], v[92:93], v[84:85]
	v_pk_mul_f32 v[84:85], v[90:91], v[82:83]
	v_lshl_add_u64 v[102:103], v[102:103], 0, v[148:149]
	v_pk_mul_f32 v[88:89], v[96:97], v[88:89]
	v_pk_mul_f32 v[86:87], v[94:95], v[86:87]
	v_pk_mul_f32 v[90:91], v[74:75], s[10:11] op_sel_hi:[1,0]
	v_cvt_pk_bf16_f32 v82, v86, v87
	v_cvt_pk_bf16_f32 v83, v88, v89
	v_cvt_pk_bf16_f32 v84, v84, v85
	v_cvt_pk_bf16_f32 v85, v92, v93
	global_store_dwordx4 v[102:103], v[82:85], off
	v_pk_mul_f32 v[88:89], v[76:77], s[10:11] op_sel_hi:[1,0]
	v_exp_f32_e32 v90, v90
	v_pk_mul_f32 v[82:83], v[80:81], s[10:11] op_sel_hi:[1,0]
; __device__ __forceinline__ unsigned cvt_pk_bf16(float lo, float hi) { unsigned r; asm volatile("v_cvt_pk_bf16_f32 %0, %1, %2" : "=v"(r) : "v"(lo), "v"(hi)); return r; }
;     __device__ __forceinline__ void operator()(const f32x4 (&acc)[2][2][4][2], const Unit& u, int wr, int wc, int fr, int fq) const {
;     ...
; #pragma unroll
;         for (int ai = 0; ai < 2; ++ai)
; #pragma unroll
;             for (int m = 0; m < 4; ++m) { bf16_t* rowp = O + (size_t)(row0 + ai * HALF + m * 16) * ldc + col0;
;                 const f32x4 g0 = acc[ai][0][m][0], g1 = acc[ai][0][m][1], u0 = acc[ai][1][m][0], u1 = acc[ai][1][m][1];
;                 const f32x4 h0 = silu_mul4(g0, u0), h1 = silu_mul4(g1, u1);
;                 u32x4 w; w.x = cvt_pk_bf16(h0[0], h0[1]); w.y = cvt_pk_bf16(h0[2], h0[3]); w.z = cvt_pk_bf16(h1[0], h1[1]); w.w = cvt_pk_bf16(h1[2], h1[3]);
;                 *(u32x4*)(rowp) = w; }
	v_pk_mul_f32 v[84:85], v[78:79], s[10:11] op_sel_hi:[1,0]
	v_exp_f32_e32 v82, v82
	v_exp_f32_e32 v84, v84
	v_exp_f32_e32 v85, v85
	v_exp_f32_e32 v83, v83
	v_exp_f32_e32 v88, v88
	v_exp_f32_e32 v89, v89
	v_pk_add_f32 v[84:85], v[84:85], 1.0 op_sel_hi:[1,0]
	v_pk_add_f32 v[82:83], v[82:83], 1.0 op_sel_hi:[1,0]
	v_rcp_f32_e32 v84, v84
	v_rcp_f32_e32 v85, v85
	v_rcp_f32_e32 v82, v82
	v_rcp_f32_e32 v83, v83
	v_exp_f32_e32 v91, v91
	v_pk_mul_f32 v[78:79], v[78:79], v[84:85]
	v_or_b32_e32 v86, 48, v156
	v_pk_mul_f32 v[80:81], v[80:81], v[82:83]
	v_pk_add_f32 v[82:83], v[88:89], 1.0 op_sel_hi:[1,0]
	v_pk_add_f32 v[84:85], v[90:91], 1.0 op_sel_hi:[1,0]
	v_rcp_f32_e32 v82, v82
	v_rcp_f32_e32 v84, v84
	v_rcp_f32_e32 v83, v83
	v_rcp_f32_e32 v85, v85
	v_mad_i64_i32 v[86:87], s[22:23], v86, s42, v[146:147]
	v_pk_mul_f32 v[76:77], v[76:77], v[82:83]
	v_pk_mul_f32 v[74:75], v[74:75], v[84:85]
	v_pk_mul_f32 v[76:77], v[76:77], v[68:69]
	v_pk_mul_f32 v[68:69], v[74:75], v[66:67]
	v_lshl_add_u64 v[86:87], v[86:87], 0, v[148:149]
	v_pk_mul_f32 v[72:73], v[80:81], v[72:73]
	v_pk_mul_f32 v[70:71], v[78:79], v[70:71]
	v_pk_mul_f32 v[74:75], v[58:59], s[10:11] op_sel_hi:[1,0]
	v_cvt_pk_bf16_f32 v66, v70, v71
	v_cvt_pk_bf16_f32 v67, v72, v73
	v_cvt_pk_bf16_f32 v68, v68, v69
	v_cvt_pk_bf16_f32 v69, v76, v77
	global_store_dwordx4 v[86:87], v[66:69], off
	v_pk_mul_f32 v[72:73], v[60:61], s[10:11] op_sel_hi:[1,0]
	v_exp_f32_e32 v74, v74
	v_pk_mul_f32 v[66:67], v[64:65], s[10:11] op_sel_hi:[1,0]
	v_pk_mul_f32 v[68:69], v[62:63], s[10:11] op_sel_hi:[1,0]
	v_exp_f32_e32 v66, v66
	v_exp_f32_e32 v68, v68
	v_exp_f32_e32 v69, v69
	v_exp_f32_e32 v67, v67
	v_exp_f32_e32 v72, v72
	v_exp_f32_e32 v73, v73
	v_pk_add_f32 v[68:69], v[68:69], 1.0 op_sel_hi:[1,0]
	v_pk_add_f32 v[66:67], v[66:67], 1.0 op_sel_hi:[1,0]
	v_rcp_f32_e32 v68, v68
	v_rcp_f32_e32 v69, v69
	v_rcp_f32_e32 v66, v66
	v_rcp_f32_e32 v67, v67
	v_exp_f32_e32 v75, v75
	v_pk_mul_f32 v[62:63], v[62:63], v[68:69]
	v_add_u32_e32 v70, 0x80, v156
	v_pk_mul_f32 v[64:65], v[64:65], v[66:67]
	v_pk_add_f32 v[66:67], v[72:73], 1.0 op_sel_hi:[1,0]
	v_pk_add_f32 v[68:69], v[74:75], 1.0 op_sel_hi:[1,0]
	v_rcp_f32_e32 v66, v66
	v_rcp_f32_e32 v68, v68
	v_rcp_f32_e32 v67, v67
	v_rcp_f32_e32 v69, v69
	v_mad_i64_i32 v[70:71], s[22:23], v70, s42, v[146:147]
	v_pk_mul_f32 v[60:61], v[60:61], v[66:67]
	v_pk_mul_f32 v[58:59], v[58:59], v[68:69]
	v_pk_mul_f32 v[60:61], v[60:61], v[52:53]
	v_pk_mul_f32 v[52:53], v[58:59], v[50:51]
	v_lshl_add_u64 v[70:71], v[70:71], 0, v[148:149]
	v_pk_mul_f32 v[56:57], v[64:65], v[56:57]
	v_pk_mul_f32 v[54:55], v[62:63], v[54:55]
	v_pk_mul_f32 v[58:59], v[42:43], s[10:11] op_sel_hi:[1,0]
	v_cvt_pk_bf16_f32 v50, v54, v55
	v_cvt_pk_bf16_f32 v51, v56, v57
	v_cvt_pk_bf16_f32 v52, v52, v53
	v_cvt_pk_bf16_f32 v53, v60, v61
	global_store_dwordx4 v[70:71], v[50:53], off
	v_pk_mul_f32 v[56:57], v[44:45], s[10:11] op_sel_hi:[1,0]
	v_exp_f32_e32 v58, v58
	v_pk_mul_f32 v[50:51], v[48:49], s[10:11] op_sel_hi:[1,0]
	v_pk_mul_f32 v[52:53], v[46:47], s[10:11] op_sel_hi:[1,0]
	v_exp_f32_e32 v50, v50
	v_exp_f32_e32 v52, v52
	v_exp_f32_e32 v53, v53
	v_exp_f32_e32 v51, v51
	v_exp_f32_e32 v56, v56
	v_exp_f32_e32 v57, v57
	v_pk_add_f32 v[52:53], v[52:53], 1.0 op_sel_hi:[1,0]
	v_pk_add_f32 v[50:51], v[50:51], 1.0 op_sel_hi:[1,0]
	v_rcp_f32_e32 v52, v52
	v_rcp_f32_e32 v53, v53
	v_rcp_f32_e32 v50, v50
	v_rcp_f32_e32 v51, v51
	v_exp_f32_e32 v59, v59
	v_pk_mul_f32 v[46:47], v[46:47], v[52:53]
	v_add_u32_e32 v54, 0x90, v156
	v_pk_mul_f32 v[48:49], v[48:49], v[50:51]
	v_pk_add_f32 v[50:51], v[56:57], 1.0 op_sel_hi:[1,0]
	v_pk_add_f32 v[52:53], v[58:59], 1.0 op_sel_hi:[1,0]
	v_rcp_f32_e32 v50, v50
	v_rcp_f32_e32 v52, v52
	v_rcp_f32_e32 v51, v51
; __device__ __forceinline__ unsigned cvt_pk_bf16(float lo, float hi) { unsigned r; asm volatile("v_cvt_pk_bf16_f32 %0, %1, %2" : "=v"(r) : "v"(lo), "v"(hi)); return r; }
; #define PG8_BAR __builtin_amdgcn_s_barrier()
;     __device__ __forceinline__ void operator()(const f32x4 (&acc)[2][2][4][2], const Unit& u, int wr, int wc, int fr, int fq) const {
;     ...
; #pragma unroll
;         for (int ai = 0; ai < 2; ++ai)
; #pragma unroll
;             for (int m = 0; m < 4; ++m) { bf16_t* rowp = O + (size_t)(row0 + ai * HALF + m * 16) * ldc + col0;
;                 const f32x4 g0 = acc[ai][0][m][0], g1 = acc[ai][0][m][1], u0 = acc[ai][1][m][0], u1 = acc[ai][1][m][1];
;                 const f32x4 h0 = silu_mul4(g0, u0), h1 = silu_mul4(g1, u1);
;                 u32x4 w; w.x = cvt_pk_bf16(h0[0], h0[1]); w.y = cvt_pk_bf16(h0[2], h0[3]); w.z = cvt_pk_bf16(h1[0], h1[1]); w.w = cvt_pk_bf16(h1[2], h1[3]);
;                 *(u32x4*)(rowp) = w; }
; template <class Epi, class Sched, bool ALIGN_EPI = false, bool SP2 = false>
; __device__ __forceinline__ void gemm_phase(PG8_LAS unsigned char* lds, const Gemm g, const Sched& S, const Epi& E) {
;     ...
;         if (!has_next) break;
; #pragma unroll
;         for (int a = 0; a < 2; ++a)
; #pragma unroll
;             for (int b = 0; b < 2; ++b)
; #pragma unroll
;                 for (int m = 0; m < 4; ++m)
; #pragma unroll
;                     for (int n = 0; n < 2; ++n) acc[a][b][m][n] = (f32x4){0.f, 0.f, 0.f, 0.f};
;         cur = nxt; cA = nA; cB = nB; ++ui;
;         if constexpr (ALIGN_EPI) { if (wr == 1) PG8_BAR; }
	v_rcp_f32_e32 v53, v53
	v_mad_i64_i32 v[54:55], s[22:23], v54, s42, v[146:147]
	v_pk_mul_f32 v[44:45], v[44:45], v[50:51]
	v_pk_mul_f32 v[42:43], v[42:43], v[52:53]
	v_pk_mul_f32 v[44:45], v[44:45], v[36:37]
	v_pk_mul_f32 v[36:37], v[42:43], v[34:35]
	v_lshl_add_u64 v[54:55], v[54:55], 0, v[148:149]
	v_pk_mul_f32 v[40:41], v[48:49], v[40:41]
	v_pk_mul_f32 v[38:39], v[46:47], v[38:39]
	v_pk_mul_f32 v[42:43], v[26:27], s[10:11] op_sel_hi:[1,0]
	v_cvt_pk_bf16_f32 v34, v38, v39
	v_cvt_pk_bf16_f32 v35, v40, v41
	v_cvt_pk_bf16_f32 v36, v36, v37
	v_cvt_pk_bf16_f32 v37, v44, v45
	global_store_dwordx4 v[54:55], v[34:37], off
	v_pk_mul_f32 v[40:41], v[28:29], s[10:11] op_sel_hi:[1,0]
	v_exp_f32_e32 v42, v42
	v_pk_mul_f32 v[34:35], v[32:33], s[10:11] op_sel_hi:[1,0]
	v_pk_mul_f32 v[36:37], v[30:31], s[10:11] op_sel_hi:[1,0]
	v_exp_f32_e32 v34, v34
	v_exp_f32_e32 v36, v36
	v_exp_f32_e32 v37, v37
	v_exp_f32_e32 v35, v35
	v_exp_f32_e32 v40, v40
	v_exp_f32_e32 v41, v41
	v_pk_add_f32 v[36:37], v[36:37], 1.0 op_sel_hi:[1,0]
	v_pk_add_f32 v[34:35], v[34:35], 1.0 op_sel_hi:[1,0]
	v_rcp_f32_e32 v36, v36
	v_rcp_f32_e32 v37, v37
	v_rcp_f32_e32 v34, v34
	v_rcp_f32_e32 v35, v35
	v_exp_f32_e32 v43, v43
	v_pk_mul_f32 v[30:31], v[30:31], v[36:37]
	v_add_u32_e32 v38, 0xa0, v156
	v_pk_mul_f32 v[32:33], v[32:33], v[34:35]
	v_pk_add_f32 v[34:35], v[40:41], 1.0 op_sel_hi:[1,0]
	v_pk_add_f32 v[36:37], v[42:43], 1.0 op_sel_hi:[1,0]
	v_rcp_f32_e32 v34, v34
	v_rcp_f32_e32 v36, v36
	v_rcp_f32_e32 v35, v35
	v_rcp_f32_e32 v37, v37
	v_mad_i64_i32 v[38:39], s[22:23], v38, s42, v[146:147]
	v_pk_mul_f32 v[28:29], v[28:29], v[34:35]
	v_pk_mul_f32 v[26:27], v[26:27], v[36:37]
	v_pk_mul_f32 v[28:29], v[28:29], v[20:21]
	v_pk_mul_f32 v[20:21], v[26:27], v[18:19]
	v_lshl_add_u64 v[38:39], v[38:39], 0, v[148:149]
	v_pk_mul_f32 v[24:25], v[32:33], v[24:25]
	v_pk_mul_f32 v[22:23], v[30:31], v[22:23]
	v_pk_mul_f32 v[26:27], v[10:11], s[10:11] op_sel_hi:[1,0]
	v_cvt_pk_bf16_f32 v18, v22, v23
	v_cvt_pk_bf16_f32 v19, v24, v25
	v_cvt_pk_bf16_f32 v20, v20, v21
	v_cvt_pk_bf16_f32 v21, v28, v29
	global_store_dwordx4 v[38:39], v[18:21], off
	v_pk_mul_f32 v[24:25], v[12:13], s[10:11] op_sel_hi:[1,0]
	v_exp_f32_e32 v26, v26
	v_pk_mul_f32 v[18:19], v[16:17], s[10:11] op_sel_hi:[1,0]
	v_pk_mul_f32 v[20:21], v[14:15], s[10:11] op_sel_hi:[1,0]
	v_exp_f32_e32 v18, v18
	v_exp_f32_e32 v20, v20
	v_exp_f32_e32 v21, v21
	v_exp_f32_e32 v19, v19
	v_exp_f32_e32 v24, v24
	v_exp_f32_e32 v25, v25
	v_pk_add_f32 v[20:21], v[20:21], 1.0 op_sel_hi:[1,0]
	v_pk_add_f32 v[18:19], v[18:19], 1.0 op_sel_hi:[1,0]
	v_rcp_f32_e32 v20, v20
	v_rcp_f32_e32 v21, v21
	v_rcp_f32_e32 v18, v18
	v_rcp_f32_e32 v19, v19
	v_exp_f32_e32 v27, v27
	v_pk_mul_f32 v[14:15], v[14:15], v[20:21]
	v_add_u32_e32 v22, 0xb0, v156
	v_pk_mul_f32 v[16:17], v[16:17], v[18:19]
	v_pk_add_f32 v[18:19], v[24:25], 1.0 op_sel_hi:[1,0]
	v_pk_add_f32 v[20:21], v[26:27], 1.0 op_sel_hi:[1,0]
	v_rcp_f32_e32 v18, v18
	v_rcp_f32_e32 v20, v20
	v_rcp_f32_e32 v19, v19
	v_rcp_f32_e32 v21, v21
	v_mad_i64_i32 v[22:23], s[22:23], v22, s42, v[146:147]
	v_pk_mul_f32 v[12:13], v[12:13], v[18:19]
	v_pk_mul_f32 v[10:11], v[10:11], v[20:21]
	v_lshl_add_u64 v[22:23], v[22:23], 0, v[148:149]
	v_pk_mul_f32 v[12:13], v[12:13], v[4:5]
	v_pk_mul_f32 v[4:5], v[10:11], v[2:3]
	s_andn2_b64 vcc, exec, s[2:3]
	s_mov_b64 s[2:3], -1
	v_pk_mul_f32 v[8:9], v[16:17], v[8:9]
	v_pk_mul_f32 v[6:7], v[14:15], v[6:7]
	s_nop 0
	v_cvt_pk_bf16_f32 v2, v6, v7
	v_cvt_pk_bf16_f32 v3, v8, v9
	v_cvt_pk_bf16_f32 v4, v4, v5
	v_cvt_pk_bf16_f32 v5, v12, v13
	global_store_dwordx4 v[22:23], v[2:5], off
	s_cbranch_vccnz .LBB0_868
	s_andn2_b64 vcc, exec, s[4:5]
	s_cbranch_vccnz .LBB0_867
	s_barrier
	s_branch .LBB0_867

; #define PG8_STAGE(bufoff, gbase, voff) do { _Pragma("unroll") for (int _i = 0; _i < 2; ++_i) \
;         __builtin_amdgcn_global_load_lds((const unsigned*)((const char*)(gbase) + (voff)[_i]), (PG8_LAS unsigned*)(lds + (bufoff) + ldsw + _i * 8192), 16, 0, 0); } while (0)
; #define PG8_LDA(dst, b, h) do { _Pragma("unroll") for (int m = 0; m < 4; ++m) _Pragma("unroll") for (int k = 0; k < 2; ++k) dst[m][k] = *(const PG8_LAS bf16x8*)(lds + PG8_SA(b, h) + aoff + m * 2048 + k * 1024); } while (0)
; #define PG8_LDB(dst, b, h) do { _Pragma("unroll") for (int n = 0; n < 2; ++n) _Pragma("unroll") for (int k = 0; k < 2; ++k) dst[n][k] = *(const PG8_LAS bf16x8*)(lds + PG8_SB(b, h) + boff + n * 2048 + k * 1024); } while (0)
; #define PG8_WAIT_V(n) asm volatile("s_waitcnt vmcnt(" #n ")" ::: "memory")
; #define PG8_WAIT_L(n) asm volatile("s_waitcnt lgkmcnt(" #n ")" ::: "memory")
; #define PG8_BAR __builtin_amdgcn_s_barrier()
; #define PG8_SCHED __builtin_amdgcn_sched_barrier(0)
; template <class Epi, class Sched, bool ALIGN_EPI = false, bool SP2 = false>
; __device__ __forceinline__ void gemm_phase(PG8_LAS unsigned char* lds, const Gemm g, const Sched& S, const Epi& E) {
;     ...
;             PG8_LDB(B0, 0, 0); PG8_LDB(B1, 0, 1); PG8_SCHED; PG8_LDA(At, 0, 0); PG8_STAGE(PG8_SA(1, 1), a1 + hstep, voffA);
;             PG8_WAIT_V(8); PG8_WAIT_L(0); PG8_BAR; PG8_MMA(0, 0, At, B0); PG8_MMA(0, 1, At, B1); PG8_BAR; PG8_SCHED;
;             PG8_LDA(At, 0, 1); PG8_STAGE(PG8_SB(0, 0), b2, voffB); PG8_STAGE(PG8_SB(0, 1), b2 + hstep, voffB); PG8_STAGE(PG8_SA(0, 0), a2, voffA);
;             PG8_WAIT_V(8); PG8_WAIT_L(0); PG8_BAR; PG8_MMA(1, 0, At, B0); PG8_MMA(1, 1, At, B1); PG8_BAR; PG8_SCHED;
;             PG8_LDB(B0, 1, 0); PG8_LDB(B1, 1, 1); PG8_SCHED; PG8_LDA(At, 1, 0); PG8_STAGE(PG8_SA(0, 1), a2 + hstep, voffA);
;             PG8_WAIT_V(8); PG8_WAIT_L(0); PG8_BAR; PG8_MMA(0, 0, At, B0); PG8_MMA(0, 1, At, B1); PG8_BAR; PG8_SCHED;
;             PG8_LDA(At, 1, 1); PG8_STAGE(PG8_SB(1, 0), b3, voffB); PG8_STAGE(PG8_SB(1, 1), b3 + hstep, voffB); PG8_STAGE(PG8_SA(1, 0), a3, voffA);
;             PG8_WAIT_V(8); PG8_WAIT_L(0); PG8_BAR; PG8_MMA(1, 0, At, B0); PG8_MMA(1, 1, At, B1); PG8_BAR; PG8_SCHED;
.LBB0_951:
	ds_read_b128 v[130:133], v177
	ds_read_b128 v[134:137], v177 offset:1024
	ds_read_b128 v[138:141], v177 offset:2048
	ds_read_b128 v[142:145], v177 offset:3072
	ds_read_b128 v[146:149], v178
	ds_read_b128 v[150:153], v178 offset:1024
	ds_read_b128 v[170:173], v178 offset:2048
	ds_read_b128 v[180:183], v178 offset:3072
	s_add_u32 s16, s14, 0xffea0080
	s_addc_u32 s17, s15, -1
	s_cmpk_eq_i32 s50, 0x54
	s_cselect_b32 s19, s5, s17
	s_cselect_b32 s18, s4, s16
	s_cselect_b32 s17, s13, s49
	s_cselect_b32 s16, s12, s48
	s_add_i32 m0, s24, 0xc000
	ds_read_b128 v[190:193], v179
	ds_read_b128 v[194:197], v179 offset:1024
	ds_read_b128 v[198:201], v179 offset:2048
	ds_read_b128 v[202:205], v179 offset:3072
	ds_read_b128 v[206:209], v179 offset:4096
	ds_read_b128 v[216:219], v179 offset:5120
	ds_read_b128 v[220:223], v179 offset:6144
	ds_read_b128 v[224:227], v179 offset:7168
	global_load_lds_dwordx4 v162, s[14:15]
	s_add_i32 m0, s24, 0xe000
	s_nop 0
	global_load_lds_dwordx4 v164, s[14:15]
	s_waitcnt vmcnt(8)
	s_waitcnt lgkmcnt(0)
	s_barrier
	s_setprio 1
	s_waitcnt lgkmcnt(0)
	v_mfma_f32_16x16x32_bf16 v[126:129], v[130:133], v[190:193], v[126:129]
	v_mfma_f32_16x16x32_bf16 v[122:125], v[138:141], v[190:193], v[122:125]
	v_mfma_f32_16x16x32_bf16 v[110:113], v[130:133], v[198:201], v[110:113]
	v_mfma_f32_16x16x32_bf16 v[106:109], v[138:141], v[198:201], v[106:109]
	v_mfma_f32_16x16x32_bf16 v[98:101], v[130:133], v[206:209], v[98:101]
	v_mfma_f32_16x16x32_bf16 v[90:93], v[138:141], v[206:209], v[90:93]
	v_mfma_f32_16x16x32_bf16 v[82:85], v[130:133], v[220:223], v[82:85]
	v_mfma_f32_16x16x32_bf16 v[74:77], v[138:141], v[220:223], v[74:77]
	v_mfma_f32_16x16x32_bf16 v[126:129], v[134:137], v[194:197], v[126:129]
	v_mfma_f32_16x16x32_bf16 v[122:125], v[142:145], v[194:197], v[122:125]
	v_mfma_f32_16x16x32_bf16 v[110:113], v[134:137], v[202:205], v[110:113]
	v_mfma_f32_16x16x32_bf16 v[106:109], v[142:145], v[202:205], v[106:109]
	v_mfma_f32_16x16x32_bf16 v[98:101], v[134:137], v[216:219], v[98:101]
	v_mfma_f32_16x16x32_bf16 v[90:93], v[142:145], v[216:219], v[90:93]
	v_mfma_f32_16x16x32_bf16 v[82:85], v[134:137], v[224:227], v[82:85]
	v_mfma_f32_16x16x32_bf16 v[74:77], v[142:145], v[224:227], v[74:77]
	s_setprio 0
	s_setprio 1
	v_mfma_f32_16x16x32_bf16 v[118:121], v[146:149], v[190:193], v[118:121]
	v_mfma_f32_16x16x32_bf16 v[114:117], v[170:173], v[190:193], v[114:117]
	v_mfma_f32_16x16x32_bf16 v[102:105], v[146:149], v[198:201], v[102:105]
	v_mfma_f32_16x16x32_bf16 v[94:97], v[170:173], v[198:201], v[94:97]
	v_mfma_f32_16x16x32_bf16 v[86:89], v[146:149], v[206:209], v[86:89]
	v_mfma_f32_16x16x32_bf16 v[78:81], v[170:173], v[206:209], v[78:81]
	v_mfma_f32_16x16x32_bf16 v[70:73], v[146:149], v[220:223], v[70:73]
	v_mfma_f32_16x16x32_bf16 v[66:69], v[170:173], v[220:223], v[66:69]
	v_mfma_f32_16x16x32_bf16 v[118:121], v[150:153], v[194:197], v[118:121]
	v_mfma_f32_16x16x32_bf16 v[114:117], v[180:183], v[194:197], v[114:117]
	v_mfma_f32_16x16x32_bf16 v[102:105], v[150:153], v[202:205], v[102:105]
	v_mfma_f32_16x16x32_bf16 v[94:97], v[180:183], v[202:205], v[94:97]
	v_mfma_f32_16x16x32_bf16 v[86:89], v[150:153], v[216:219], v[86:89]
	v_mfma_f32_16x16x32_bf16 v[78:81], v[180:183], v[216:219], v[78:81]
	v_mfma_f32_16x16x32_bf16 v[70:73], v[150:153], v[224:227], v[70:73]
	v_mfma_f32_16x16x32_bf16 v[66:69], v[180:183], v[224:227], v[66:69]
	s_setprio 0
	s_barrier
	s_add_i32 s51, s36, s23
	s_mov_b32 m0, s51
	ds_read_b128 v[190:193], v179 offset:16384
	ds_read_b128 v[194:197], v179 offset:17408
	ds_read_b128 v[198:201], v179 offset:18432
	ds_read_b128 v[202:205], v179 offset:19456
	ds_read_b128 v[206:209], v179 offset:20480
	ds_read_b128 v[216:219], v179 offset:21504
	ds_read_b128 v[220:223], v179 offset:22528
	ds_read_b128 v[224:227], v179 offset:23552
	global_load_lds_dwordx4 v156, s[16:17]
	s_add_i32 m0, s51, 0x2000
	s_add_u32 s52, s16, 0x160000
	s_addc_u32 s53, s17, 0
	s_add_i32 s51, s37, s23
	global_load_lds_dwordx4 v160, s[16:17]
	s_mov_b32 m0, s51
	s_nop 0
	global_load_lds_dwordx4 v156, s[52:53]
	s_add_i32 m0, s51, 0x2000
	s_nop 0
	global_load_lds_dwordx4 v160, s[52:53]
	s_mov_b32 m0, s24
	s_nop 0
	global_load_lds_dwordx4 v154, s[18:19]
	s_mov_b32 m0, s25
	s_nop 0
	global_load_lds_dwordx4 v158, s[18:19]
	s_waitcnt vmcnt(8)
	s_waitcnt lgkmcnt(0)
	s_barrier
	s_setprio 1
	s_waitcnt lgkmcnt(0)
	v_mfma_f32_16x16x32_bf16 v[62:65], v[130:133], v[190:193], v[62:65]
	v_mfma_f32_16x16x32_bf16 v[58:61], v[138:141], v[190:193], v[58:61]
	v_mfma_f32_16x16x32_bf16 v[50:53], v[130:133], v[198:201], v[50:53]
	v_mfma_f32_16x16x32_bf16 v[42:45], v[138:141], v[198:201], v[42:45]
	v_mfma_f32_16x16x32_bf16 v[34:37], v[130:133], v[206:209], v[34:37]
	v_mfma_f32_16x16x32_bf16 v[26:29], v[138:141], v[206:209], v[26:29]
	v_mfma_f32_16x16x32_bf16 v[18:21], v[130:133], v[220:223], v[18:21]
	v_mfma_f32_16x16x32_bf16 v[10:13], v[138:141], v[220:223], v[10:13]
	v_mfma_f32_16x16x32_bf16 v[62:65], v[134:137], v[194:197], v[62:65]
	v_mfma_f32_16x16x32_bf16 v[58:61], v[142:145], v[194:197], v[58:61]
	v_mfma_f32_16x16x32_bf16 v[50:53], v[134:137], v[202:205], v[50:53]
	v_mfma_f32_16x16x32_bf16 v[42:45], v[142:145], v[202:205], v[42:45]
	v_mfma_f32_16x16x32_bf16 v[34:37], v[134:137], v[216:219], v[34:37]
	v_mfma_f32_16x16x32_bf16 v[26:29], v[142:145], v[216:219], v[26:29]
	v_mfma_f32_16x16x32_bf16 v[18:21], v[134:137], v[224:227], v[18:21]
	v_mfma_f32_16x16x32_bf16 v[10:13], v[142:145], v[224:227], v[10:13]
	s_setprio 0
	s_setprio 1
	v_mfma_f32_16x16x32_bf16 v[54:57], v[146:149], v[190:193], v[54:57]
	v_mfma_f32_16x16x32_bf16 v[46:49], v[170:173], v[190:193], v[46:49]
	v_mfma_f32_16x16x32_bf16 v[38:41], v[146:149], v[198:201], v[38:41]
	v_mfma_f32_16x16x32_bf16 v[30:33], v[170:173], v[198:201], v[30:33]
	v_mfma_f32_16x16x32_bf16 v[22:25], v[146:149], v[206:209], v[22:25]
	v_mfma_f32_16x16x32_bf16 v[14:17], v[170:173], v[206:209], v[14:17]
	v_mfma_f32_16x16x32_bf16 v[6:9], v[146:149], v[220:223], v[6:9]
	v_mfma_f32_16x16x32_bf16 v[2:5], v[170:173], v[220:223], v[2:5]
	v_mfma_f32_16x16x32_bf16 v[54:57], v[150:153], v[194:197], v[54:57]
	v_mfma_f32_16x16x32_bf16 v[46:49], v[180:183], v[194:197], v[46:49]
	v_mfma_f32_16x16x32_bf16 v[38:41], v[150:153], v[202:205], v[38:41]
	v_mfma_f32_16x16x32_bf16 v[30:33], v[180:183], v[202:205], v[30:33]
	v_mfma_f32_16x16x32_bf16 v[22:25], v[150:153], v[216:219], v[22:25]
	v_mfma_f32_16x16x32_bf16 v[14:17], v[180:183], v[216:219], v[14:17]
	v_mfma_f32_16x16x32_bf16 v[6:9], v[150:153], v[224:227], v[6:9]
	v_mfma_f32_16x16x32_bf16 v[2:5], v[180:183], v[224:227], v[2:5]
	s_setprio 0
	s_barrier
; #define PG8_STAGE(bufoff, gbase, voff) do { _Pragma("unroll") for (int _i = 0; _i < 2; ++_i) \
;         __builtin_amdgcn_global_load_lds((const unsigned*)((const char*)(gbase) + (voff)[_i]), (PG8_LAS unsigned*)(lds + (bufoff) + ldsw + _i * 8192), 16, 0, 0); } while (0)
; #define PG8_LDA(dst, b, h) do { _Pragma("unroll") for (int m = 0; m < 4; ++m) _Pragma("unroll") for (int k = 0; k < 2; ++k) dst[m][k] = *(const PG8_LAS bf16x8*)(lds + PG8_SA(b, h) + aoff + m * 2048 + k * 1024); } while (0)
; #define PG8_LDB(dst, b, h) do { _Pragma("unroll") for (int n = 0; n < 2; ++n) _Pragma("unroll") for (int k = 0; k < 2; ++k) dst[n][k] = *(const PG8_LAS bf16x8*)(lds + PG8_SB(b, h) + boff + n * 2048 + k * 1024); } while (0)
; #define PG8_WAIT_V(n) asm volatile("s_waitcnt vmcnt(" #n ")" ::: "memory")
; #define PG8_WAIT_L(n) asm volatile("s_waitcnt lgkmcnt(" #n ")" ::: "memory")
; #define PG8_BAR __builtin_amdgcn_s_barrier()
; #define PG8_SCHED __builtin_amdgcn_sched_barrier(0)
; template <class Epi, class Sched, bool ALIGN_EPI = false, bool SP2 = false>
; __device__ __forceinline__ void gemm_phase(PG8_LAS unsigned char* lds, const Gemm g, const Sched& S, const Epi& E) {
;     ...
;             PG8_LDB(B0, 1, 0); PG8_LDB(B1, 1, 1); PG8_SCHED; PG8_LDA(At, 1, 0); PG8_STAGE(PG8_SA(0, 1), a2 + hstep, voffA);
;             PG8_WAIT_V(8); PG8_WAIT_L(0); PG8_BAR; PG8_MMA(0, 0, At, B0); PG8_MMA(0, 1, At, B1); PG8_BAR; PG8_SCHED;
;             PG8_LDA(At, 1, 1); PG8_STAGE(PG8_SB(1, 0), b3, voffB); PG8_STAGE(PG8_SB(1, 1), b3 + hstep, voffB); PG8_STAGE(PG8_SA(1, 0), a3, voffA);
;             PG8_WAIT_V(8); PG8_WAIT_L(0); PG8_BAR; PG8_MMA(1, 0, At, B0); PG8_MMA(1, 1, At, B1); PG8_BAR; PG8_SCHED;
	s_add_i32 s51, 0, 0x18000
	s_add_i32 s52, 0, 0x1c000
	ds_read_b128 v[130:133], v248
	ds_read_b128 v[134:137], v248 offset:1024
	ds_read_b128 v[138:141], v248 offset:2048
	ds_read_b128 v[142:145], v248 offset:3072
	ds_read_b128 v[146:149], v249
	ds_read_b128 v[150:153], v249 offset:1024
	ds_read_b128 v[170:173], v249 offset:2048
	ds_read_b128 v[180:183], v249 offset:3072
	s_add_u32 s18, s18, 0x160000
	s_addc_u32 s19, s19, 0
	s_mov_b32 m0, s26
	ds_read_b128 v[190:193], v179 offset:32768
	ds_read_b128 v[194:197], v179 offset:33792
	ds_read_b128 v[198:201], v179 offset:34816
	ds_read_b128 v[202:205], v179 offset:35840
	ds_read_b128 v[206:209], v179 offset:36864
	ds_read_b128 v[216:219], v179 offset:37888
	ds_read_b128 v[220:223], v179 offset:38912
	ds_read_b128 v[224:227], v179 offset:39936
	global_load_lds_dwordx4 v154, s[18:19]
	s_mov_b32 m0, s27
	s_nop 0
	global_load_lds_dwordx4 v158, s[18:19]
	s_waitcnt vmcnt(8)
	s_waitcnt lgkmcnt(0)
	s_barrier
	s_setprio 1
	s_waitcnt lgkmcnt(0)
	v_mfma_f32_16x16x32_bf16 v[126:129], v[130:133], v[190:193], v[126:129]
	v_mfma_f32_16x16x32_bf16 v[122:125], v[138:141], v[190:193], v[122:125]
	v_mfma_f32_16x16x32_bf16 v[110:113], v[130:133], v[198:201], v[110:113]
	v_mfma_f32_16x16x32_bf16 v[106:109], v[138:141], v[198:201], v[106:109]
	v_mfma_f32_16x16x32_bf16 v[98:101], v[130:133], v[206:209], v[98:101]
	v_mfma_f32_16x16x32_bf16 v[90:93], v[138:141], v[206:209], v[90:93]
	v_mfma_f32_16x16x32_bf16 v[82:85], v[130:133], v[220:223], v[82:85]
	v_mfma_f32_16x16x32_bf16 v[74:77], v[138:141], v[220:223], v[74:77]
	v_mfma_f32_16x16x32_bf16 v[126:129], v[134:137], v[194:197], v[126:129]
	v_mfma_f32_16x16x32_bf16 v[122:125], v[142:145], v[194:197], v[122:125]
	v_mfma_f32_16x16x32_bf16 v[110:113], v[134:137], v[202:205], v[110:113]
	v_mfma_f32_16x16x32_bf16 v[106:109], v[142:145], v[202:205], v[106:109]
	v_mfma_f32_16x16x32_bf16 v[98:101], v[134:137], v[216:219], v[98:101]
	v_mfma_f32_16x16x32_bf16 v[90:93], v[142:145], v[216:219], v[90:93]
	v_mfma_f32_16x16x32_bf16 v[82:85], v[134:137], v[224:227], v[82:85]
	v_mfma_f32_16x16x32_bf16 v[74:77], v[142:145], v[224:227], v[74:77]
	s_setprio 0
	s_setprio 1
	v_mfma_f32_16x16x32_bf16 v[118:121], v[146:149], v[190:193], v[118:121]
	v_mfma_f32_16x16x32_bf16 v[114:117], v[170:173], v[190:193], v[114:117]
	v_mfma_f32_16x16x32_bf16 v[102:105], v[146:149], v[198:201], v[102:105]
	v_mfma_f32_16x16x32_bf16 v[94:97], v[170:173], v[198:201], v[94:97]
	v_mfma_f32_16x16x32_bf16 v[86:89], v[146:149], v[206:209], v[86:89]
	v_mfma_f32_16x16x32_bf16 v[78:81], v[170:173], v[206:209], v[78:81]
	v_mfma_f32_16x16x32_bf16 v[70:73], v[146:149], v[220:223], v[70:73]
	v_mfma_f32_16x16x32_bf16 v[66:69], v[170:173], v[220:223], v[66:69]
	v_mfma_f32_16x16x32_bf16 v[118:121], v[150:153], v[194:197], v[118:121]
	v_mfma_f32_16x16x32_bf16 v[114:117], v[180:183], v[194:197], v[114:117]
	v_mfma_f32_16x16x32_bf16 v[102:105], v[150:153], v[202:205], v[102:105]
	v_mfma_f32_16x16x32_bf16 v[94:97], v[180:183], v[202:205], v[94:97]
	v_mfma_f32_16x16x32_bf16 v[86:89], v[150:153], v[216:219], v[86:89]
	v_mfma_f32_16x16x32_bf16 v[78:81], v[180:183], v[216:219], v[78:81]
	v_mfma_f32_16x16x32_bf16 v[70:73], v[150:153], v[224:227], v[70:73]
	v_mfma_f32_16x16x32_bf16 v[66:69], v[180:183], v[224:227], v[66:69]
	s_setprio 0
	s_barrier
	s_add_u32 s98, s16, 0x80
	s_addc_u32 s99, s17, 0
	s_add_u32 s100, s18, 0xffea0080
	s_addc_u32 s101, s19, -1
	s_add_i32 s18, s51, s23
	s_mov_b32 m0, s18
	ds_read_b128 v[190:193], v179 offset:49152
	ds_read_b128 v[194:197], v179 offset:50176
	ds_read_b128 v[198:201], v179 offset:51200
	ds_read_b128 v[202:205], v179 offset:52224
	ds_read_b128 v[206:209], v179 offset:53248
	ds_read_b128 v[216:219], v179 offset:54272
	ds_read_b128 v[220:223], v179 offset:55296
	ds_read_b128 v[224:227], v179 offset:56320
	global_load_lds_dwordx4 v156, s[98:99]
	s_add_i32 m0, s18, 0x2000
	s_add_u32 s16, s16, 0x160080
	s_addc_u32 s17, s17, 0
	s_add_i32 s18, s52, s23
	global_load_lds_dwordx4 v160, s[98:99]
	s_mov_b32 m0, s18
	s_nop 0
	global_load_lds_dwordx4 v156, s[16:17]
	s_add_i32 m0, s18, 0x2000
	s_nop 0
	global_load_lds_dwordx4 v160, s[16:17]
	s_mov_b32 m0, s33
	s_nop 0
	global_load_lds_dwordx4 v154, s[100:101]
	s_mov_b32 m0, s34
	s_nop 0
	global_load_lds_dwordx4 v158, s[100:101]
	s_waitcnt vmcnt(8)
	s_waitcnt lgkmcnt(0)
	s_barrier
	s_setprio 1
	s_waitcnt lgkmcnt(0)
	v_mfma_f32_16x16x32_bf16 v[62:65], v[130:133], v[190:193], v[62:65]
	v_mfma_f32_16x16x32_bf16 v[58:61], v[138:141], v[190:193], v[58:61]
	v_mfma_f32_16x16x32_bf16 v[50:53], v[130:133], v[198:201], v[50:53]
	v_mfma_f32_16x16x32_bf16 v[42:45], v[138:141], v[198:201], v[42:45]
	v_mfma_f32_16x16x32_bf16 v[34:37], v[130:133], v[206:209], v[34:37]
	v_mfma_f32_16x16x32_bf16 v[26:29], v[138:141], v[206:209], v[26:29]
	v_mfma_f32_16x16x32_bf16 v[18:21], v[130:133], v[220:223], v[18:21]
	v_mfma_f32_16x16x32_bf16 v[10:13], v[138:141], v[220:223], v[10:13]
	v_mfma_f32_16x16x32_bf16 v[62:65], v[134:137], v[194:197], v[62:65]
	v_mfma_f32_16x16x32_bf16 v[58:61], v[142:145], v[194:197], v[58:61]
	v_mfma_f32_16x16x32_bf16 v[50:53], v[134:137], v[202:205], v[50:53]
	v_mfma_f32_16x16x32_bf16 v[42:45], v[142:145], v[202:205], v[42:45]
	v_mfma_f32_16x16x32_bf16 v[34:37], v[134:137], v[216:219], v[34:37]
	v_mfma_f32_16x16x32_bf16 v[26:29], v[142:145], v[216:219], v[26:29]
	v_mfma_f32_16x16x32_bf16 v[18:21], v[134:137], v[224:227], v[18:21]
	v_mfma_f32_16x16x32_bf16 v[10:13], v[142:145], v[224:227], v[10:13]
	s_setprio 0
	s_setprio 1
	v_mfma_f32_16x16x32_bf16 v[54:57], v[146:149], v[190:193], v[54:57]
	v_mfma_f32_16x16x32_bf16 v[46:49], v[170:173], v[190:193], v[46:49]
	v_mfma_f32_16x16x32_bf16 v[38:41], v[146:149], v[198:201], v[38:41]
	v_mfma_f32_16x16x32_bf16 v[30:33], v[170:173], v[198:201], v[30:33]
	v_mfma_f32_16x16x32_bf16 v[22:25], v[146:149], v[206:209], v[22:25]
	v_mfma_f32_16x16x32_bf16 v[14:17], v[170:173], v[206:209], v[14:17]
	v_mfma_f32_16x16x32_bf16 v[6:9], v[146:149], v[220:223], v[6:9]
	v_mfma_f32_16x16x32_bf16 v[2:5], v[170:173], v[220:223], v[2:5]
	v_mfma_f32_16x16x32_bf16 v[54:57], v[150:153], v[194:197], v[54:57]
	v_mfma_f32_16x16x32_bf16 v[46:49], v[180:183], v[194:197], v[46:49]
	v_mfma_f32_16x16x32_bf16 v[38:41], v[150:153], v[202:205], v[38:41]
	v_mfma_f32_16x16x32_bf16 v[30:33], v[180:183], v[202:205], v[30:33]
	v_mfma_f32_16x16x32_bf16 v[22:25], v[150:153], v[216:219], v[22:25]
	v_mfma_f32_16x16x32_bf16 v[14:17], v[180:183], v[216:219], v[14:17]
	v_mfma_f32_16x16x32_bf16 v[6:9], v[150:153], v[224:227], v[6:9]
	v_mfma_f32_16x16x32_bf16 v[2:5], v[180:183], v[224:227], v[2:5]
	s_setprio 0
	s_barrier
;     __device__ __forceinline__ void operator()(const f32x4 (&acc)[2][2][4][2], const Unit& u, int wr, int wc, int fr, int fq) const {
;         const int row0 = u.pm * BM + wr * 64 + fr, col0 = u.pn * BM + wc * 32 + 8 * fq;
;         const float* __restrict__ gp = gate + (size_t)(u.pm >> 3) * 12288 + col0;
;         bf16_t* __restrict__ op = out + (size_t)row0 * 2048 + col0;
;         f32x4 gv[2][2];
; #pragma unroll
;         for (int bj = 0; bj < 2; ++bj)
; #pragma unroll
;             for (int n = 0; n < 2; ++n) gv[bj][n] = *(const f32x4*)(gp + bj * HALF + n * 4);
; #pragma unroll
;         for (int ai = 0; ai < 2; ++ai) {
;             if constexpr (BASE_F32) {
;                 const float* __restrict__ bp = (const float*)base + (size_t)row0 * 2048 + col0;
;                 f32x4 bs[4][2][2];
; #pragma unroll
;                 for (int m = 0; m < 4; ++m)
; #pragma unroll
;                     for (int bj = 0; bj < 2; ++bj)
; #pragma unroll
;                         for (int n = 0; n < 2; ++n) bs[m][bj][n] = *(const f32x4*)(bp + (size_t)(ai * HALF + m * 16) * 2048 + bj * HALF + n * 4);
; #pragma unroll
;                 for (int m = 0; m < 4; ++m)
; #pragma unroll
;                     for (int bj = 0; bj < 2; ++bj) { const f32x4 v0 = bs[m][bj][0] + gv[bj][0] * acc[ai][bj][m][0], v1 = bs[m][bj][1] + gv[bj][1] * acc[ai][bj][m][1];
;                         u32x4 w; w.x = cvt_pk_bf16(v0[0], v0[1]); w.y = cvt_pk_bf16(v0[2], v0[3]); w.z = cvt_pk_bf16(v1[0], v1[1]); w.w = cvt_pk_bf16(v1[2], v1[3]);
;                         *(u32x4*)(op + (size_t)(ai * HALF + m * 16) * 2048 + bj * HALF) = w; }
;             } else {
;                 const bf16_t* __restrict__ bp = (const bf16_t*)base + (size_t)row0 * 2048 + col0;
;                 u32x4 bs[4][2];
; #pragma unroll
;                 for (int m = 0; m < 4; ++m)
; #pragma unroll
;                     for (int bj = 0; bj < 2; ++bj) bs[m][bj] = *(const u32x4*)(bp + (size_t)(ai * HALF + m * 16) * 2048 + bj * HALF);
; #pragma unroll
;                 for (int m = 0; m < 4; ++m)
; #pragma unroll
;                     for (int bj = 0; bj < 2; ++bj) { const u32x4 b = bs[m][bj]; const f32x4 a0 = acc[ai][bj][m][0], a1 = acc[ai][bj][m][1], g0 = gv[bj][0], g1 = gv[bj][1];
;                         u32x4 w;
	s_add_i32 s50, s50, 2
	s_add_u32 s14, s14, 0x100
	s_addc_u32 s15, s15, 0
	s_add_u32 s48, s48, 0x100
	s_addc_u32 s49, s49, 0
	s_cmpk_gt_u32 s50, 0x55
	s_cbranch_scc0 .LBB0_951
	v_lshl_add_u32 v130, s46, 8, v174
	v_lshl_or_b32 v132, s47, 8, v176
	v_ashrrev_i32_e32 v131, 31, v130
	v_ashrrev_i32_e32 v133, 31, v132
	v_lshlrev_b64 v[146:147], 12, v[130:131]
	s_ashr_i32 s14, s46, 3
	v_lshlrev_b64 v[148:149], 1, v[132:133]
	v_lshl_add_u64 v[130:131], s[66:67], 0, v[146:147]
	s_mul_hi_i32 s15, s14, 0xc000
	s_mul_i32 s14, s14, 0xc000
	v_lshl_add_u64 v[172:173], v[130:131], 0, v[148:149]
	s_add_u32 s14, s30, s14
	s_addc_u32 s15, s31, s15
	v_add_co_u32_e32 v150, vcc, s29, v172
	global_load_dwordx4 v[180:183], v[172:173], off
	global_load_dwordx4 v[190:193], v[172:173], off offset:256
	v_lshl_add_u64 v[130:131], v[132:133], 2, s[14:15]
	v_addc_co_u32_e32 v151, vcc, 0, v173, vcc
	global_load_dwordx4 v[142:145], v[130:131], off
	global_load_dwordx4 v[138:141], v[130:131], off offset:16
	global_load_dwordx4 v[134:137], v[130:131], off offset:512
	s_nop 0
	global_load_dwordx4 v[130:133], v[130:131], off offset:528
	v_readlane_b32 s14, v247, 30
	global_load_dwordx4 v[194:197], v[150:151], off
	global_load_dwordx4 v[198:201], v[150:151], off offset:256
	v_readlane_b32 s15, v247, 31
	s_and_b64 vcc, exec, s[10:11]
	s_cbranch_vccz .LBB0_954
	s_barrier
.LBB0_954:
	s_waitcnt vmcnt(0)
	v_lshlrev_b32_e32 v184, 16, v180
	v_lshl_add_u64 v[146:147], s[14:15], 0, v[146:147]
	v_lshl_add_u64 v[170:171], v[146:147], 0, v[148:149]
	v_add_co_u32_e32 v146, vcc, s38, v172
	v_lshlrev_b32_e32 v218, 16, v191
	s_nop 0
	v_addc_co_u32_e32 v147, vcc, 0, v173, vcc
	v_add_co_u32_e32 v148, vcc, s39, v172
	v_fmac_f32_e32 v218, v120, v136
	s_nop 0
	v_addc_co_u32_e32 v149, vcc, 0, v173, vcc
	global_load_dwordx4 v[202:205], v[146:147], off
	global_load_dwordx4 v[206:209], v[146:147], off offset:256
	global_load_dwordx4 v[150:153], v[148:149], off
	s_nop 0
	global_load_dwordx4 v[146:149], v[148:149], off offset:256
	v_lshlrev_b32_e32 v120, 16, v195
	v_fmac_f32_e32 v120, v112, v144
	v_lshlrev_b32_e32 v112, 16, v196
	v_and_b32_e32 v180, 0xffff0000, v180
	v_lshlrev_b32_e32 v185, 16, v181
	v_and_b32_e32 v181, 0xffff0000, v181
	v_lshlrev_b32_e32 v189, 16, v182
	v_and_b32_e32 v182, 0xffff0000, v182
	v_lshlrev_b32_e32 v216, 16, v183
	v_and_b32_e32 v183, 0xffff0000, v183
	v_lshlrev_b32_e32 v217, 16, v190
	v_and_b32_e32 v190, 0xffff0000, v190
	v_and_b32_e32 v191, 0xffff0000, v191
	v_lshlrev_b32_e32 v219, 16, v192
	v_and_b32_e32 v192, 0xffff0000, v192
	v_lshlrev_b32_e32 v220, 16, v193
	v_and_b32_e32 v193, 0xffff0000, v193
	v_fmac_f32_e32 v112, v106, v138
	v_and_b32_e32 v106, 0xffff0000, v196
	v_fmac_f32_e32 v184, v126, v142
	v_fmac_f32_e32 v180, v127, v143
	v_fmac_f32_e32 v185, v128, v144
	v_fmac_f32_e32 v181, v129, v145
	v_fmac_f32_e32 v189, v122, v138
	v_fmac_f32_e32 v182, v123, v139
	v_fmac_f32_e32 v216, v124, v140
	v_fmac_f32_e32 v183, v125, v141
	v_fmac_f32_e32 v217, v118, v134
	v_fmac_f32_e32 v190, v119, v135
	v_fmac_f32_e32 v191, v121, v137
	v_fmac_f32_e32 v219, v114, v130
	v_fmac_f32_e32 v192, v115, v131
	v_fmac_f32_e32 v220, v116, v132
	v_fmac_f32_e32 v193, v117, v133
	v_lshlrev_b32_e32 v118, 16, v194
	v_and_b32_e32 v119, 0xffff0000, v194
	v_and_b32_e32 v121, 0xffff0000, v195
	v_cvt_pk_bf16_f32 v114, v184, v180
	v_cvt_pk_bf16_f32 v115, v185, v181
	v_cvt_pk_bf16_f32 v116, v189, v182
	v_cvt_pk_bf16_f32 v117, v216, v183
	v_fmac_f32_e32 v106, v107, v139
	v_fmac_f32_e32 v118, v110, v142
	v_fmac_f32_e32 v119, v111, v143
	global_store_dwordx4 v[170:171], v[114:117], off
	v_fmac_f32_e32 v121, v113, v145
	v_and_b32_e32 v107, 0xffff0000, v197
	v_cvt_pk_bf16_f32 v114, v217, v190
	v_cvt_pk_bf16_f32 v115, v218, v191
	v_cvt_pk_bf16_f32 v116, v219, v192
	v_cvt_pk_bf16_f32 v117, v220, v193
	global_store_dwordx4 v[170:171], v[114:117], off offset:256
	v_cvt_pk_bf16_f32 v110, v118, v119
	v_cvt_pk_bf16_f32 v111, v120, v121
	v_cvt_pk_bf16_f32 v112, v112, v106
	v_lshlrev_b32_e32 v106, 16, v197
	v_fmac_f32_e32 v106, v108, v140
	v_lshlrev_b32_e32 v108, 16, v198
	v_fmac_f32_e32 v108, v102, v134
	v_and_b32_e32 v102, 0xffff0000, v198
	v_fmac_f32_e32 v102, v103, v135
	v_lshlrev_b32_e32 v103, 16, v199
	v_fmac_f32_e32 v107, v109, v141
	v_cvt_pk_bf16_f32 v113, v106, v107
	v_add_co_u32_e32 v106, vcc, s29, v170
	v_fmac_f32_e32 v103, v104, v136
	v_and_b32_e32 v104, 0xffff0000, v199
	v_addc_co_u32_e32 v107, vcc, 0, v171, vcc
	v_fmac_f32_e32 v104, v105, v137
	global_store_dwordx4 v[106:107], v[110:113], off
	v_cvt_pk_bf16_f32 v102, v108, v102
	v_cvt_pk_bf16_f32 v103, v103, v104
	v_lshlrev_b32_e32 v104, 16, v200
	v_fmac_f32_e32 v104, v94, v130
	v_and_b32_e32 v94, 0xffff0000, v200
	v_fmac_f32_e32 v94, v95, v131
	v_cvt_pk_bf16_f32 v104, v104, v94
	v_lshlrev_b32_e32 v94, 16, v201
	v_and_b32_e32 v95, 0xffff0000, v201
	v_fmac_f32_e32 v94, v96, v132
	v_fmac_f32_e32 v95, v97, v133
	v_cvt_pk_bf16_f32 v105, v94, v95
	s_waitcnt vmcnt(6)
	v_lshlrev_b32_e32 v94, 16, v202
	v_and_b32_e32 v95, 0xffff0000, v202
	v_fmac_f32_e32 v94, v98, v142
	v_fmac_f32_e32 v95, v99, v143
	global_store_dwordx4 v[106:107], v[102:105], off offset:256
	v_cvt_pk_bf16_f32 v94, v94, v95
	v_lshlrev_b32_e32 v95, 16, v203
	v_and_b32_e32 v96, 0xffff0000, v203
	v_fmac_f32_e32 v95, v100, v144
	v_fmac_f32_e32 v96, v101, v145
	v_cvt_pk_bf16_f32 v95, v95, v96
	v_lshlrev_b32_e32 v96, 16, v204
	v_fmac_f32_e32 v96, v90, v138
	v_and_b32_e32 v90, 0xffff0000, v204
	v_fmac_f32_e32 v90, v91, v139
	v_cvt_pk_bf16_f32 v96, v96, v90
	v_lshlrev_b32_e32 v90, 16, v205
	v_fmac_f32_e32 v90, v92, v140
	s_waitcnt vmcnt(6)
; __device__ __forceinline__ unsigned cvt_pk_bf16(float lo, float hi) { unsigned r; asm volatile("v_cvt_pk_bf16_f32 %0, %1, %2" : "=v"(r) : "v"(lo), "v"(hi)); return r; }
;     __device__ __forceinline__ void operator()(const f32x4 (&acc)[2][2][4][2], const Unit& u, int wr, int wc, int fr, int fq) const {
;     ...
;                 for (int m = 0; m < 4; ++m)
; #pragma unroll
;                     for (int bj = 0; bj < 2; ++bj) { const u32x4 b = bs[m][bj]; const f32x4 a0 = acc[ai][bj][m][0], a1 = acc[ai][bj][m][1], g0 = gv[bj][0], g1 = gv[bj][1];
;                         u32x4 w;
;                         w.x = cvt_pk_bf16(__builtin_bit_cast(float, b.x << 16) + g0[0] * a0[0], __builtin_bit_cast(float, b.x & 0xffff0000u) + g0[1] * a0[1]);
;                         w.y = cvt_pk_bf16(__builtin_bit_cast(float, b.y << 16) + g0[2] * a0[2], __builtin_bit_cast(float, b.y & 0xffff0000u) + g0[3] * a0[3]);
;                         w.z = cvt_pk_bf16(__builtin_bit_cast(float, b.z << 16) + g1[0] * a1[0], __builtin_bit_cast(float, b.z & 0xffff0000u) + g1[1] * a1[1]);
;                         w.w = cvt_pk_bf16(__builtin_bit_cast(float, b.w << 16) + g1[2] * a1[2], __builtin_bit_cast(float, b.w & 0xffff0000u) + g1[3] * a1[3]);
;                         *(u32x4*)(op + (size_t)(ai * HALF + m * 16) * 2048 + bj * HALF) = w; }
	v_lshlrev_b32_e32 v92, 16, v206
	v_fmac_f32_e32 v92, v86, v134
	v_and_b32_e32 v86, 0xffff0000, v206
	v_and_b32_e32 v91, 0xffff0000, v205
	v_fmac_f32_e32 v86, v87, v135
	v_lshlrev_b32_e32 v87, 16, v207
	v_fmac_f32_e32 v91, v93, v141
	v_cvt_pk_bf16_f32 v97, v90, v91
	v_add_co_u32_e32 v90, vcc, s38, v170
	v_fmac_f32_e32 v87, v88, v136
	v_and_b32_e32 v88, 0xffff0000, v207
	v_addc_co_u32_e32 v91, vcc, 0, v171, vcc
	v_fmac_f32_e32 v88, v89, v137
	global_store_dwordx4 v[90:91], v[94:97], off
	v_cvt_pk_bf16_f32 v86, v92, v86
	v_cvt_pk_bf16_f32 v87, v87, v88
	v_lshlrev_b32_e32 v88, 16, v208
	v_fmac_f32_e32 v88, v78, v130
	v_and_b32_e32 v78, 0xffff0000, v208
	v_fmac_f32_e32 v78, v79, v131
	v_cvt_pk_bf16_f32 v88, v88, v78
	v_lshlrev_b32_e32 v78, 16, v209
	v_and_b32_e32 v79, 0xffff0000, v209
	v_fmac_f32_e32 v78, v80, v132
	v_fmac_f32_e32 v79, v81, v133
	v_cvt_pk_bf16_f32 v89, v78, v79
	s_waitcnt vmcnt(6)
	v_lshlrev_b32_e32 v78, 16, v150
	v_and_b32_e32 v79, 0xffff0000, v150
	v_fmac_f32_e32 v78, v82, v142
	v_fmac_f32_e32 v79, v83, v143
	global_store_dwordx4 v[90:91], v[86:89], off offset:256
	v_cvt_pk_bf16_f32 v78, v78, v79
	v_lshlrev_b32_e32 v79, 16, v151
	v_and_b32_e32 v80, 0xffff0000, v151
	v_fmac_f32_e32 v79, v84, v144
	v_fmac_f32_e32 v80, v85, v145
	v_cvt_pk_bf16_f32 v79, v79, v80
	v_lshlrev_b32_e32 v80, 16, v152
	v_fmac_f32_e32 v80, v74, v138
	v_and_b32_e32 v74, 0xffff0000, v152
	v_fmac_f32_e32 v74, v75, v139
	v_cvt_pk_bf16_f32 v80, v80, v74
	v_lshlrev_b32_e32 v74, 16, v153
	v_fmac_f32_e32 v74, v76, v140
	s_waitcnt vmcnt(6)
	v_lshlrev_b32_e32 v76, 16, v146
	v_fmac_f32_e32 v76, v70, v134
	v_and_b32_e32 v70, 0xffff0000, v146
	v_and_b32_e32 v75, 0xffff0000, v153
	v_fmac_f32_e32 v70, v71, v135
	v_lshlrev_b32_e32 v71, 16, v147
	v_fmac_f32_e32 v75, v77, v141
	v_cvt_pk_bf16_f32 v81, v74, v75
	v_add_co_u32_e32 v74, vcc, s39, v170
	v_fmac_f32_e32 v71, v72, v136
	v_and_b32_e32 v72, 0xffff0000, v147
	v_addc_co_u32_e32 v75, vcc, 0, v171, vcc
	v_fmac_f32_e32 v72, v73, v137
	global_store_dwordx4 v[74:75], v[78:81], off
	v_cvt_pk_bf16_f32 v70, v76, v70
	v_cvt_pk_bf16_f32 v71, v71, v72
	v_lshlrev_b32_e32 v72, 16, v148
	v_fmac_f32_e32 v72, v66, v130
	v_and_b32_e32 v66, 0xffff0000, v148
	v_fmac_f32_e32 v66, v67, v131
	v_cvt_pk_bf16_f32 v72, v72, v66
	v_lshlrev_b32_e32 v66, 16, v149
	v_fmac_f32_e32 v66, v68, v132
	v_and_b32_e32 v67, 0xffff0000, v149
	v_fmac_f32_e32 v67, v69, v133
	v_cvt_pk_bf16_f32 v73, v66, v67
	global_store_dwordx4 v[74:75], v[70:73], off offset:256
	v_add_co_u32_e32 v66, vcc, s40, v172
	s_nop 1
	v_addc_co_u32_e32 v67, vcc, 0, v173, vcc
	global_load_dwordx4 v[70:73], v[66:67], off
	global_load_dwordx4 v[74:77], v[66:67], off offset:256
	v_add_co_u32_e32 v66, vcc, s41, v172
	s_waitcnt vmcnt(1)
	v_lshlrev_b32_e32 v98, 16, v70
	v_addc_co_u32_e32 v67, vcc, 0, v173, vcc
	global_load_dwordx4 v[78:81], v[66:67], off
	global_load_dwordx4 v[82:85], v[66:67], off offset:256
	v_add_co_u32_e32 v66, vcc, s42, v172
	v_fmac_f32_e32 v98, v62, v142
	s_nop 0
	v_addc_co_u32_e32 v67, vcc, 0, v173, vcc
	global_load_dwordx4 v[86:89], v[66:67], off
	global_load_dwordx4 v[90:93], v[66:67], off offset:256
	v_add_co_u32_e32 v66, vcc, s43, v172
	v_and_b32_e32 v62, 0xffff0000, v70
	s_nop 0
	v_addc_co_u32_e32 v67, vcc, 0, v173, vcc
	global_load_dwordx4 v[94:97], v[66:67], off
	s_nop 0
	global_load_dwordx4 v[66:69], v[66:67], off offset:256
	v_fmac_f32_e32 v62, v63, v143
	v_lshlrev_b32_e32 v63, 16, v71
	v_fmac_f32_e32 v63, v64, v144
	v_and_b32_e32 v64, 0xffff0000, v71
	v_fmac_f32_e32 v64, v65, v145
	v_cvt_pk_bf16_f32 v62, v98, v62
	v_cvt_pk_bf16_f32 v63, v63, v64
	v_lshlrev_b32_e32 v64, 16, v72
	v_fmac_f32_e32 v64, v58, v138
	v_and_b32_e32 v58, 0xffff0000, v72
	v_fmac_f32_e32 v58, v59, v139
	v_cvt_pk_bf16_f32 v64, v64, v58
	v_lshlrev_b32_e32 v58, 16, v73
	v_fmac_f32_e32 v58, v60, v140
	s_waitcnt vmcnt(6)
	v_lshlrev_b32_e32 v60, 16, v74
	v_fmac_f32_e32 v60, v54, v134
	v_and_b32_e32 v54, 0xffff0000, v74
	v_and_b32_e32 v59, 0xffff0000, v73
	v_fmac_f32_e32 v54, v55, v135
	v_lshlrev_b32_e32 v55, 16, v75
	v_fmac_f32_e32 v59, v61, v141
	v_cvt_pk_bf16_f32 v65, v58, v59
	v_add_co_u32_e32 v58, vcc, s40, v170
	v_fmac_f32_e32 v55, v56, v136
	v_and_b32_e32 v56, 0xffff0000, v75
	v_addc_co_u32_e32 v59, vcc, 0, v171, vcc
	v_fmac_f32_e32 v56, v57, v137
	global_store_dwordx4 v[58:59], v[62:65], off
	v_cvt_pk_bf16_f32 v54, v60, v54
	v_cvt_pk_bf16_f32 v55, v55, v56
	v_lshlrev_b32_e32 v56, 16, v76
	v_fmac_f32_e32 v56, v46, v130
	v_and_b32_e32 v46, 0xffff0000, v76
	v_fmac_f32_e32 v46, v47, v131
	v_cvt_pk_bf16_f32 v56, v56, v46
	v_lshlrev_b32_e32 v46, 16, v77
	v_and_b32_e32 v47, 0xffff0000, v77
	v_fmac_f32_e32 v46, v48, v132
	v_fmac_f32_e32 v47, v49, v133
	v_cvt_pk_bf16_f32 v57, v46, v47
	global_store_dwordx4 v[58:59], v[54:57], off offset:256
	s_waitcnt vmcnt(7)
; __device__ __forceinline__ unsigned cvt_pk_bf16(float lo, float hi) { unsigned r; asm volatile("v_cvt_pk_bf16_f32 %0, %1, %2" : "=v"(r) : "v"(lo), "v"(hi)); return r; }
; #define PG8_BAR __builtin_amdgcn_s_barrier()
;     __device__ __forceinline__ void operator()(const f32x4 (&acc)[2][2][4][2], const Unit& u, int wr, int wc, int fr, int fq) const {
;     ...
;                 for (int m = 0; m < 4; ++m)
; #pragma unroll
;                     for (int bj = 0; bj < 2; ++bj) { const u32x4 b = bs[m][bj]; const f32x4 a0 = acc[ai][bj][m][0], a1 = acc[ai][bj][m][1], g0 = gv[bj][0], g1 = gv[bj][1];
;                         u32x4 w;
;                         w.x = cvt_pk_bf16(__builtin_bit_cast(float, b.x << 16) + g0[0] * a0[0], __builtin_bit_cast(float, b.x & 0xffff0000u) + g0[1] * a0[1]);
;                         w.y = cvt_pk_bf16(__builtin_bit_cast(float, b.y << 16) + g0[2] * a0[2], __builtin_bit_cast(float, b.y & 0xffff0000u) + g0[3] * a0[3]);
;                         w.z = cvt_pk_bf16(__builtin_bit_cast(float, b.z << 16) + g1[0] * a1[0], __builtin_bit_cast(float, b.z & 0xffff0000u) + g1[1] * a1[1]);
;                         w.w = cvt_pk_bf16(__builtin_bit_cast(float, b.w << 16) + g1[2] * a1[2], __builtin_bit_cast(float, b.w & 0xffff0000u) + g1[3] * a1[3]);
;                         *(u32x4*)(op + (size_t)(ai * HALF + m * 16) * 2048 + bj * HALF) = w; }
; template <class Epi, class Sched, bool ALIGN_EPI = false, bool SP2 = false>
; __device__ __forceinline__ void gemm_phase(PG8_LAS unsigned char* lds, const Gemm g, const Sched& S, const Epi& E) {
;     ...
;         if (!has_next) break;
; #pragma unroll
;         for (int a = 0; a < 2; ++a)
; #pragma unroll
;             for (int b = 0; b < 2; ++b)
; #pragma unroll
;                 for (int m = 0; m < 4; ++m)
; #pragma unroll
;                     for (int n = 0; n < 2; ++n) acc[a][b][m][n] = (f32x4){0.f, 0.f, 0.f, 0.f};
;         cur = nxt; cA = nA; cB = nB; ++ui;
;         if constexpr (ALIGN_EPI) { if (wr == 1) PG8_BAR; }
	v_lshlrev_b32_e32 v46, 16, v78
	v_and_b32_e32 v47, 0xffff0000, v78
	v_fmac_f32_e32 v46, v50, v142
	v_fmac_f32_e32 v47, v51, v143
	v_cvt_pk_bf16_f32 v46, v46, v47
	v_lshlrev_b32_e32 v47, 16, v79
	v_and_b32_e32 v48, 0xffff0000, v79
	v_fmac_f32_e32 v47, v52, v144
	v_fmac_f32_e32 v48, v53, v145
	v_cvt_pk_bf16_f32 v47, v47, v48
	v_lshlrev_b32_e32 v48, 16, v80
	v_fmac_f32_e32 v48, v42, v138
	v_and_b32_e32 v42, 0xffff0000, v80
	v_fmac_f32_e32 v42, v43, v139
	v_cvt_pk_bf16_f32 v48, v48, v42
	v_lshlrev_b32_e32 v42, 16, v81
	v_fmac_f32_e32 v42, v44, v140
	s_waitcnt vmcnt(6)
	v_lshlrev_b32_e32 v44, 16, v82
	v_fmac_f32_e32 v44, v38, v134
	v_and_b32_e32 v38, 0xffff0000, v82
	v_and_b32_e32 v43, 0xffff0000, v81
	v_fmac_f32_e32 v38, v39, v135
	v_lshlrev_b32_e32 v39, 16, v83
	v_fmac_f32_e32 v43, v45, v141
	v_cvt_pk_bf16_f32 v49, v42, v43
	v_add_co_u32_e32 v42, vcc, s41, v170
	v_fmac_f32_e32 v39, v40, v136
	v_and_b32_e32 v40, 0xffff0000, v83
	v_addc_co_u32_e32 v43, vcc, 0, v171, vcc
	v_fmac_f32_e32 v40, v41, v137
	global_store_dwordx4 v[42:43], v[46:49], off
	v_cvt_pk_bf16_f32 v38, v44, v38
	v_cvt_pk_bf16_f32 v39, v39, v40
	v_lshlrev_b32_e32 v40, 16, v84
	v_fmac_f32_e32 v40, v30, v130
	v_and_b32_e32 v30, 0xffff0000, v84
	v_fmac_f32_e32 v30, v31, v131
	v_cvt_pk_bf16_f32 v40, v40, v30
	v_lshlrev_b32_e32 v30, 16, v85
	v_and_b32_e32 v31, 0xffff0000, v85
	v_fmac_f32_e32 v30, v32, v132
	v_fmac_f32_e32 v31, v33, v133
	v_cvt_pk_bf16_f32 v41, v30, v31
	s_waitcnt vmcnt(6)
	v_lshlrev_b32_e32 v30, 16, v86
	v_and_b32_e32 v31, 0xffff0000, v86
	v_fmac_f32_e32 v30, v34, v142
	v_fmac_f32_e32 v31, v35, v143
	global_store_dwordx4 v[42:43], v[38:41], off offset:256
	v_cvt_pk_bf16_f32 v30, v30, v31
	v_lshlrev_b32_e32 v31, 16, v87
	v_and_b32_e32 v32, 0xffff0000, v87
	v_fmac_f32_e32 v31, v36, v144
	v_fmac_f32_e32 v32, v37, v145
	v_cvt_pk_bf16_f32 v31, v31, v32
	v_lshlrev_b32_e32 v32, 16, v88
	v_fmac_f32_e32 v32, v26, v138
	v_and_b32_e32 v26, 0xffff0000, v88
	v_fmac_f32_e32 v26, v27, v139
	v_cvt_pk_bf16_f32 v32, v32, v26
	v_lshlrev_b32_e32 v26, 16, v89
	v_fmac_f32_e32 v26, v28, v140
	s_waitcnt vmcnt(6)
	v_lshlrev_b32_e32 v28, 16, v90
	v_fmac_f32_e32 v28, v22, v134
	v_and_b32_e32 v22, 0xffff0000, v90
	v_and_b32_e32 v27, 0xffff0000, v89
	v_fmac_f32_e32 v22, v23, v135
	v_lshlrev_b32_e32 v23, 16, v91
	v_fmac_f32_e32 v27, v29, v141
	v_cvt_pk_bf16_f32 v33, v26, v27
	v_add_co_u32_e32 v26, vcc, s42, v170
	v_fmac_f32_e32 v23, v24, v136
	v_and_b32_e32 v24, 0xffff0000, v91
	v_addc_co_u32_e32 v27, vcc, 0, v171, vcc
	v_fmac_f32_e32 v24, v25, v137
	global_store_dwordx4 v[26:27], v[30:33], off
	v_cvt_pk_bf16_f32 v22, v28, v22
	v_cvt_pk_bf16_f32 v23, v23, v24
	v_lshlrev_b32_e32 v24, 16, v92
	v_fmac_f32_e32 v24, v14, v130
	v_and_b32_e32 v14, 0xffff0000, v92
	v_fmac_f32_e32 v14, v15, v131
	v_cvt_pk_bf16_f32 v24, v24, v14
	v_lshlrev_b32_e32 v14, 16, v93
	v_and_b32_e32 v15, 0xffff0000, v93
	v_fmac_f32_e32 v14, v16, v132
	v_fmac_f32_e32 v15, v17, v133
	v_cvt_pk_bf16_f32 v25, v14, v15
	s_waitcnt vmcnt(6)
	v_lshlrev_b32_e32 v14, 16, v94
	v_and_b32_e32 v15, 0xffff0000, v94
	v_fmac_f32_e32 v14, v18, v142
	v_fmac_f32_e32 v15, v19, v143
	global_store_dwordx4 v[26:27], v[22:25], off offset:256
	v_cvt_pk_bf16_f32 v14, v14, v15
	v_lshlrev_b32_e32 v15, 16, v95
	v_and_b32_e32 v16, 0xffff0000, v95
	v_fmac_f32_e32 v15, v20, v144
	v_fmac_f32_e32 v16, v21, v145
	v_cvt_pk_bf16_f32 v15, v15, v16
	v_lshlrev_b32_e32 v16, 16, v96
	v_fmac_f32_e32 v16, v10, v138
	v_and_b32_e32 v10, 0xffff0000, v96
	v_fmac_f32_e32 v10, v11, v139
	v_cvt_pk_bf16_f32 v16, v16, v10
	v_lshlrev_b32_e32 v10, 16, v97
	v_fmac_f32_e32 v10, v12, v140
	s_waitcnt vmcnt(6)
	v_lshlrev_b32_e32 v12, 16, v66
	v_fmac_f32_e32 v12, v6, v134
	v_and_b32_e32 v6, 0xffff0000, v66
	v_and_b32_e32 v11, 0xffff0000, v97
	v_fmac_f32_e32 v6, v7, v135
	v_lshlrev_b32_e32 v7, 16, v67
	v_fmac_f32_e32 v11, v13, v141
	v_cvt_pk_bf16_f32 v17, v10, v11
	v_add_co_u32_e32 v10, vcc, s43, v170
	v_fmac_f32_e32 v7, v8, v136
	v_and_b32_e32 v8, 0xffff0000, v67
	v_addc_co_u32_e32 v11, vcc, 0, v171, vcc
	v_fmac_f32_e32 v8, v9, v137
	global_store_dwordx4 v[10:11], v[14:17], off
	v_cvt_pk_bf16_f32 v6, v12, v6
	v_cvt_pk_bf16_f32 v7, v7, v8
	v_lshlrev_b32_e32 v8, 16, v68
	v_fmac_f32_e32 v8, v2, v130
	v_and_b32_e32 v2, 0xffff0000, v68
	v_fmac_f32_e32 v2, v3, v131
	v_cvt_pk_bf16_f32 v8, v8, v2
	v_lshlrev_b32_e32 v2, 16, v69
	v_and_b32_e32 v3, 0xffff0000, v69
	v_fmac_f32_e32 v2, v4, v132
	v_fmac_f32_e32 v3, v5, v133
	v_cvt_pk_bf16_f32 v9, v2, v3
	global_store_dwordx4 v[10:11], v[6:9], off offset:256
	s_and_b64 vcc, exec, s[2:3]
	s_mov_b64 s[2:3], -1
	s_cbranch_vccnz .LBB0_939
	s_andn2_b64 vcc, exec, s[6:7]
	s_cbranch_vccnz .LBB0_938
	s_barrier
	s_branch .LBB0_938

; #define PG8_STAGE(bufoff, gbase, voff) do { _Pragma("unroll") for (int _i = 0; _i < 2; ++_i) \
;         __builtin_amdgcn_global_load_lds((const unsigned*)((const char*)(gbase) + (voff)[_i]), (PG8_LAS unsigned*)(lds + (bufoff) + ldsw + _i * 8192), 16, 0, 0); } while (0)
; #define PG8_LDA(dst, b, h) do { _Pragma("unroll") for (int m = 0; m < 4; ++m) _Pragma("unroll") for (int k = 0; k < 2; ++k) dst[m][k] = *(const PG8_LAS bf16x8*)(lds + PG8_SA(b, h) + aoff + m * 2048 + k * 1024); } while (0)
; #define PG8_LDB(dst, b, h) do { _Pragma("unroll") for (int n = 0; n < 2; ++n) _Pragma("unroll") for (int k = 0; k < 2; ++k) dst[n][k] = *(const PG8_LAS bf16x8*)(lds + PG8_SB(b, h) + boff + n * 2048 + k * 1024); } while (0)
; #define PG8_WAIT_V(n) asm volatile("s_waitcnt vmcnt(" #n ")" ::: "memory")
; #define PG8_WAIT_L(n) asm volatile("s_waitcnt lgkmcnt(" #n ")" ::: "memory")
; #define PG8_BAR __builtin_amdgcn_s_barrier()
; #define PG8_SCHED __builtin_amdgcn_sched_barrier(0)
; template <class Epi, class Sched, bool ALIGN_EPI = false, bool SP2 = false>
; __device__ __forceinline__ void gemm_phase(PG8_LAS unsigned char* lds, const Gemm g, const Sched& S, const Epi& E) {
;     ...
;             const bool last = (t == nt - 2);
;             const char* a1 = cA + (size_t)(t + 1) * kstep;
;             const char* a2 = last ? nA : cA + (size_t)(t + 2) * kstep; const char* b2 = last ? nB : cB + (size_t)(t + 2) * kstep;
;             const char* a3 = a2 + kstep; const char* b3 = b2 + kstep;
;             if (last && has_next) S.a_ready(nxt);
;             if constexpr (SP2) {
;             PG8_LDB(B0, 0, 0); PG8_LDB(B1, 0, 1); PG8_SCHED; PG8_LDA(At, 0, 0); PG8_STAGE(PG8_SA(1, 1), a1 + hstep, voffA);
;             PG8_WAIT_V(8); PG8_WAIT_L(0); PG8_BAR; PG8_MMA(0, 0, At, B0); PG8_MMA(0, 1, At, B1); PG8_BAR; PG8_SCHED;
;             PG8_LDA(At, 0, 1); PG8_STAGE(PG8_SB(0, 0), b2, voffB); PG8_STAGE(PG8_SB(0, 1), b2 + hstep, voffB); PG8_STAGE(PG8_SA(0, 0), a2, voffA);
;             PG8_WAIT_V(8); PG8_WAIT_L(0); PG8_BAR; PG8_MMA(1, 0, At, B0); PG8_MMA(1, 1, At, B1); PG8_BAR; PG8_SCHED;
.LBB0_1456:
	ds_read_b128 v[130:133], v176
	ds_read_b128 v[134:137], v176 offset:1024
	ds_read_b128 v[138:141], v176 offset:2048
	ds_read_b128 v[142:145], v176 offset:3072
	ds_read_b128 v[146:149], v177
	ds_read_b128 v[150:153], v177 offset:1024
	ds_read_b128 v[170:173], v177 offset:2048
	ds_read_b128 v[180:183], v177 offset:3072
	s_add_u32 s22, s20, 0xfff80080
	s_addc_u32 s23, s21, -1
	s_cmp_eq_u32 s54, 28
	s_cselect_b32 s25, s13, s23
	s_cselect_b32 s24, s50, s22
	s_cselect_b32 s23, s11, s53
	s_cselect_b32 s22, s51, s52
	s_add_i32 m0, s19, 0xc000
	ds_read_b128 v[188:191], v178
	ds_read_b128 v[192:195], v178 offset:1024
	ds_read_b128 v[196:199], v178 offset:2048
	ds_read_b128 v[200:203], v178 offset:3072
	ds_read_b128 v[204:207], v178 offset:4096
	ds_read_b128 v[214:217], v178 offset:5120
	ds_read_b128 v[218:221], v178 offset:6144
	ds_read_b128 v[222:225], v178 offset:7168
	global_load_lds_dwordx4 v162, s[20:21]
	s_add_i32 m0, s19, 0xe000
	s_nop 0
	global_load_lds_dwordx4 v164, s[20:21]
	s_waitcnt vmcnt(8)
	s_waitcnt lgkmcnt(0)
	s_barrier
	s_setprio 1
	s_waitcnt lgkmcnt(0)
	v_mfma_f32_16x16x32_bf16 v[126:129], v[130:133], v[188:191], v[126:129]
	v_mfma_f32_16x16x32_bf16 v[122:125], v[138:141], v[188:191], v[122:125]
	v_mfma_f32_16x16x32_bf16 v[110:113], v[130:133], v[196:199], v[110:113]
	v_mfma_f32_16x16x32_bf16 v[106:109], v[138:141], v[196:199], v[106:109]
	v_mfma_f32_16x16x32_bf16 v[98:101], v[130:133], v[204:207], v[98:101]
	v_mfma_f32_16x16x32_bf16 v[90:93], v[138:141], v[204:207], v[90:93]
	v_mfma_f32_16x16x32_bf16 v[82:85], v[130:133], v[218:221], v[82:85]
	v_mfma_f32_16x16x32_bf16 v[74:77], v[138:141], v[218:221], v[74:77]
	v_mfma_f32_16x16x32_bf16 v[126:129], v[134:137], v[192:195], v[126:129]
	v_mfma_f32_16x16x32_bf16 v[122:125], v[142:145], v[192:195], v[122:125]
	v_mfma_f32_16x16x32_bf16 v[110:113], v[134:137], v[200:203], v[110:113]
	v_mfma_f32_16x16x32_bf16 v[106:109], v[142:145], v[200:203], v[106:109]
	v_mfma_f32_16x16x32_bf16 v[98:101], v[134:137], v[214:217], v[98:101]
	v_mfma_f32_16x16x32_bf16 v[90:93], v[142:145], v[214:217], v[90:93]
	v_mfma_f32_16x16x32_bf16 v[82:85], v[134:137], v[222:225], v[82:85]
	v_mfma_f32_16x16x32_bf16 v[74:77], v[142:145], v[222:225], v[74:77]
	s_setprio 0
	s_setprio 1
	v_mfma_f32_16x16x32_bf16 v[118:121], v[146:149], v[188:191], v[118:121]
	v_mfma_f32_16x16x32_bf16 v[114:117], v[170:173], v[188:191], v[114:117]
	v_mfma_f32_16x16x32_bf16 v[102:105], v[146:149], v[196:199], v[102:105]
	v_mfma_f32_16x16x32_bf16 v[94:97], v[170:173], v[196:199], v[94:97]
	v_mfma_f32_16x16x32_bf16 v[86:89], v[146:149], v[204:207], v[86:89]
	v_mfma_f32_16x16x32_bf16 v[78:81], v[170:173], v[204:207], v[78:81]
	v_mfma_f32_16x16x32_bf16 v[70:73], v[146:149], v[218:221], v[70:73]
	v_mfma_f32_16x16x32_bf16 v[66:69], v[170:173], v[218:221], v[66:69]
	v_mfma_f32_16x16x32_bf16 v[118:121], v[150:153], v[192:195], v[118:121]
	v_mfma_f32_16x16x32_bf16 v[114:117], v[180:183], v[192:195], v[114:117]
	v_mfma_f32_16x16x32_bf16 v[102:105], v[150:153], v[200:203], v[102:105]
	v_mfma_f32_16x16x32_bf16 v[94:97], v[180:183], v[200:203], v[94:97]
	v_mfma_f32_16x16x32_bf16 v[86:89], v[150:153], v[214:217], v[86:89]
	v_mfma_f32_16x16x32_bf16 v[78:81], v[180:183], v[214:217], v[78:81]
	v_mfma_f32_16x16x32_bf16 v[70:73], v[150:153], v[222:225], v[70:73]
	v_mfma_f32_16x16x32_bf16 v[66:69], v[180:183], v[222:225], v[66:69]
	s_setprio 0
	s_barrier
	s_add_i32 s55, s42, s29
	s_mov_b32 m0, s55
	ds_read_b128 v[188:191], v178 offset:16384
	ds_read_b128 v[192:195], v178 offset:17408
	ds_read_b128 v[196:199], v178 offset:18432
	ds_read_b128 v[200:203], v178 offset:19456
	ds_read_b128 v[204:207], v178 offset:20480
	ds_read_b128 v[214:217], v178 offset:21504
	ds_read_b128 v[218:221], v178 offset:22528
	ds_read_b128 v[222:225], v178 offset:23552
	global_load_lds_dwordx4 v156, s[22:23]
	s_add_i32 m0, s55, 0x2000
	s_add_u32 s56, s22, 0x80000
	s_addc_u32 s57, s23, 0
	s_add_i32 s55, s43, s29
	global_load_lds_dwordx4 v160, s[22:23]
	s_mov_b32 m0, s55
	s_nop 0
	global_load_lds_dwordx4 v156, s[56:57]
	s_add_i32 m0, s55, 0x2000
	s_nop 0
	global_load_lds_dwordx4 v160, s[56:57]
	s_mov_b32 m0, s19
	s_nop 0
	global_load_lds_dwordx4 v154, s[24:25]
	s_mov_b32 m0, s30
	s_nop 0
	global_load_lds_dwordx4 v158, s[24:25]
	s_waitcnt vmcnt(8)
	s_waitcnt lgkmcnt(0)
	s_barrier
	s_setprio 1
	s_waitcnt lgkmcnt(0)
	v_mfma_f32_16x16x32_bf16 v[62:65], v[130:133], v[188:191], v[62:65]
	v_mfma_f32_16x16x32_bf16 v[58:61], v[138:141], v[188:191], v[58:61]
	v_mfma_f32_16x16x32_bf16 v[50:53], v[130:133], v[196:199], v[50:53]
	v_mfma_f32_16x16x32_bf16 v[42:45], v[138:141], v[196:199], v[42:45]
	v_mfma_f32_16x16x32_bf16 v[34:37], v[130:133], v[204:207], v[34:37]
	v_mfma_f32_16x16x32_bf16 v[26:29], v[138:141], v[204:207], v[26:29]
	v_mfma_f32_16x16x32_bf16 v[18:21], v[130:133], v[218:221], v[18:21]
	v_mfma_f32_16x16x32_bf16 v[10:13], v[138:141], v[218:221], v[10:13]
	v_mfma_f32_16x16x32_bf16 v[62:65], v[134:137], v[192:195], v[62:65]
	v_mfma_f32_16x16x32_bf16 v[58:61], v[142:145], v[192:195], v[58:61]
	v_mfma_f32_16x16x32_bf16 v[50:53], v[134:137], v[200:203], v[50:53]
	v_mfma_f32_16x16x32_bf16 v[42:45], v[142:145], v[200:203], v[42:45]
	v_mfma_f32_16x16x32_bf16 v[34:37], v[134:137], v[214:217], v[34:37]
	v_mfma_f32_16x16x32_bf16 v[26:29], v[142:145], v[214:217], v[26:29]
	v_mfma_f32_16x16x32_bf16 v[18:21], v[134:137], v[222:225], v[18:21]
	v_mfma_f32_16x16x32_bf16 v[10:13], v[142:145], v[222:225], v[10:13]
	s_setprio 0
	s_setprio 1
	v_mfma_f32_16x16x32_bf16 v[54:57], v[146:149], v[188:191], v[54:57]
	v_mfma_f32_16x16x32_bf16 v[46:49], v[170:173], v[188:191], v[46:49]
	v_mfma_f32_16x16x32_bf16 v[38:41], v[146:149], v[196:199], v[38:41]
	v_mfma_f32_16x16x32_bf16 v[30:33], v[170:173], v[196:199], v[30:33]
	v_mfma_f32_16x16x32_bf16 v[22:25], v[146:149], v[204:207], v[22:25]
	v_mfma_f32_16x16x32_bf16 v[14:17], v[170:173], v[204:207], v[14:17]
	v_mfma_f32_16x16x32_bf16 v[6:9], v[146:149], v[218:221], v[6:9]
	v_mfma_f32_16x16x32_bf16 v[2:5], v[170:173], v[218:221], v[2:5]
	v_mfma_f32_16x16x32_bf16 v[54:57], v[150:153], v[192:195], v[54:57]
	v_mfma_f32_16x16x32_bf16 v[46:49], v[180:183], v[192:195], v[46:49]
	v_mfma_f32_16x16x32_bf16 v[38:41], v[150:153], v[200:203], v[38:41]
	v_mfma_f32_16x16x32_bf16 v[30:33], v[180:183], v[200:203], v[30:33]
	v_mfma_f32_16x16x32_bf16 v[22:25], v[150:153], v[214:217], v[22:25]
	v_mfma_f32_16x16x32_bf16 v[14:17], v[180:183], v[214:217], v[14:17]
	v_mfma_f32_16x16x32_bf16 v[6:9], v[150:153], v[222:225], v[6:9]
	v_mfma_f32_16x16x32_bf16 v[2:5], v[180:183], v[222:225], v[2:5]
	s_setprio 0
	s_barrier
; #define PG8_STAGE(bufoff, gbase, voff) do { _Pragma("unroll") for (int _i = 0; _i < 2; ++_i) \
;         __builtin_amdgcn_global_load_lds((const unsigned*)((const char*)(gbase) + (voff)[_i]), (PG8_LAS unsigned*)(lds + (bufoff) + ldsw + _i * 8192), 16, 0, 0); } while (0)
; #define PG8_LDA(dst, b, h) do { _Pragma("unroll") for (int m = 0; m < 4; ++m) _Pragma("unroll") for (int k = 0; k < 2; ++k) dst[m][k] = *(const PG8_LAS bf16x8*)(lds + PG8_SA(b, h) + aoff + m * 2048 + k * 1024); } while (0)
; #define PG8_LDB(dst, b, h) do { _Pragma("unroll") for (int n = 0; n < 2; ++n) _Pragma("unroll") for (int k = 0; k < 2; ++k) dst[n][k] = *(const PG8_LAS bf16x8*)(lds + PG8_SB(b, h) + boff + n * 2048 + k * 1024); } while (0)
; #define PG8_WAIT_V(n) asm volatile("s_waitcnt vmcnt(" #n ")" ::: "memory")
; #define PG8_WAIT_L(n) asm volatile("s_waitcnt lgkmcnt(" #n ")" ::: "memory")
; #define PG8_BAR __builtin_amdgcn_s_barrier()
; #define PG8_SCHED __builtin_amdgcn_sched_barrier(0)
; template <class Epi, class Sched, bool ALIGN_EPI = false, bool SP2 = false>
; __device__ __forceinline__ void gemm_phase(PG8_LAS unsigned char* lds, const Gemm g, const Sched& S, const Epi& E) {
;     ...
;             PG8_LDB(B0, 1, 0); PG8_LDB(B1, 1, 1); PG8_SCHED; PG8_LDA(At, 1, 0); PG8_STAGE(PG8_SA(0, 1), a2 + hstep, voffA);
;             PG8_WAIT_V(8); PG8_WAIT_L(0); PG8_BAR; PG8_MMA(0, 0, At, B0); PG8_MMA(0, 1, At, B1); PG8_BAR; PG8_SCHED;
;             PG8_LDA(At, 1, 1); PG8_STAGE(PG8_SB(1, 0), b3, voffB); PG8_STAGE(PG8_SB(1, 1), b3 + hstep, voffB); PG8_STAGE(PG8_SA(1, 0), a3, voffA);
;             PG8_WAIT_V(8); PG8_WAIT_L(0); PG8_BAR; PG8_MMA(1, 0, At, B0); PG8_MMA(1, 1, At, B1); PG8_BAR; PG8_SCHED;
	s_add_i32 s55, 0, 0x18000
	s_add_i32 s56, 0, 0x1c000
	ds_read_b128 v[130:133], v248
	ds_read_b128 v[134:137], v248 offset:1024
	ds_read_b128 v[138:141], v248 offset:2048
	ds_read_b128 v[142:145], v248 offset:3072
	ds_read_b128 v[146:149], v249
	ds_read_b128 v[150:153], v249 offset:1024
	ds_read_b128 v[170:173], v249 offset:2048
	ds_read_b128 v[180:183], v249 offset:3072
	s_add_u32 s24, s24, 0x80000
	s_addc_u32 s25, s25, 0
	s_mov_b32 m0, s31
	ds_read_b128 v[188:191], v178 offset:32768
	ds_read_b128 v[192:195], v178 offset:33792
	ds_read_b128 v[196:199], v178 offset:34816
	ds_read_b128 v[200:203], v178 offset:35840
	ds_read_b128 v[204:207], v178 offset:36864
	ds_read_b128 v[214:217], v178 offset:37888
	ds_read_b128 v[218:221], v178 offset:38912
	ds_read_b128 v[222:225], v178 offset:39936
	global_load_lds_dwordx4 v154, s[24:25]
	s_mov_b32 m0, s33
	s_nop 0
	global_load_lds_dwordx4 v158, s[24:25]
	s_waitcnt vmcnt(8)
	s_waitcnt lgkmcnt(0)
	s_barrier
	s_setprio 1
	s_waitcnt lgkmcnt(0)
	v_mfma_f32_16x16x32_bf16 v[126:129], v[130:133], v[188:191], v[126:129]
	v_mfma_f32_16x16x32_bf16 v[122:125], v[138:141], v[188:191], v[122:125]
	v_mfma_f32_16x16x32_bf16 v[110:113], v[130:133], v[196:199], v[110:113]
	v_mfma_f32_16x16x32_bf16 v[106:109], v[138:141], v[196:199], v[106:109]
	v_mfma_f32_16x16x32_bf16 v[98:101], v[130:133], v[204:207], v[98:101]
	v_mfma_f32_16x16x32_bf16 v[90:93], v[138:141], v[204:207], v[90:93]
	v_mfma_f32_16x16x32_bf16 v[82:85], v[130:133], v[218:221], v[82:85]
	v_mfma_f32_16x16x32_bf16 v[74:77], v[138:141], v[218:221], v[74:77]
	v_mfma_f32_16x16x32_bf16 v[126:129], v[134:137], v[192:195], v[126:129]
	v_mfma_f32_16x16x32_bf16 v[122:125], v[142:145], v[192:195], v[122:125]
	v_mfma_f32_16x16x32_bf16 v[110:113], v[134:137], v[200:203], v[110:113]
	v_mfma_f32_16x16x32_bf16 v[106:109], v[142:145], v[200:203], v[106:109]
	v_mfma_f32_16x16x32_bf16 v[98:101], v[134:137], v[214:217], v[98:101]
	v_mfma_f32_16x16x32_bf16 v[90:93], v[142:145], v[214:217], v[90:93]
	v_mfma_f32_16x16x32_bf16 v[82:85], v[134:137], v[222:225], v[82:85]
	v_mfma_f32_16x16x32_bf16 v[74:77], v[142:145], v[222:225], v[74:77]
	s_setprio 0
	s_setprio 1
	v_mfma_f32_16x16x32_bf16 v[118:121], v[146:149], v[188:191], v[118:121]
	v_mfma_f32_16x16x32_bf16 v[114:117], v[170:173], v[188:191], v[114:117]
	v_mfma_f32_16x16x32_bf16 v[102:105], v[146:149], v[196:199], v[102:105]
	v_mfma_f32_16x16x32_bf16 v[94:97], v[170:173], v[196:199], v[94:97]
	v_mfma_f32_16x16x32_bf16 v[86:89], v[146:149], v[204:207], v[86:89]
	v_mfma_f32_16x16x32_bf16 v[78:81], v[170:173], v[204:207], v[78:81]
	v_mfma_f32_16x16x32_bf16 v[70:73], v[146:149], v[218:221], v[70:73]
	v_mfma_f32_16x16x32_bf16 v[66:69], v[170:173], v[218:221], v[66:69]
	v_mfma_f32_16x16x32_bf16 v[118:121], v[150:153], v[192:195], v[118:121]
	v_mfma_f32_16x16x32_bf16 v[114:117], v[180:183], v[192:195], v[114:117]
	v_mfma_f32_16x16x32_bf16 v[102:105], v[150:153], v[200:203], v[102:105]
	v_mfma_f32_16x16x32_bf16 v[94:97], v[180:183], v[200:203], v[94:97]
	v_mfma_f32_16x16x32_bf16 v[86:89], v[150:153], v[214:217], v[86:89]
	v_mfma_f32_16x16x32_bf16 v[78:81], v[180:183], v[214:217], v[78:81]
	v_mfma_f32_16x16x32_bf16 v[70:73], v[150:153], v[222:225], v[70:73]
	v_mfma_f32_16x16x32_bf16 v[66:69], v[180:183], v[222:225], v[66:69]
	s_setprio 0
	s_barrier
	s_add_u32 s98, s22, 0x80
	s_addc_u32 s99, s23, 0
	s_add_u32 s100, s24, 0xfff80080
	s_addc_u32 s101, s25, -1
	s_add_i32 s24, s55, s29
	s_mov_b32 m0, s24
	ds_read_b128 v[188:191], v178 offset:49152
	ds_read_b128 v[192:195], v178 offset:50176
	ds_read_b128 v[196:199], v178 offset:51200
	ds_read_b128 v[200:203], v178 offset:52224
	ds_read_b128 v[204:207], v178 offset:53248
	ds_read_b128 v[214:217], v178 offset:54272
	ds_read_b128 v[218:221], v178 offset:55296
	ds_read_b128 v[222:225], v178 offset:56320
	global_load_lds_dwordx4 v156, s[98:99]
	s_add_i32 m0, s24, 0x2000
	s_add_u32 s22, s22, 0x80080
	s_addc_u32 s23, s23, 0
	s_add_i32 s24, s56, s29
	global_load_lds_dwordx4 v160, s[98:99]
	s_mov_b32 m0, s24
	s_nop 0
	global_load_lds_dwordx4 v156, s[22:23]
	s_add_i32 m0, s24, 0x2000
	s_nop 0
	global_load_lds_dwordx4 v160, s[22:23]
	s_mov_b32 m0, s38
	s_nop 0
	global_load_lds_dwordx4 v154, s[100:101]
	s_mov_b32 m0, s39
	s_nop 0
	global_load_lds_dwordx4 v158, s[100:101]
	s_waitcnt vmcnt(8)
	s_waitcnt lgkmcnt(0)
	s_barrier
	s_setprio 1
	s_waitcnt lgkmcnt(0)
	v_mfma_f32_16x16x32_bf16 v[62:65], v[130:133], v[188:191], v[62:65]
	v_mfma_f32_16x16x32_bf16 v[58:61], v[138:141], v[188:191], v[58:61]
	v_mfma_f32_16x16x32_bf16 v[50:53], v[130:133], v[196:199], v[50:53]
	v_mfma_f32_16x16x32_bf16 v[42:45], v[138:141], v[196:199], v[42:45]
	v_mfma_f32_16x16x32_bf16 v[34:37], v[130:133], v[204:207], v[34:37]
	v_mfma_f32_16x16x32_bf16 v[26:29], v[138:141], v[204:207], v[26:29]
	v_mfma_f32_16x16x32_bf16 v[18:21], v[130:133], v[218:221], v[18:21]
	v_mfma_f32_16x16x32_bf16 v[10:13], v[138:141], v[218:221], v[10:13]
	v_mfma_f32_16x16x32_bf16 v[62:65], v[134:137], v[192:195], v[62:65]
	v_mfma_f32_16x16x32_bf16 v[58:61], v[142:145], v[192:195], v[58:61]
	v_mfma_f32_16x16x32_bf16 v[50:53], v[134:137], v[200:203], v[50:53]
	v_mfma_f32_16x16x32_bf16 v[42:45], v[142:145], v[200:203], v[42:45]
	v_mfma_f32_16x16x32_bf16 v[34:37], v[134:137], v[214:217], v[34:37]
	v_mfma_f32_16x16x32_bf16 v[26:29], v[142:145], v[214:217], v[26:29]
	v_mfma_f32_16x16x32_bf16 v[18:21], v[134:137], v[222:225], v[18:21]
	v_mfma_f32_16x16x32_bf16 v[10:13], v[142:145], v[222:225], v[10:13]
	s_setprio 0
	s_setprio 1
	v_mfma_f32_16x16x32_bf16 v[54:57], v[146:149], v[188:191], v[54:57]
	v_mfma_f32_16x16x32_bf16 v[46:49], v[170:173], v[188:191], v[46:49]
	v_mfma_f32_16x16x32_bf16 v[38:41], v[146:149], v[196:199], v[38:41]
	v_mfma_f32_16x16x32_bf16 v[30:33], v[170:173], v[196:199], v[30:33]
	v_mfma_f32_16x16x32_bf16 v[22:25], v[146:149], v[204:207], v[22:25]
	v_mfma_f32_16x16x32_bf16 v[14:17], v[170:173], v[204:207], v[14:17]
	v_mfma_f32_16x16x32_bf16 v[6:9], v[146:149], v[218:221], v[6:9]
	v_mfma_f32_16x16x32_bf16 v[2:5], v[170:173], v[218:221], v[2:5]
	v_mfma_f32_16x16x32_bf16 v[54:57], v[150:153], v[192:195], v[54:57]
	v_mfma_f32_16x16x32_bf16 v[46:49], v[180:183], v[192:195], v[46:49]
	v_mfma_f32_16x16x32_bf16 v[38:41], v[150:153], v[200:203], v[38:41]
	v_mfma_f32_16x16x32_bf16 v[30:33], v[180:183], v[200:203], v[30:33]
	v_mfma_f32_16x16x32_bf16 v[22:25], v[150:153], v[214:217], v[22:25]
	v_mfma_f32_16x16x32_bf16 v[14:17], v[180:183], v[214:217], v[14:17]
	v_mfma_f32_16x16x32_bf16 v[6:9], v[150:153], v[222:225], v[6:9]
	v_mfma_f32_16x16x32_bf16 v[2:5], v[180:183], v[222:225], v[2:5]
	s_setprio 0
	s_barrier
;     __device__ __forceinline__ void operator()(const f32x4 (&acc)[2][2][4][2], const Unit& u, int wr, int wc, int fr, int fq) const {
;         const int row0 = u.pm * BM + wr * 64 + fr, col0 = u.pn * BM + wc * 32 + 8 * fq;
;         const float* __restrict__ gp = gate + (size_t)(u.pm >> 3) * 12288 + col0;
;         bf16_t* __restrict__ op = out + (size_t)row0 * 2048 + col0;
;         f32x4 gv[2][2];
; #pragma unroll
;         for (int bj = 0; bj < 2; ++bj)
; #pragma unroll
;             for (int n = 0; n < 2; ++n) gv[bj][n] = *(const f32x4*)(gp + bj * HALF + n * 4);
; #pragma unroll
;         for (int ai = 0; ai < 2; ++ai) {
;             if constexpr (BASE_F32) {
;                 const float* __restrict__ bp = (const float*)base + (size_t)row0 * 2048 + col0;
;                 f32x4 bs[4][2][2];
; #pragma unroll
;                 for (int m = 0; m < 4; ++m)
; #pragma unroll
;                     for (int bj = 0; bj < 2; ++bj)
; #pragma unroll
;                         for (int n = 0; n < 2; ++n) bs[m][bj][n] = *(const f32x4*)(bp + (size_t)(ai * HALF + m * 16) * 2048 + bj * HALF + n * 4);
; #pragma unroll
;                 for (int m = 0; m < 4; ++m)
; #pragma unroll
;                     for (int bj = 0; bj < 2; ++bj) { const f32x4 v0 = bs[m][bj][0] + gv[bj][0] * acc[ai][bj][m][0], v1 = bs[m][bj][1] + gv[bj][1] * acc[ai][bj][m][1];
;                         u32x4 w; w.x = cvt_pk_bf16(v0[0], v0[1]); w.y = cvt_pk_bf16(v0[2], v0[3]); w.z = cvt_pk_bf16(v1[0], v1[1]); w.w = cvt_pk_bf16(v1[2], v1[3]);
;                         *(u32x4*)(op + (size_t)(ai * HALF + m * 16) * 2048 + bj * HALF) = w; }
;             } else {
;                 const bf16_t* __restrict__ bp = (const bf16_t*)base + (size_t)row0 * 2048 + col0;
;                 u32x4 bs[4][2];
; #pragma unroll
;                 for (int m = 0; m < 4; ++m)
; #pragma unroll
;                     for (int bj = 0; bj < 2; ++bj) bs[m][bj] = *(const u32x4*)(bp + (size_t)(ai * HALF + m * 16) * 2048 + bj * HALF);
; #pragma unroll
;                 for (int m = 0; m < 4; ++m)
; #pragma unroll
;                     for (int bj = 0; bj < 2; ++bj) { const u32x4 b = bs[m][bj]; const f32x4 a0 = acc[ai][bj][m][0], a1 = acc[ai][bj][m][1], g0 = gv[bj][0], g1 = gv[bj][1];
;                         u32x4 w;
	s_add_i32 s54, s54, 2
	s_add_u32 s20, s20, 0x100
	s_addc_u32 s21, s21, 0
	s_add_u32 s52, s52, 0x100
	s_addc_u32 s53, s53, 0
	s_cmp_gt_u32 s54, 29
	s_cbranch_scc0 .LBB0_1456
	v_lshl_add_u32 v130, s18, 8, v1
	v_lshl_or_b32 v132, s49, 8, v175
	v_ashrrev_i32_e32 v131, 31, v130
	v_readlane_b32 s20, v247, 30
	v_ashrrev_i32_e32 v133, 31, v132
	v_lshlrev_b64 v[146:147], 12, v[130:131]
	v_readlane_b32 s21, v247, 31
	s_ashr_i32 s11, s18, 3
	v_lshlrev_b64 v[148:149], 1, v[132:133]
	v_lshl_add_u64 v[130:131], s[20:21], 0, v[146:147]
	s_mul_hi_i32 s13, s11, 0xc000
	s_mul_i32 s11, s11, 0xc000
	v_lshl_add_u64 v[172:173], v[130:131], 0, v[148:149]
	s_add_u32 s20, s36, s11
	s_addc_u32 s21, s37, s13
	v_add_co_u32_e32 v150, vcc, s35, v172
	global_load_dwordx4 v[180:183], v[172:173], off
	global_load_dwordx4 v[188:191], v[172:173], off offset:256
	v_lshl_add_u64 v[130:131], v[132:133], 2, s[20:21]
	v_addc_co_u32_e32 v151, vcc, 0, v173, vcc
	global_load_dwordx4 v[142:145], v[130:131], off
	global_load_dwordx4 v[138:141], v[130:131], off offset:16
	global_load_dwordx4 v[134:137], v[130:131], off offset:512
	s_nop 0
	global_load_dwordx4 v[130:133], v[130:131], off offset:528
	v_lshl_add_u64 v[146:147], s[66:67], 0, v[146:147]
	global_load_dwordx4 v[192:195], v[150:151], off
	global_load_dwordx4 v[196:199], v[150:151], off offset:256
	v_lshl_add_u64 v[170:171], v[146:147], 0, v[148:149]
	s_and_b64 vcc, exec, s[8:9]
	s_cbranch_vccz .LBB0_1459
	s_barrier
.LBB0_1459:
	v_add_co_u32_e32 v146, vcc, s44, v172
	s_waitcnt vmcnt(0)
	v_lshlrev_b32_e32 v179, 16, v180
	v_addc_co_u32_e32 v147, vcc, 0, v173, vcc
	v_add_co_u32_e32 v148, vcc, s41, v172
	v_lshlrev_b32_e32 v213, 16, v189
	s_nop 0
	v_addc_co_u32_e32 v149, vcc, 0, v173, vcc
	global_load_dwordx4 v[200:203], v[146:147], off
	global_load_dwordx4 v[204:207], v[146:147], off offset:256
	global_load_dwordx4 v[150:153], v[148:149], off
	s_nop 0
	global_load_dwordx4 v[146:149], v[148:149], off offset:256
	v_fmac_f32_e32 v213, v120, v136
	v_lshlrev_b32_e32 v120, 16, v193
	v_fmac_f32_e32 v120, v112, v144
	v_lshlrev_b32_e32 v112, 16, v194
	v_and_b32_e32 v180, 0xffff0000, v180
	v_lshlrev_b32_e32 v184, 16, v181
	v_and_b32_e32 v181, 0xffff0000, v181
	v_lshlrev_b32_e32 v185, 16, v182
	v_and_b32_e32 v182, 0xffff0000, v182
	v_lshlrev_b32_e32 v208, 16, v183
	v_and_b32_e32 v183, 0xffff0000, v183
	v_lshlrev_b32_e32 v209, 16, v188
	v_and_b32_e32 v188, 0xffff0000, v188
	v_and_b32_e32 v189, 0xffff0000, v189
	v_lshlrev_b32_e32 v214, 16, v190
	v_and_b32_e32 v190, 0xffff0000, v190
	v_lshlrev_b32_e32 v215, 16, v191
	v_and_b32_e32 v191, 0xffff0000, v191
	v_fmac_f32_e32 v112, v106, v138
	v_and_b32_e32 v106, 0xffff0000, v194
	v_fmac_f32_e32 v179, v126, v142
	v_fmac_f32_e32 v180, v127, v143
	v_fmac_f32_e32 v184, v128, v144
	v_fmac_f32_e32 v181, v129, v145
	v_fmac_f32_e32 v185, v122, v138
	v_fmac_f32_e32 v182, v123, v139
	v_fmac_f32_e32 v208, v124, v140
	v_fmac_f32_e32 v183, v125, v141
	v_fmac_f32_e32 v209, v118, v134
	v_fmac_f32_e32 v188, v119, v135
	v_fmac_f32_e32 v189, v121, v137
	v_fmac_f32_e32 v214, v114, v130
	v_fmac_f32_e32 v190, v115, v131
	v_fmac_f32_e32 v215, v116, v132
	v_fmac_f32_e32 v191, v117, v133
	v_lshlrev_b32_e32 v118, 16, v192
	v_and_b32_e32 v119, 0xffff0000, v192
	v_and_b32_e32 v121, 0xffff0000, v193
	v_cvt_pk_bf16_f32 v114, v179, v180
	v_cvt_pk_bf16_f32 v115, v184, v181
	v_cvt_pk_bf16_f32 v116, v185, v182
	v_cvt_pk_bf16_f32 v117, v208, v183
	v_fmac_f32_e32 v106, v107, v139
	v_fmac_f32_e32 v118, v110, v142
	v_fmac_f32_e32 v119, v111, v143
	global_store_dwordx4 v[170:171], v[114:117], off
	v_fmac_f32_e32 v121, v113, v145
	v_and_b32_e32 v107, 0xffff0000, v195
	v_cvt_pk_bf16_f32 v114, v209, v188
	v_cvt_pk_bf16_f32 v115, v213, v189
	v_cvt_pk_bf16_f32 v116, v214, v190
	v_cvt_pk_bf16_f32 v117, v215, v191
	global_store_dwordx4 v[170:171], v[114:117], off offset:256
	v_cvt_pk_bf16_f32 v110, v118, v119
	v_cvt_pk_bf16_f32 v111, v120, v121
	v_cvt_pk_bf16_f32 v112, v112, v106
	v_lshlrev_b32_e32 v106, 16, v195
	v_fmac_f32_e32 v106, v108, v140
	v_lshlrev_b32_e32 v108, 16, v196
	v_fmac_f32_e32 v108, v102, v134
	v_and_b32_e32 v102, 0xffff0000, v196
	v_fmac_f32_e32 v102, v103, v135
	v_lshlrev_b32_e32 v103, 16, v197
	v_fmac_f32_e32 v107, v109, v141
	v_cvt_pk_bf16_f32 v113, v106, v107
	v_add_co_u32_e32 v106, vcc, s35, v170
	v_fmac_f32_e32 v103, v104, v136
	v_and_b32_e32 v104, 0xffff0000, v197
	v_addc_co_u32_e32 v107, vcc, 0, v171, vcc
	v_fmac_f32_e32 v104, v105, v137
	global_store_dwordx4 v[106:107], v[110:113], off
	v_cvt_pk_bf16_f32 v102, v108, v102
	v_cvt_pk_bf16_f32 v103, v103, v104
	v_lshlrev_b32_e32 v104, 16, v198
	v_fmac_f32_e32 v104, v94, v130
	v_and_b32_e32 v94, 0xffff0000, v198
	v_fmac_f32_e32 v94, v95, v131
	v_cvt_pk_bf16_f32 v104, v104, v94
	v_lshlrev_b32_e32 v94, 16, v199
	v_and_b32_e32 v95, 0xffff0000, v199
	v_fmac_f32_e32 v94, v96, v132
	v_fmac_f32_e32 v95, v97, v133
	v_cvt_pk_bf16_f32 v105, v94, v95
	s_waitcnt vmcnt(6)
	v_lshlrev_b32_e32 v94, 16, v200
	v_and_b32_e32 v95, 0xffff0000, v200
	v_fmac_f32_e32 v94, v98, v142
	v_fmac_f32_e32 v95, v99, v143
	global_store_dwordx4 v[106:107], v[102:105], off offset:256
	v_cvt_pk_bf16_f32 v94, v94, v95
	v_lshlrev_b32_e32 v95, 16, v201
	v_and_b32_e32 v96, 0xffff0000, v201
	v_fmac_f32_e32 v95, v100, v144
	v_fmac_f32_e32 v96, v101, v145
	v_cvt_pk_bf16_f32 v95, v95, v96
	v_lshlrev_b32_e32 v96, 16, v202
	v_fmac_f32_e32 v96, v90, v138
	v_and_b32_e32 v90, 0xffff0000, v202
	v_fmac_f32_e32 v90, v91, v139
	v_cvt_pk_bf16_f32 v96, v96, v90
	v_lshlrev_b32_e32 v90, 16, v203
	v_fmac_f32_e32 v90, v92, v140
	s_waitcnt vmcnt(6)
; __device__ __forceinline__ unsigned cvt_pk_bf16(float lo, float hi) { unsigned r; asm volatile("v_cvt_pk_bf16_f32 %0, %1, %2" : "=v"(r) : "v"(lo), "v"(hi)); return r; }
;     __device__ __forceinline__ void operator()(const f32x4 (&acc)[2][2][4][2], const Unit& u, int wr, int wc, int fr, int fq) const {
;     ...
;                 for (int m = 0; m < 4; ++m)
; #pragma unroll
;                     for (int bj = 0; bj < 2; ++bj) { const u32x4 b = bs[m][bj]; const f32x4 a0 = acc[ai][bj][m][0], a1 = acc[ai][bj][m][1], g0 = gv[bj][0], g1 = gv[bj][1];
;                         u32x4 w;
;                         w.x = cvt_pk_bf16(__builtin_bit_cast(float, b.x << 16) + g0[0] * a0[0], __builtin_bit_cast(float, b.x & 0xffff0000u) + g0[1] * a0[1]);
;                         w.y = cvt_pk_bf16(__builtin_bit_cast(float, b.y << 16) + g0[2] * a0[2], __builtin_bit_cast(float, b.y & 0xffff0000u) + g0[3] * a0[3]);
;                         w.z = cvt_pk_bf16(__builtin_bit_cast(float, b.z << 16) + g1[0] * a1[0], __builtin_bit_cast(float, b.z & 0xffff0000u) + g1[1] * a1[1]);
;                         w.w = cvt_pk_bf16(__builtin_bit_cast(float, b.w << 16) + g1[2] * a1[2], __builtin_bit_cast(float, b.w & 0xffff0000u) + g1[3] * a1[3]);
;                         *(u32x4*)(op + (size_t)(ai * HALF + m * 16) * 2048 + bj * HALF) = w; }
	v_lshlrev_b32_e32 v92, 16, v204
	v_fmac_f32_e32 v92, v86, v134
	v_and_b32_e32 v86, 0xffff0000, v204
	v_and_b32_e32 v91, 0xffff0000, v203
	v_fmac_f32_e32 v86, v87, v135
	v_lshlrev_b32_e32 v87, 16, v205
	v_fmac_f32_e32 v91, v93, v141
	v_cvt_pk_bf16_f32 v97, v90, v91
	v_add_co_u32_e32 v90, vcc, s44, v170
	v_fmac_f32_e32 v87, v88, v136
	v_and_b32_e32 v88, 0xffff0000, v205
	v_addc_co_u32_e32 v91, vcc, 0, v171, vcc
	v_fmac_f32_e32 v88, v89, v137
	global_store_dwordx4 v[90:91], v[94:97], off
	v_cvt_pk_bf16_f32 v86, v92, v86
	v_cvt_pk_bf16_f32 v87, v87, v88
	v_lshlrev_b32_e32 v88, 16, v206
	v_fmac_f32_e32 v88, v78, v130
	v_and_b32_e32 v78, 0xffff0000, v206
	v_fmac_f32_e32 v78, v79, v131
	v_cvt_pk_bf16_f32 v88, v88, v78
	v_lshlrev_b32_e32 v78, 16, v207
	v_and_b32_e32 v79, 0xffff0000, v207
	v_fmac_f32_e32 v78, v80, v132
	v_fmac_f32_e32 v79, v81, v133
	v_cvt_pk_bf16_f32 v89, v78, v79
	s_waitcnt vmcnt(6)
	v_lshlrev_b32_e32 v78, 16, v150
	v_and_b32_e32 v79, 0xffff0000, v150
	v_fmac_f32_e32 v78, v82, v142
	v_fmac_f32_e32 v79, v83, v143
	global_store_dwordx4 v[90:91], v[86:89], off offset:256
	v_cvt_pk_bf16_f32 v78, v78, v79
	v_lshlrev_b32_e32 v79, 16, v151
	v_and_b32_e32 v80, 0xffff0000, v151
	v_fmac_f32_e32 v79, v84, v144
	v_fmac_f32_e32 v80, v85, v145
	v_cvt_pk_bf16_f32 v79, v79, v80
	v_lshlrev_b32_e32 v80, 16, v152
	v_fmac_f32_e32 v80, v74, v138
	v_and_b32_e32 v74, 0xffff0000, v152
	v_fmac_f32_e32 v74, v75, v139
	v_cvt_pk_bf16_f32 v80, v80, v74
	v_lshlrev_b32_e32 v74, 16, v153
	v_fmac_f32_e32 v74, v76, v140
	s_waitcnt vmcnt(6)
	v_lshlrev_b32_e32 v76, 16, v146
	v_fmac_f32_e32 v76, v70, v134
	v_and_b32_e32 v70, 0xffff0000, v146
	v_and_b32_e32 v75, 0xffff0000, v153
	v_fmac_f32_e32 v70, v71, v135
	v_lshlrev_b32_e32 v71, 16, v147
	v_fmac_f32_e32 v75, v77, v141
	v_cvt_pk_bf16_f32 v81, v74, v75
	v_add_co_u32_e32 v74, vcc, s41, v170
	v_fmac_f32_e32 v71, v72, v136
	v_and_b32_e32 v72, 0xffff0000, v147
	v_addc_co_u32_e32 v75, vcc, 0, v171, vcc
	v_fmac_f32_e32 v72, v73, v137
	global_store_dwordx4 v[74:75], v[78:81], off
	v_cvt_pk_bf16_f32 v70, v76, v70
	v_cvt_pk_bf16_f32 v71, v71, v72
	v_lshlrev_b32_e32 v72, 16, v148
	v_fmac_f32_e32 v72, v66, v130
	v_and_b32_e32 v66, 0xffff0000, v148
	v_fmac_f32_e32 v66, v67, v131
	v_cvt_pk_bf16_f32 v72, v72, v66
	v_lshlrev_b32_e32 v66, 16, v149
	v_fmac_f32_e32 v66, v68, v132
	v_and_b32_e32 v67, 0xffff0000, v149
	v_fmac_f32_e32 v67, v69, v133
	v_cvt_pk_bf16_f32 v73, v66, v67
	global_store_dwordx4 v[74:75], v[70:73], off offset:256
	v_add_co_u32_e32 v66, vcc, s45, v172
	s_nop 1
	v_addc_co_u32_e32 v67, vcc, 0, v173, vcc
	global_load_dwordx4 v[70:73], v[66:67], off
	global_load_dwordx4 v[74:77], v[66:67], off offset:256
	v_add_co_u32_e32 v66, vcc, s46, v172
	s_waitcnt vmcnt(1)
	v_lshlrev_b32_e32 v98, 16, v70
	v_addc_co_u32_e32 v67, vcc, 0, v173, vcc
	global_load_dwordx4 v[78:81], v[66:67], off
	global_load_dwordx4 v[82:85], v[66:67], off offset:256
	v_add_co_u32_e32 v66, vcc, s47, v172
	v_fmac_f32_e32 v98, v62, v142
	s_nop 0
	v_addc_co_u32_e32 v67, vcc, 0, v173, vcc
	global_load_dwordx4 v[86:89], v[66:67], off
	global_load_dwordx4 v[90:93], v[66:67], off offset:256
	v_add_co_u32_e32 v66, vcc, s48, v172
	v_and_b32_e32 v62, 0xffff0000, v70
	s_nop 0
	v_addc_co_u32_e32 v67, vcc, 0, v173, vcc
	global_load_dwordx4 v[94:97], v[66:67], off
	s_nop 0
	global_load_dwordx4 v[66:69], v[66:67], off offset:256
	v_fmac_f32_e32 v62, v63, v143
	v_lshlrev_b32_e32 v63, 16, v71
	v_fmac_f32_e32 v63, v64, v144
	v_and_b32_e32 v64, 0xffff0000, v71
	v_fmac_f32_e32 v64, v65, v145
	v_cvt_pk_bf16_f32 v62, v98, v62
	v_cvt_pk_bf16_f32 v63, v63, v64
	v_lshlrev_b32_e32 v64, 16, v72
	v_fmac_f32_e32 v64, v58, v138
	v_and_b32_e32 v58, 0xffff0000, v72
	v_fmac_f32_e32 v58, v59, v139
	v_cvt_pk_bf16_f32 v64, v64, v58
	v_lshlrev_b32_e32 v58, 16, v73
	v_fmac_f32_e32 v58, v60, v140
	s_waitcnt vmcnt(6)
	v_lshlrev_b32_e32 v60, 16, v74
	v_fmac_f32_e32 v60, v54, v134
	v_and_b32_e32 v54, 0xffff0000, v74
	v_and_b32_e32 v59, 0xffff0000, v73
	v_fmac_f32_e32 v54, v55, v135
	v_lshlrev_b32_e32 v55, 16, v75
	v_fmac_f32_e32 v59, v61, v141
	v_cvt_pk_bf16_f32 v65, v58, v59
	v_add_co_u32_e32 v58, vcc, s45, v170
	v_fmac_f32_e32 v55, v56, v136
	v_and_b32_e32 v56, 0xffff0000, v75
	v_addc_co_u32_e32 v59, vcc, 0, v171, vcc
	v_fmac_f32_e32 v56, v57, v137
	global_store_dwordx4 v[58:59], v[62:65], off
	v_cvt_pk_bf16_f32 v54, v60, v54
	v_cvt_pk_bf16_f32 v55, v55, v56
	v_lshlrev_b32_e32 v56, 16, v76
	v_fmac_f32_e32 v56, v46, v130
	v_and_b32_e32 v46, 0xffff0000, v76
	v_fmac_f32_e32 v46, v47, v131
	v_cvt_pk_bf16_f32 v56, v56, v46
	v_lshlrev_b32_e32 v46, 16, v77
	v_and_b32_e32 v47, 0xffff0000, v77
	v_fmac_f32_e32 v46, v48, v132
	v_fmac_f32_e32 v47, v49, v133
	v_cvt_pk_bf16_f32 v57, v46, v47
	global_store_dwordx4 v[58:59], v[54:57], off offset:256
	s_waitcnt vmcnt(7)
; __device__ __forceinline__ unsigned cvt_pk_bf16(float lo, float hi) { unsigned r; asm volatile("v_cvt_pk_bf16_f32 %0, %1, %2" : "=v"(r) : "v"(lo), "v"(hi)); return r; }
; #define PG8_BAR __builtin_amdgcn_s_barrier()
;     __device__ __forceinline__ void operator()(const f32x4 (&acc)[2][2][4][2], const Unit& u, int wr, int wc, int fr, int fq) const {
;     ...
;                 for (int m = 0; m < 4; ++m)
; #pragma unroll
;                     for (int bj = 0; bj < 2; ++bj) { const u32x4 b = bs[m][bj]; const f32x4 a0 = acc[ai][bj][m][0], a1 = acc[ai][bj][m][1], g0 = gv[bj][0], g1 = gv[bj][1];
;                         u32x4 w;
;                         w.x = cvt_pk_bf16(__builtin_bit_cast(float, b.x << 16) + g0[0] * a0[0], __builtin_bit_cast(float, b.x & 0xffff0000u) + g0[1] * a0[1]);
;                         w.y = cvt_pk_bf16(__builtin_bit_cast(float, b.y << 16) + g0[2] * a0[2], __builtin_bit_cast(float, b.y & 0xffff0000u) + g0[3] * a0[3]);
;                         w.z = cvt_pk_bf16(__builtin_bit_cast(float, b.z << 16) + g1[0] * a1[0], __builtin_bit_cast(float, b.z & 0xffff0000u) + g1[1] * a1[1]);
;                         w.w = cvt_pk_bf16(__builtin_bit_cast(float, b.w << 16) + g1[2] * a1[2], __builtin_bit_cast(float, b.w & 0xffff0000u) + g1[3] * a1[3]);
;                         *(u32x4*)(op + (size_t)(ai * HALF + m * 16) * 2048 + bj * HALF) = w; }
; template <class Epi, class Sched, bool ALIGN_EPI = false, bool SP2 = false>
; __device__ __forceinline__ void gemm_phase(PG8_LAS unsigned char* lds, const Gemm g, const Sched& S, const Epi& E) {
;     ...
;         if (!has_next) break;
; #pragma unroll
;         for (int a = 0; a < 2; ++a)
; #pragma unroll
;             for (int b = 0; b < 2; ++b)
; #pragma unroll
;                 for (int m = 0; m < 4; ++m)
; #pragma unroll
;                     for (int n = 0; n < 2; ++n) acc[a][b][m][n] = (f32x4){0.f, 0.f, 0.f, 0.f};
;         cur = nxt; cA = nA; cB = nB; ++ui;
;         if constexpr (ALIGN_EPI) { if (wr == 1) PG8_BAR; }
	v_lshlrev_b32_e32 v46, 16, v78
	v_and_b32_e32 v47, 0xffff0000, v78
	v_fmac_f32_e32 v46, v50, v142
	v_fmac_f32_e32 v47, v51, v143
	v_cvt_pk_bf16_f32 v46, v46, v47
	v_lshlrev_b32_e32 v47, 16, v79
	v_and_b32_e32 v48, 0xffff0000, v79
	v_fmac_f32_e32 v47, v52, v144
	v_fmac_f32_e32 v48, v53, v145
	v_cvt_pk_bf16_f32 v47, v47, v48
	v_lshlrev_b32_e32 v48, 16, v80
	v_fmac_f32_e32 v48, v42, v138
	v_and_b32_e32 v42, 0xffff0000, v80
	v_fmac_f32_e32 v42, v43, v139
	v_cvt_pk_bf16_f32 v48, v48, v42
	v_lshlrev_b32_e32 v42, 16, v81
	v_fmac_f32_e32 v42, v44, v140
	s_waitcnt vmcnt(6)
	v_lshlrev_b32_e32 v44, 16, v82
	v_fmac_f32_e32 v44, v38, v134
	v_and_b32_e32 v38, 0xffff0000, v82
	v_and_b32_e32 v43, 0xffff0000, v81
	v_fmac_f32_e32 v38, v39, v135
	v_lshlrev_b32_e32 v39, 16, v83
	v_fmac_f32_e32 v43, v45, v141
	v_cvt_pk_bf16_f32 v49, v42, v43
	v_add_co_u32_e32 v42, vcc, s46, v170
	v_fmac_f32_e32 v39, v40, v136
	v_and_b32_e32 v40, 0xffff0000, v83
	v_addc_co_u32_e32 v43, vcc, 0, v171, vcc
	v_fmac_f32_e32 v40, v41, v137
	global_store_dwordx4 v[42:43], v[46:49], off
	v_cvt_pk_bf16_f32 v38, v44, v38
	v_cvt_pk_bf16_f32 v39, v39, v40
	v_lshlrev_b32_e32 v40, 16, v84
	v_fmac_f32_e32 v40, v30, v130
	v_and_b32_e32 v30, 0xffff0000, v84
	v_fmac_f32_e32 v30, v31, v131
	v_cvt_pk_bf16_f32 v40, v40, v30
	v_lshlrev_b32_e32 v30, 16, v85
	v_and_b32_e32 v31, 0xffff0000, v85
	v_fmac_f32_e32 v30, v32, v132
	v_fmac_f32_e32 v31, v33, v133
	v_cvt_pk_bf16_f32 v41, v30, v31
	s_waitcnt vmcnt(6)
	v_lshlrev_b32_e32 v30, 16, v86
	v_and_b32_e32 v31, 0xffff0000, v86
	v_fmac_f32_e32 v30, v34, v142
	v_fmac_f32_e32 v31, v35, v143
	global_store_dwordx4 v[42:43], v[38:41], off offset:256
	v_cvt_pk_bf16_f32 v30, v30, v31
	v_lshlrev_b32_e32 v31, 16, v87
	v_and_b32_e32 v32, 0xffff0000, v87
	v_fmac_f32_e32 v31, v36, v144
	v_fmac_f32_e32 v32, v37, v145
	v_cvt_pk_bf16_f32 v31, v31, v32
	v_lshlrev_b32_e32 v32, 16, v88
	v_fmac_f32_e32 v32, v26, v138
	v_and_b32_e32 v26, 0xffff0000, v88
	v_fmac_f32_e32 v26, v27, v139
	v_cvt_pk_bf16_f32 v32, v32, v26
	v_lshlrev_b32_e32 v26, 16, v89
	v_fmac_f32_e32 v26, v28, v140
	s_waitcnt vmcnt(6)
	v_lshlrev_b32_e32 v28, 16, v90
	v_fmac_f32_e32 v28, v22, v134
	v_and_b32_e32 v22, 0xffff0000, v90
	v_and_b32_e32 v27, 0xffff0000, v89
	v_fmac_f32_e32 v22, v23, v135
	v_lshlrev_b32_e32 v23, 16, v91
	v_fmac_f32_e32 v27, v29, v141
	v_cvt_pk_bf16_f32 v33, v26, v27
	v_add_co_u32_e32 v26, vcc, s47, v170
	v_fmac_f32_e32 v23, v24, v136
	v_and_b32_e32 v24, 0xffff0000, v91
	v_addc_co_u32_e32 v27, vcc, 0, v171, vcc
	v_fmac_f32_e32 v24, v25, v137
	global_store_dwordx4 v[26:27], v[30:33], off
	v_cvt_pk_bf16_f32 v22, v28, v22
	v_cvt_pk_bf16_f32 v23, v23, v24
	v_lshlrev_b32_e32 v24, 16, v92
	v_fmac_f32_e32 v24, v14, v130
	v_and_b32_e32 v14, 0xffff0000, v92
	v_fmac_f32_e32 v14, v15, v131
	v_cvt_pk_bf16_f32 v24, v24, v14
	v_lshlrev_b32_e32 v14, 16, v93
	v_and_b32_e32 v15, 0xffff0000, v93
	v_fmac_f32_e32 v14, v16, v132
	v_fmac_f32_e32 v15, v17, v133
	v_cvt_pk_bf16_f32 v25, v14, v15
	s_waitcnt vmcnt(6)
	v_lshlrev_b32_e32 v14, 16, v94
	v_and_b32_e32 v15, 0xffff0000, v94
	v_fmac_f32_e32 v14, v18, v142
	v_fmac_f32_e32 v15, v19, v143
	global_store_dwordx4 v[26:27], v[22:25], off offset:256
	v_cvt_pk_bf16_f32 v14, v14, v15
	v_lshlrev_b32_e32 v15, 16, v95
	v_and_b32_e32 v16, 0xffff0000, v95
	v_fmac_f32_e32 v15, v20, v144
	v_fmac_f32_e32 v16, v21, v145
	v_cvt_pk_bf16_f32 v15, v15, v16
	v_lshlrev_b32_e32 v16, 16, v96
	v_fmac_f32_e32 v16, v10, v138
	v_and_b32_e32 v10, 0xffff0000, v96
	v_fmac_f32_e32 v10, v11, v139
	v_cvt_pk_bf16_f32 v16, v16, v10
	v_lshlrev_b32_e32 v10, 16, v97
	v_fmac_f32_e32 v10, v12, v140
	s_waitcnt vmcnt(6)
	v_lshlrev_b32_e32 v12, 16, v66
	v_fmac_f32_e32 v12, v6, v134
	v_and_b32_e32 v6, 0xffff0000, v66
	v_and_b32_e32 v11, 0xffff0000, v97
	v_fmac_f32_e32 v6, v7, v135
	v_lshlrev_b32_e32 v7, 16, v67
	v_fmac_f32_e32 v11, v13, v141
	v_cvt_pk_bf16_f32 v17, v10, v11
	v_add_co_u32_e32 v10, vcc, s48, v170
	v_fmac_f32_e32 v7, v8, v136
	v_and_b32_e32 v8, 0xffff0000, v67
	v_addc_co_u32_e32 v11, vcc, 0, v171, vcc
	v_fmac_f32_e32 v8, v9, v137
	global_store_dwordx4 v[10:11], v[14:17], off
	v_cvt_pk_bf16_f32 v6, v12, v6
	v_cvt_pk_bf16_f32 v7, v7, v8
	v_lshlrev_b32_e32 v8, 16, v68
	v_fmac_f32_e32 v8, v2, v130
	v_and_b32_e32 v2, 0xffff0000, v68
	v_fmac_f32_e32 v2, v3, v131
	v_cvt_pk_bf16_f32 v8, v8, v2
	v_lshlrev_b32_e32 v2, 16, v69
	v_and_b32_e32 v3, 0xffff0000, v69
	v_fmac_f32_e32 v2, v4, v132
	v_fmac_f32_e32 v3, v5, v133
	v_cvt_pk_bf16_f32 v9, v2, v3
	global_store_dwordx4 v[10:11], v[6:9], off offset:256
	s_andn2_b64 vcc, exec, s[2:3]
	s_mov_b64 s[2:3], -1
	s_cbranch_vccnz .LBB0_1448
	s_andn2_b64 vcc, exec, s[4:5]
	s_cbranch_vccnz .LBB0_1447
	s_barrier
	s_branch .LBB0_1447

; #define PG8_STAGE(bufoff, gbase, voff) do { _Pragma("unroll") for (int _i = 0; _i < 2; ++_i) \
;         __builtin_amdgcn_global_load_lds((const unsigned*)((const char*)(gbase) + (voff)[_i]), (PG8_LAS unsigned*)(lds + (bufoff) + ldsw + _i * 8192), 16, 0, 0); } while (0)
; #define PG8_LDA(dst, b, h) do { _Pragma("unroll") for (int m = 0; m < 4; ++m) _Pragma("unroll") for (int k = 0; k < 2; ++k) dst[m][k] = *(const PG8_LAS bf16x8*)(lds + PG8_SA(b, h) + aoff + m * 2048 + k * 1024); } while (0)
; #define PG8_LDB(dst, b, h) do { _Pragma("unroll") for (int n = 0; n < 2; ++n) _Pragma("unroll") for (int k = 0; k < 2; ++k) dst[n][k] = *(const PG8_LAS bf16x8*)(lds + PG8_SB(b, h) + boff + n * 2048 + k * 1024); } while (0)
; #define PG8_WAIT_V(n) asm volatile("s_waitcnt vmcnt(" #n ")" ::: "memory")
; #define PG8_WAIT_L(n) asm volatile("s_waitcnt lgkmcnt(" #n ")" ::: "memory")
; #define PG8_BAR __builtin_amdgcn_s_barrier()
; #define PG8_SCHED __builtin_amdgcn_sched_barrier(0)
; template <class Epi, class Sched, bool ALIGN_EPI = false, bool SP2 = false>
; __device__ __forceinline__ void gemm_phase(PG8_LAS unsigned char* lds, const Gemm g, const Sched& S, const Epi& E) {
;     ...
;             const bool last = (t == nt - 2);
;             const char* a1 = cA + (size_t)(t + 1) * kstep;
;             const char* a2 = last ? nA : cA + (size_t)(t + 2) * kstep; const char* b2 = last ? nB : cB + (size_t)(t + 2) * kstep;
;             const char* a3 = a2 + kstep; const char* b3 = b2 + kstep;
;             if (last && has_next) S.a_ready(nxt);
;             if constexpr (SP2) {
;             PG8_LDB(B0, 0, 0); PG8_LDB(B1, 0, 1); PG8_SCHED; PG8_LDA(At, 0, 0); PG8_STAGE(PG8_SA(1, 1), a1 + hstep, voffA);
;             PG8_WAIT_V(8); PG8_WAIT_L(0); PG8_BAR; PG8_MMA(0, 0, At, B0); PG8_MMA(0, 1, At, B1); PG8_BAR; PG8_SCHED;
;             PG8_LDA(At, 0, 1); PG8_STAGE(PG8_SB(0, 0), b2, voffB); PG8_STAGE(PG8_SB(0, 1), b2 + hstep, voffB); PG8_STAGE(PG8_SA(0, 0), a2, voffA);
;             PG8_WAIT_V(8); PG8_WAIT_L(0); PG8_BAR; PG8_MMA(1, 0, At, B0); PG8_MMA(1, 1, At, B1); PG8_BAR; PG8_SCHED;
.LBB0_1883:
	ds_read_b128 v[26:29], v190
	ds_read_b128 v[30:33], v190 offset:1024
	ds_read_b128 v[18:21], v190 offset:2048
	ds_read_b128 v[22:25], v190 offset:3072
	ds_read_b128 v[10:13], v191
	ds_read_b128 v[14:17], v191 offset:1024
	ds_read_b128 v[2:5], v191 offset:2048
	ds_read_b128 v[6:9], v191 offset:3072
	s_add_u32 s28, s26, 0xfffc0080
	s_addc_u32 s29, s27, -1
	s_cmp_eq_u32 s53, 12
	s_cselect_b32 s31, s15, s29
	s_cselect_b32 s30, s49, s28
	s_cselect_b32 s29, s17, s52
	s_cselect_b32 s28, s50, s51
	s_add_i32 m0, s23, 0xc000
	ds_read_b128 v[176:179], v192
	ds_read_b128 v[180:183], v192 offset:1024
	ds_read_b128 v[194:197], v192 offset:2048
	ds_read_b128 v[198:201], v192 offset:3072
	ds_read_b128 v[202:205], v192 offset:4096
	ds_read_b128 v[206:209], v192 offset:5120
	ds_read_b128 v[214:217], v192 offset:6144
	ds_read_b128 v[218:221], v192 offset:7168
	global_load_lds_dwordx4 v170, s[26:27]
	s_add_i32 m0, s23, 0xe000
	s_nop 0
	global_load_lds_dwordx4 v172, s[26:27]
	s_waitcnt vmcnt(8)
	s_waitcnt lgkmcnt(0)
	s_barrier
	s_setprio 1
	s_waitcnt lgkmcnt(0)
	v_mfma_scale_f32_16x16x128_f8f6f4 v[158:161], v[26:33], v[176:183], v[158:161], v1, v184 op_sel_hi:[0,0,0]
	v_mfma_scale_f32_16x16x128_f8f6f4 v[154:157], v[18:25], v[176:183], v[154:157], v1, v184 op_sel_hi:[0,0,0]
	v_mfma_scale_f32_16x16x128_f8f6f4 v[142:145], v[26:33], v[194:201], v[142:145], v1, v184 op_sel_hi:[0,0,0]
	v_mfma_scale_f32_16x16x128_f8f6f4 v[138:141], v[18:25], v[194:201], v[138:141], v1, v184 op_sel_hi:[0,0,0]
	v_mfma_scale_f32_16x16x128_f8f6f4 v[126:129], v[26:33], v[202:209], v[126:129], v1, v184 op_sel_hi:[0,0,0]
	v_mfma_scale_f32_16x16x128_f8f6f4 v[122:125], v[18:25], v[202:209], v[122:125], v1, v184 op_sel_hi:[0,0,0]
	v_mfma_scale_f32_16x16x128_f8f6f4 v[110:113], v[26:33], v[214:221], v[110:113], v1, v184 op_sel_hi:[0,0,0]
	v_mfma_scale_f32_16x16x128_f8f6f4 v[106:109], v[18:25], v[214:221], v[106:109], v1, v184 op_sel_hi:[0,0,0]
	s_setprio 0
	s_setprio 1
	v_mfma_scale_f32_16x16x128_f8f6f4 v[150:153], v[10:17], v[176:183], v[150:153], v1, v184 op_sel_hi:[0,0,0]
	v_mfma_scale_f32_16x16x128_f8f6f4 v[146:149], v[2:9], v[176:183], v[146:149], v1, v184 op_sel_hi:[0,0,0]
	v_mfma_scale_f32_16x16x128_f8f6f4 v[134:137], v[10:17], v[194:201], v[134:137], v1, v184 op_sel_hi:[0,0,0]
	v_mfma_scale_f32_16x16x128_f8f6f4 v[130:133], v[2:9], v[194:201], v[130:133], v1, v184 op_sel_hi:[0,0,0]
	v_mfma_scale_f32_16x16x128_f8f6f4 v[118:121], v[10:17], v[202:209], v[118:121], v1, v184 op_sel_hi:[0,0,0]
	v_mfma_scale_f32_16x16x128_f8f6f4 v[114:117], v[2:9], v[202:209], v[114:117], v1, v184 op_sel_hi:[0,0,0]
	v_mfma_scale_f32_16x16x128_f8f6f4 v[102:105], v[10:17], v[214:221], v[102:105], v1, v184 op_sel_hi:[0,0,0]
	v_mfma_scale_f32_16x16x128_f8f6f4 v[98:101], v[2:9], v[214:221], v[98:101], v1, v184 op_sel_hi:[0,0,0]
	s_setprio 0
	s_barrier
	s_add_i32 s54, s45, s35
	s_mov_b32 m0, s54
	ds_read_b128 v[194:197], v192 offset:16384
	ds_read_b128 v[198:201], v192 offset:17408
	ds_read_b128 v[202:205], v192 offset:18432
	ds_read_b128 v[206:209], v192 offset:19456
	ds_read_b128 v[214:217], v192 offset:20480
	ds_read_b128 v[218:221], v192 offset:21504
	ds_read_b128 v[222:225], v192 offset:22528
	ds_read_b128 v[226:229], v192 offset:23552
	global_load_lds_dwordx4 v166, s[28:29]
	s_add_i32 m0, s54, 0x2000
	s_add_u32 s54, s28, 0x40000
	s_addc_u32 s55, s29, 0
	s_add_i32 s56, s46, s35
	global_load_lds_dwordx4 v162, s[28:29]
	s_mov_b32 m0, s56
	s_nop 0
	global_load_lds_dwordx4 v166, s[54:55]
	s_add_i32 m0, s56, 0x2000
	s_nop 0
	global_load_lds_dwordx4 v162, s[54:55]
	s_mov_b32 m0, s23
	s_nop 0
	global_load_lds_dwordx4 v168, s[30:31]
	s_mov_b32 m0, s25
	s_nop 0
	global_load_lds_dwordx4 v164, s[30:31]
	s_waitcnt vmcnt(8)
	s_waitcnt lgkmcnt(0)
	s_barrier
	s_setprio 1
	s_waitcnt lgkmcnt(0)
	v_mfma_scale_f32_16x16x128_f8f6f4 v[94:97], v[26:33], v[194:201], v[94:97], v1, v184 op_sel_hi:[0,0,0]
	v_mfma_scale_f32_16x16x128_f8f6f4 v[90:93], v[18:25], v[194:201], v[90:93], v1, v184 op_sel_hi:[0,0,0]
	v_mfma_scale_f32_16x16x128_f8f6f4 v[78:81], v[26:33], v[202:209], v[78:81], v1, v184 op_sel_hi:[0,0,0]
	v_mfma_scale_f32_16x16x128_f8f6f4 v[74:77], v[18:25], v[202:209], v[74:77], v1, v184 op_sel_hi:[0,0,0]
	v_mfma_scale_f32_16x16x128_f8f6f4 v[62:65], v[26:33], v[214:221], v[62:65], v1, v184 op_sel_hi:[0,0,0]
	v_mfma_scale_f32_16x16x128_f8f6f4 v[58:61], v[18:25], v[214:221], v[58:61], v1, v184 op_sel_hi:[0,0,0]
	v_mfma_scale_f32_16x16x128_f8f6f4 v[46:49], v[26:33], v[222:229], v[46:49], v1, v184 op_sel_hi:[0,0,0]
	v_mfma_scale_f32_16x16x128_f8f6f4 v[42:45], v[18:25], v[222:229], v[42:45], v1, v184 op_sel_hi:[0,0,0]
	s_setprio 0
	s_setprio 1
	v_mfma_scale_f32_16x16x128_f8f6f4 v[86:89], v[10:17], v[194:201], v[86:89], v1, v184 op_sel_hi:[0,0,0]
	v_mfma_scale_f32_16x16x128_f8f6f4 v[82:85], v[2:9], v[194:201], v[82:85], v1, v184 op_sel_hi:[0,0,0]
	v_mfma_scale_f32_16x16x128_f8f6f4 v[70:73], v[10:17], v[202:209], v[70:73], v1, v184 op_sel_hi:[0,0,0]
	v_mfma_scale_f32_16x16x128_f8f6f4 v[66:69], v[2:9], v[202:209], v[66:69], v1, v184 op_sel_hi:[0,0,0]
	v_mfma_scale_f32_16x16x128_f8f6f4 v[54:57], v[10:17], v[214:221], v[54:57], v1, v184 op_sel_hi:[0,0,0]
	v_mfma_scale_f32_16x16x128_f8f6f4 v[50:53], v[2:9], v[214:221], v[50:53], v1, v184 op_sel_hi:[0,0,0]
	v_mfma_scale_f32_16x16x128_f8f6f4 v[38:41], v[10:17], v[222:229], v[38:41], v1, v184 op_sel_hi:[0,0,0]
	v_mfma_scale_f32_16x16x128_f8f6f4 v[34:37], v[2:9], v[222:229], v[34:37], v1, v184 op_sel_hi:[0,0,0]
	s_setprio 0
	s_barrier
; #define PG8_STAGE(bufoff, gbase, voff) do { _Pragma("unroll") for (int _i = 0; _i < 2; ++_i) \
;         __builtin_amdgcn_global_load_lds((const unsigned*)((const char*)(gbase) + (voff)[_i]), (PG8_LAS unsigned*)(lds + (bufoff) + ldsw + _i * 8192), 16, 0, 0); } while (0)
; #define PG8_LDA(dst, b, h) do { _Pragma("unroll") for (int m = 0; m < 4; ++m) _Pragma("unroll") for (int k = 0; k < 2; ++k) dst[m][k] = *(const PG8_LAS bf16x8*)(lds + PG8_SA(b, h) + aoff + m * 2048 + k * 1024); } while (0)
; #define PG8_LDB(dst, b, h) do { _Pragma("unroll") for (int n = 0; n < 2; ++n) _Pragma("unroll") for (int k = 0; k < 2; ++k) dst[n][k] = *(const PG8_LAS bf16x8*)(lds + PG8_SB(b, h) + boff + n * 2048 + k * 1024); } while (0)
; template <class Epi, class Sched, bool ALIGN_EPI = false, bool SP2 = false>
; __device__ __forceinline__ void gemm_phase(PG8_LAS unsigned char* lds, const Gemm g, const Sched& S, const Epi& E) {
;     ...
;         for (int t = 0; t < nt; t += 2) {
;             const bool last = (t == nt - 2);
;             const char* a1 = cA + (size_t)(t + 1) * kstep;
;             const char* a2 = last ? nA : cA + (size_t)(t + 2) * kstep; const char* b2 = last ? nB : cB + (size_t)(t + 2) * kstep;
;             const char* a3 = a2 + kstep; const char* b3 = b2 + kstep;
;             if (last && has_next) S.a_ready(nxt);
;             if constexpr (SP2) {
;             PG8_LDB(B0, 0, 0); PG8_LDB(B1, 0, 1); PG8_SCHED; PG8_LDA(At, 0, 0); PG8_STAGE(PG8_SA(1, 1), a1 + hstep, voffA);
;             PG8_WAIT_V(8); PG8_WAIT_L(0); PG8_BAR; PG8_MMA(0, 0, At, B0); PG8_MMA(0, 1, At, B1); PG8_BAR; PG8_SCHED;
;             PG8_LDA(At, 0, 1); PG8_STAGE(PG8_SB(0, 0), b2, voffB); PG8_STAGE(PG8_SB(0, 1), b2 + hstep, voffB); PG8_STAGE(PG8_SA(0, 0), a2, voffA);
;             PG8_WAIT_V(8); PG8_WAIT_L(0); PG8_BAR; PG8_MMA(1, 0, At, B0); PG8_MMA(1, 1, At, B1); PG8_BAR; PG8_SCHED;
;             PG8_LDB(B0, 1, 0); PG8_LDB(B1, 1, 1); PG8_SCHED; PG8_LDA(At, 1, 0); PG8_STAGE(PG8_SA(0, 1), a2 + hstep, voffA);
;             PG8_WAIT_V(8); PG8_WAIT_L(0); PG8_BAR; PG8_MMA(0, 0, At, B0); PG8_MMA(0, 1, At, B1); PG8_BAR; PG8_SCHED;
;             PG8_LDA(At, 1, 1); PG8_STAGE(PG8_SB(1, 0), b3, voffB); PG8_STAGE(PG8_SB(1, 1), b3 + hstep, voffB); PG8_STAGE(PG8_SA(1, 0), a3, voffA);
;             PG8_WAIT_V(8); PG8_WAIT_L(0); PG8_BAR; PG8_MMA(1, 0, At, B0); PG8_MMA(1, 1, At, B1); PG8_BAR; PG8_SCHED;
	s_add_i32 s54, 0, 0x18000
	s_add_i32 s55, 0, 0x1c000
	ds_read_b128 v[2:5], v248
	ds_read_b128 v[6:9], v248 offset:1024
	ds_read_b128 v[10:13], v248 offset:2048
	ds_read_b128 v[14:17], v248 offset:3072
	ds_read_b128 v[18:21], v249
	ds_read_b128 v[22:25], v249 offset:1024
	ds_read_b128 v[26:29], v249 offset:2048
	ds_read_b128 v[30:33], v249 offset:3072
	s_add_u32 s30, s30, 0x40000
	s_addc_u32 s31, s31, 0
	s_mov_b32 m0, s39
	ds_read_b128 v[194:197], v192 offset:32768
	ds_read_b128 v[198:201], v192 offset:33792
	ds_read_b128 v[202:205], v192 offset:34816
	ds_read_b128 v[206:209], v192 offset:35840
	ds_read_b128 v[214:217], v192 offset:36864
	ds_read_b128 v[218:221], v192 offset:37888
	ds_read_b128 v[222:225], v192 offset:38912
	ds_read_b128 v[226:229], v192 offset:39936
	global_load_lds_dwordx4 v168, s[30:31]
	s_mov_b32 m0, s40
	s_nop 0
	global_load_lds_dwordx4 v164, s[30:31]
	s_waitcnt vmcnt(8)
	s_waitcnt lgkmcnt(0)
	s_barrier
	s_setprio 1
	s_waitcnt lgkmcnt(0)
	v_mfma_scale_f32_16x16x128_f8f6f4 v[158:161], v[2:9], v[194:201], v[158:161], v1, v184 op_sel_hi:[0,0,0]
	v_mfma_scale_f32_16x16x128_f8f6f4 v[154:157], v[10:17], v[194:201], v[154:157], v1, v184 op_sel_hi:[0,0,0]
	v_mfma_scale_f32_16x16x128_f8f6f4 v[142:145], v[2:9], v[202:209], v[142:145], v1, v184 op_sel_hi:[0,0,0]
	v_mfma_scale_f32_16x16x128_f8f6f4 v[138:141], v[10:17], v[202:209], v[138:141], v1, v184 op_sel_hi:[0,0,0]
	v_mfma_scale_f32_16x16x128_f8f6f4 v[126:129], v[2:9], v[214:221], v[126:129], v1, v184 op_sel_hi:[0,0,0]
	v_mfma_scale_f32_16x16x128_f8f6f4 v[122:125], v[10:17], v[214:221], v[122:125], v1, v184 op_sel_hi:[0,0,0]
	v_mfma_scale_f32_16x16x128_f8f6f4 v[110:113], v[2:9], v[222:229], v[110:113], v1, v184 op_sel_hi:[0,0,0]
	v_mfma_scale_f32_16x16x128_f8f6f4 v[106:109], v[10:17], v[222:229], v[106:109], v1, v184 op_sel_hi:[0,0,0]
	s_setprio 0
	s_setprio 1
	v_mfma_scale_f32_16x16x128_f8f6f4 v[150:153], v[18:25], v[194:201], v[150:153], v1, v184 op_sel_hi:[0,0,0]
	v_mfma_scale_f32_16x16x128_f8f6f4 v[146:149], v[26:33], v[194:201], v[146:149], v1, v184 op_sel_hi:[0,0,0]
	v_mfma_scale_f32_16x16x128_f8f6f4 v[134:137], v[18:25], v[202:209], v[134:137], v1, v184 op_sel_hi:[0,0,0]
	v_mfma_scale_f32_16x16x128_f8f6f4 v[130:133], v[26:33], v[202:209], v[130:133], v1, v184 op_sel_hi:[0,0,0]
	v_mfma_scale_f32_16x16x128_f8f6f4 v[118:121], v[18:25], v[214:221], v[118:121], v1, v184 op_sel_hi:[0,0,0]
	v_mfma_scale_f32_16x16x128_f8f6f4 v[114:117], v[26:33], v[214:221], v[114:117], v1, v184 op_sel_hi:[0,0,0]
	v_mfma_scale_f32_16x16x128_f8f6f4 v[102:105], v[18:25], v[222:229], v[102:105], v1, v184 op_sel_hi:[0,0,0]
	v_mfma_scale_f32_16x16x128_f8f6f4 v[98:101], v[26:33], v[222:229], v[98:101], v1, v184 op_sel_hi:[0,0,0]
	s_setprio 0
	s_barrier
	s_add_u32 s98, s28, 0x80
	s_addc_u32 s99, s29, 0
	s_add_u32 s100, s30, 0xfffc0080
	s_addc_u32 s101, s31, -1
	s_add_i32 s30, s54, s35
	s_mov_b32 m0, s30
	ds_read_b128 v[194:197], v192 offset:49152
	ds_read_b128 v[198:201], v192 offset:50176
	ds_read_b128 v[202:205], v192 offset:51200
	ds_read_b128 v[206:209], v192 offset:52224
	ds_read_b128 v[214:217], v192 offset:53248
	ds_read_b128 v[218:221], v192 offset:54272
	ds_read_b128 v[222:225], v192 offset:55296
	ds_read_b128 v[226:229], v192 offset:56320
	global_load_lds_dwordx4 v166, s[98:99]
	s_add_i32 m0, s30, 0x2000
	s_add_u32 s28, s28, 0x40080
	s_addc_u32 s29, s29, 0
	s_add_i32 s30, s55, s35
	global_load_lds_dwordx4 v162, s[98:99]
	s_mov_b32 m0, s30
	s_nop 0
	global_load_lds_dwordx4 v166, s[28:29]
	s_add_i32 m0, s30, 0x2000
	s_nop 0
	global_load_lds_dwordx4 v162, s[28:29]
	s_mov_b32 m0, s41
	s_nop 0
	global_load_lds_dwordx4 v168, s[100:101]
	s_mov_b32 m0, s42
	s_nop 0
	global_load_lds_dwordx4 v164, s[100:101]
	s_waitcnt vmcnt(8)
	s_waitcnt lgkmcnt(0)
	s_barrier
	s_setprio 1
	s_waitcnt lgkmcnt(0)
	v_mfma_scale_f32_16x16x128_f8f6f4 v[94:97], v[2:9], v[194:201], v[94:97], v1, v184 op_sel_hi:[0,0,0]
	v_mfma_scale_f32_16x16x128_f8f6f4 v[90:93], v[10:17], v[194:201], v[90:93], v1, v184 op_sel_hi:[0,0,0]
	v_mfma_scale_f32_16x16x128_f8f6f4 v[78:81], v[2:9], v[202:209], v[78:81], v1, v184 op_sel_hi:[0,0,0]
	v_mfma_scale_f32_16x16x128_f8f6f4 v[74:77], v[10:17], v[202:209], v[74:77], v1, v184 op_sel_hi:[0,0,0]
	v_mfma_scale_f32_16x16x128_f8f6f4 v[62:65], v[2:9], v[214:221], v[62:65], v1, v184 op_sel_hi:[0,0,0]
	v_mfma_scale_f32_16x16x128_f8f6f4 v[58:61], v[10:17], v[214:221], v[58:61], v1, v184 op_sel_hi:[0,0,0]
	v_mfma_scale_f32_16x16x128_f8f6f4 v[46:49], v[2:9], v[222:229], v[46:49], v1, v184 op_sel_hi:[0,0,0]
	v_mfma_scale_f32_16x16x128_f8f6f4 v[42:45], v[10:17], v[222:229], v[42:45], v1, v184 op_sel_hi:[0,0,0]
	s_setprio 0
	s_setprio 1
	v_mfma_scale_f32_16x16x128_f8f6f4 v[86:89], v[18:25], v[194:201], v[86:89], v1, v184 op_sel_hi:[0,0,0]
	v_mfma_scale_f32_16x16x128_f8f6f4 v[82:85], v[26:33], v[194:201], v[82:85], v1, v184 op_sel_hi:[0,0,0]
	v_mfma_scale_f32_16x16x128_f8f6f4 v[70:73], v[18:25], v[202:209], v[70:73], v1, v184 op_sel_hi:[0,0,0]
	v_mfma_scale_f32_16x16x128_f8f6f4 v[66:69], v[26:33], v[202:209], v[66:69], v1, v184 op_sel_hi:[0,0,0]
	v_mfma_scale_f32_16x16x128_f8f6f4 v[54:57], v[18:25], v[214:221], v[54:57], v1, v184 op_sel_hi:[0,0,0]
	v_mfma_scale_f32_16x16x128_f8f6f4 v[50:53], v[26:33], v[214:221], v[50:53], v1, v184 op_sel_hi:[0,0,0]
	v_mfma_scale_f32_16x16x128_f8f6f4 v[38:41], v[18:25], v[222:229], v[38:41], v1, v184 op_sel_hi:[0,0,0]
	v_mfma_scale_f32_16x16x128_f8f6f4 v[34:37], v[26:33], v[222:229], v[34:37], v1, v184 op_sel_hi:[0,0,0]
	s_setprio 0
	s_barrier
	s_add_i32 s53, s53, 2
	s_add_u32 s26, s26, 0x100
	s_addc_u32 s27, s27, 0
	s_add_u32 s51, s51, 0x100
	s_addc_u32 s52, s52, 0
	s_cmp_gt_u32 s53, 13
	s_cbranch_scc0 .LBB0_1883
; __device__ __forceinline__ float fast_silu(float g) { return g * __builtin_amdgcn_rcpf(1.0f + __expf(-g)); }
; __device__ __forceinline__ float clamp448(float x) { return __builtin_amdgcn_fmed3f(x, -448.f, 448.f); }
; __device__ __forceinline__ unsigned pk4_fp8(float a, float b, float c, float d) { int w = 0; w = __builtin_amdgcn_cvt_pk_fp8_f32(clamp448(a), clamp448(b), w, false); w = __builtin_amdgcn_cvt_pk_fp8_f32(clamp448(c), clamp448(d), w, true); return (unsigned)w; }
; __device__ __forceinline__ f32x4_e silu_mul4(f32x4_e g, f32x4_e u) {
;     const f32x4_e t = g * -1.44269504088896341f;
;     f32x4_e e; e[0] = __builtin_amdgcn_exp2f(t[0]); e[1] = __builtin_amdgcn_exp2f(t[1]); e[2] = __builtin_amdgcn_exp2f(t[2]); e[3] = __builtin_amdgcn_exp2f(t[3]);
;     const f32x4_e d = e + 1.0f;
;     f32x4_e r; r[0] = __builtin_amdgcn_rcpf(d[0]); r[1] = __builtin_amdgcn_rcpf(d[1]); r[2] = __builtin_amdgcn_rcpf(d[2]); r[3] = __builtin_amdgcn_rcpf(d[3]);
;     return (g * r) * u;
; }
;     __device__ __forceinline__ void operator()(const f32x4 (&acc)[2][2][4][2], const Unit& u, int wr, int wc, int fr, int fq) const {
;         const int row0 = u.pm * BM + wr * 64 + fr, col0 = (u.pn % nN) * HALF + wc * 32 + 8 * fq;
; #pragma unroll
;         for (int ai = 0; ai < 2; ++ai)
; #pragma unroll
;             for (int m = 0; m < 4; ++m) { unsigned char* rowp = O + (size_t)(row0 + ai * HALF + m * 16) * ldc + col0;
;                 f32x4 g0 = acc[ai][0][m][0], g1 = acc[ai][0][m][1], u0 = acc[ai][1][m][0], u1 = acc[ai][1][m][1];
;                 if (PROBE_REPEAT == 300) {
; #pragma unroll
;                     for (int q = 0; q < 4; ++q) { float t0 = fast_silu(g0[q] + 1.0f) * u0[q], t1 = fast_silu(g1[q] + 1.0f) * u1[q]; asm volatile("" : "+v"(t0), "+v"(t1)); u0[q] += 0.0f * clamp448(t0); u1[q] += 0.0f * clamp448(t1); } }
;                 const f32x4 h0 = silu_mul4(g0, u0), h1 = silu_mul4(g1, u1);
;                 u32x2 w; w.x = pk4_fp8(h0[0], h0[1], h0[2], h0[3]); w.y = pk4_fp8(h1[0], h1[1], h1[2], h1[3]);
;                 *(u32x2*)(rowp) = w; }
	v_pk_mul_f32 v[10:11], v[158:159], s[12:13] op_sel_hi:[1,0]
	v_pk_mul_f32 v[8:9], v[160:161], s[12:13] op_sel_hi:[1,0]
	v_exp_f32_e32 v10, v10
	v_exp_f32_e32 v11, v11
	v_pk_mul_f32 v[16:17], v[154:155], s[12:13] op_sel_hi:[1,0]
	v_exp_f32_e32 v8, v8
	v_exp_f32_e32 v9, v9
	v_exp_f32_e32 v16, v16
	v_exp_f32_e32 v17, v17
	v_pk_add_f32 v[10:11], v[10:11], 1.0 op_sel_hi:[1,0]
	v_pk_mul_f32 v[14:15], v[156:157], s[12:13] op_sel_hi:[1,0]
	v_pk_add_f32 v[8:9], v[8:9], 1.0 op_sel_hi:[1,0]
	v_rcp_f32_e32 v10, v10
	v_rcp_f32_e32 v11, v11
	v_exp_f32_e32 v14, v14
	v_exp_f32_e32 v15, v15
	v_pk_add_f32 v[16:17], v[16:17], 1.0 op_sel_hi:[1,0]
	v_rcp_f32_e32 v8, v8
	v_rcp_f32_e32 v9, v9
	v_rcp_f32_e32 v16, v16
	v_rcp_f32_e32 v17, v17
	v_pk_mul_f32 v[10:11], v[158:159], v[10:11]
	v_pk_add_f32 v[14:15], v[14:15], 1.0 op_sel_hi:[1,0]
	v_pk_mul_f32 v[8:9], v[160:161], v[8:9]
	v_rcp_f32_e32 v14, v14
	v_rcp_f32_e32 v15, v15
	v_pk_mul_f32 v[10:11], v[150:151], v[10:11]
	v_pk_mul_f32 v[16:17], v[154:155], v[16:17]
	v_pk_mul_f32 v[8:9], v[152:153], v[8:9]
	v_pk_mul_f32 v[16:17], v[146:147], v[16:17]
	v_med3_f32 v7, v10, s48, v193
	v_med3_f32 v11, v11, s48, v193
	v_mov_b32_e32 v10, 0
	s_mul_hi_i32 s15, s24, 0x92492493
	v_cvt_pk_fp8_f32 v10, v7, v11
	v_med3_f32 v7, v8, s48, v193
	v_med3_f32 v8, v9, s48, v193
	v_med3_f32 v9, v16, s48, v193
	v_med3_f32 v16, v17, s48, v193
	v_mov_b32_e32 v11, 0
	s_add_i32 s15, s15, s24
	v_cvt_pk_fp8_f32 v11, v9, v16
	s_lshr_b32 s17, s15, 31
	s_lshr_b32 s15, s15, 5
	v_pk_mul_f32 v[14:15], v[156:157], v[14:15]
	s_add_i32 s15, s15, s17
	v_pk_mul_f32 v[14:15], v[148:149], v[14:15]
	s_mul_i32 s15, s15, 56
	v_readlane_b32 s26, v247, 13
	v_cvt_pk_fp8_f32 v10, v7, v8 op_sel:[0,0,1]
	v_med3_f32 v7, v14, s48, v193
	v_med3_f32 v8, v15, s48, v193
	v_pk_mul_f32 v[14:15], v[142:143], s[12:13] op_sel_hi:[1,0]
	s_sub_i32 s15, s24, s15
	v_readlane_b32 s27, v247, 14
	v_cvt_pk_fp8_f32 v11, v7, v8 op_sel:[0,0,1]
	v_exp_f32_e32 v14, v14
	v_exp_f32_e32 v15, v15
	v_lshl_add_u32 v6, s22, 8, v185
	v_lshl_or_b32 v2, s15, 7, v189
	v_mov_b64_e32 v[4:5], s[26:27]
	v_ashrrev_i32_e32 v3, 31, v2
	v_mad_i64_i32 v[12:13], s[26:27], v6, s47, v[4:5]
	v_lshl_add_u64 v[12:13], v[12:13], 0, v[2:3]
	global_store_dwordx2 v[12:13], v[10:11], off
	v_pk_add_f32 v[10:11], v[14:15], 1.0 op_sel_hi:[1,0]
	v_pk_mul_f32 v[14:15], v[138:139], s[12:13] op_sel_hi:[1,0]
	v_pk_mul_f32 v[8:9], v[144:145], s[12:13] op_sel_hi:[1,0]
	v_exp_f32_e32 v14, v14
	v_exp_f32_e32 v15, v15
	v_exp_f32_e32 v8, v8
	v_exp_f32_e32 v9, v9
	v_pk_mul_f32 v[12:13], v[140:141], s[12:13] op_sel_hi:[1,0]
	v_rcp_f32_e32 v10, v10
	v_rcp_f32_e32 v11, v11
	v_exp_f32_e32 v12, v12
	v_exp_f32_e32 v13, v13
	v_pk_add_f32 v[14:15], v[14:15], 1.0 op_sel_hi:[1,0]
	v_pk_add_f32 v[8:9], v[8:9], 1.0 op_sel_hi:[1,0]
	v_rcp_f32_e32 v14, v14
	v_rcp_f32_e32 v15, v15
	v_rcp_f32_e32 v8, v8
	v_rcp_f32_e32 v9, v9
	v_pk_mul_f32 v[10:11], v[142:143], v[10:11]
	v_pk_add_f32 v[12:13], v[12:13], 1.0 op_sel_hi:[1,0]
	v_pk_mul_f32 v[10:11], v[134:135], v[10:11]
	v_rcp_f32_e32 v12, v12
	v_rcp_f32_e32 v13, v13
	v_pk_mul_f32 v[14:15], v[138:139], v[14:15]
	v_med3_f32 v16, v10, s48, v193
	v_pk_mul_f32 v[14:15], v[130:131], v[14:15]
	v_med3_f32 v11, v11, s48, v193
	v_mov_b32_e32 v10, 0
	v_cvt_pk_fp8_f32 v10, v16, v11
	v_med3_f32 v14, v14, s48, v193
	v_med3_f32 v15, v15, s48, v193
	v_mov_b32_e32 v11, 0
	v_pk_mul_f32 v[8:9], v[144:145], v[8:9]
	v_cvt_pk_fp8_f32 v11, v14, v15
	v_pk_mul_f32 v[8:9], v[136:137], v[8:9]
	v_pk_mul_f32 v[12:13], v[140:141], v[12:13]
	v_med3_f32 v8, v8, s48, v193
	v_pk_mul_f32 v[12:13], v[132:133], v[12:13]
	v_med3_f32 v9, v9, s48, v193
	v_cvt_pk_fp8_f32 v10, v8, v9 op_sel:[0,0,1]
	v_med3_f32 v8, v12, s48, v193
	v_med3_f32 v9, v13, s48, v193
	v_cvt_pk_fp8_f32 v11, v8, v9 op_sel:[0,0,1]
	v_or_b32_e32 v7, 16, v6
	v_mad_i64_i32 v[8:9], s[26:27], v7, s47, v[4:5]
	v_lshl_add_u64 v[8:9], v[8:9], 0, v[2:3]
	global_store_dwordx2 v[8:9], v[10:11], off
	s_and_b64 vcc, exec, s[10:11]
	s_cbranch_vccz .LBB0_1886
	s_barrier
.LBB0_1886:
	v_pk_mul_f32 v[10:11], v[126:127], s[12:13] op_sel_hi:[1,0]
	v_pk_mul_f32 v[8:9], v[128:129], s[12:13] op_sel_hi:[1,0]
	v_exp_f32_e32 v10, v10
	v_exp_f32_e32 v11, v11
	v_pk_mul_f32 v[16:17], v[122:123], s[12:13] op_sel_hi:[1,0]
	v_exp_f32_e32 v8, v8
	v_exp_f32_e32 v9, v9
	v_exp_f32_e32 v16, v16
	v_exp_f32_e32 v17, v17
	v_pk_add_f32 v[10:11], v[10:11], 1.0 op_sel_hi:[1,0]
	v_pk_mul_f32 v[14:15], v[124:125], s[12:13] op_sel_hi:[1,0]
	v_pk_add_f32 v[8:9], v[8:9], 1.0 op_sel_hi:[1,0]
	v_rcp_f32_e32 v10, v10
	v_rcp_f32_e32 v11, v11
	v_exp_f32_e32 v14, v14
	v_exp_f32_e32 v15, v15
	v_pk_add_f32 v[16:17], v[16:17], 1.0 op_sel_hi:[1,0]
	v_rcp_f32_e32 v8, v8
	v_rcp_f32_e32 v9, v9
	v_rcp_f32_e32 v16, v16
	v_rcp_f32_e32 v17, v17
	v_pk_mul_f32 v[10:11], v[126:127], v[10:11]
	v_pk_add_f32 v[14:15], v[14:15], 1.0 op_sel_hi:[1,0]
	v_or_b32_e32 v7, 32, v6
	v_pk_mul_f32 v[8:9], v[128:129], v[8:9]
	v_rcp_f32_e32 v14, v14
	v_rcp_f32_e32 v15, v15
	v_pk_mul_f32 v[10:11], v[118:119], v[10:11]
	v_pk_mul_f32 v[16:17], v[122:123], v[16:17]
	v_mad_i64_i32 v[12:13], s[26:27], v7, s47, v[4:5]
	v_pk_mul_f32 v[8:9], v[120:121], v[8:9]
	v_pk_mul_f32 v[16:17], v[114:115], v[16:17]
	v_med3_f32 v7, v10, s48, v193
	v_med3_f32 v11, v11, s48, v193
	v_mov_b32_e32 v10, 0
	v_cvt_pk_fp8_f32 v10, v7, v11
	v_med3_f32 v7, v8, s48, v193
	v_med3_f32 v8, v9, s48, v193
	v_med3_f32 v9, v16, s48, v193
	v_med3_f32 v16, v17, s48, v193
	v_mov_b32_e32 v11, 0
	v_cvt_pk_fp8_f32 v11, v9, v16
	v_pk_mul_f32 v[14:15], v[124:125], v[14:15]
	v_cvt_pk_fp8_f32 v10, v7, v8 op_sel:[0,0,1]
	v_pk_mul_f32 v[14:15], v[116:117], v[14:15]
	v_lshl_add_u64 v[12:13], v[12:13], 0, v[2:3]
; __device__ __forceinline__ float fast_silu(float g) { return g * __builtin_amdgcn_rcpf(1.0f + __expf(-g)); }
; __device__ __forceinline__ float clamp448(float x) { return __builtin_amdgcn_fmed3f(x, -448.f, 448.f); }
; __device__ __forceinline__ unsigned pk4_fp8(float a, float b, float c, float d) { int w = 0; w = __builtin_amdgcn_cvt_pk_fp8_f32(clamp448(a), clamp448(b), w, false); w = __builtin_amdgcn_cvt_pk_fp8_f32(clamp448(c), clamp448(d), w, true); return (unsigned)w; }
; __device__ __forceinline__ f32x4_e silu_mul4(f32x4_e g, f32x4_e u) {
;     const f32x4_e t = g * -1.44269504088896341f;
;     f32x4_e e; e[0] = __builtin_amdgcn_exp2f(t[0]); e[1] = __builtin_amdgcn_exp2f(t[1]); e[2] = __builtin_amdgcn_exp2f(t[2]); e[3] = __builtin_amdgcn_exp2f(t[3]);
;     const f32x4_e d = e + 1.0f;
;     f32x4_e r; r[0] = __builtin_amdgcn_rcpf(d[0]); r[1] = __builtin_amdgcn_rcpf(d[1]); r[2] = __builtin_amdgcn_rcpf(d[2]); r[3] = __builtin_amdgcn_rcpf(d[3]);
;     return (g * r) * u;
; }
;     __device__ __forceinline__ void operator()(const f32x4 (&acc)[2][2][4][2], const Unit& u, int wr, int wc, int fr, int fq) const {
;     ...
;         for (int ai = 0; ai < 2; ++ai)
; #pragma unroll
;             for (int m = 0; m < 4; ++m) { unsigned char* rowp = O + (size_t)(row0 + ai * HALF + m * 16) * ldc + col0;
;                 f32x4 g0 = acc[ai][0][m][0], g1 = acc[ai][0][m][1], u0 = acc[ai][1][m][0], u1 = acc[ai][1][m][1];
;                 if (PROBE_REPEAT == 300) {
; #pragma unroll
;                     for (int q = 0; q < 4; ++q) { float t0 = fast_silu(g0[q] + 1.0f) * u0[q], t1 = fast_silu(g1[q] + 1.0f) * u1[q]; asm volatile("" : "+v"(t0), "+v"(t1)); u0[q] += 0.0f * clamp448(t0); u1[q] += 0.0f * clamp448(t1); } }
;                 const f32x4 h0 = silu_mul4(g0, u0), h1 = silu_mul4(g1, u1);
;                 u32x2 w; w.x = pk4_fp8(h0[0], h0[1], h0[2], h0[3]); w.y = pk4_fp8(h1[0], h1[1], h1[2], h1[3]);
;                 *(u32x2*)(rowp) = w; }
	v_med3_f32 v7, v14, s48, v193
	v_med3_f32 v8, v15, s48, v193
	v_pk_mul_f32 v[14:15], v[110:111], s[12:13] op_sel_hi:[1,0]
	v_cvt_pk_fp8_f32 v11, v7, v8 op_sel:[0,0,1]
	v_exp_f32_e32 v14, v14
	v_exp_f32_e32 v15, v15
	v_pk_mul_f32 v[8:9], v[112:113], s[12:13] op_sel_hi:[1,0]
	global_store_dwordx2 v[12:13], v[10:11], off
	v_exp_f32_e32 v8, v8
	v_pk_add_f32 v[10:11], v[14:15], 1.0 op_sel_hi:[1,0]
	v_pk_mul_f32 v[14:15], v[106:107], s[12:13] op_sel_hi:[1,0]
	v_exp_f32_e32 v9, v9
	v_exp_f32_e32 v14, v14
	v_exp_f32_e32 v15, v15
	v_pk_mul_f32 v[12:13], v[108:109], s[12:13] op_sel_hi:[1,0]
	v_rcp_f32_e32 v10, v10
	v_rcp_f32_e32 v11, v11
	v_exp_f32_e32 v12, v12
	v_exp_f32_e32 v13, v13
	v_pk_add_f32 v[14:15], v[14:15], 1.0 op_sel_hi:[1,0]
	v_pk_add_f32 v[8:9], v[8:9], 1.0 op_sel_hi:[1,0]
	v_rcp_f32_e32 v14, v14
	v_rcp_f32_e32 v15, v15
	v_rcp_f32_e32 v8, v8
	v_rcp_f32_e32 v9, v9
	v_pk_mul_f32 v[10:11], v[110:111], v[10:11]
	v_pk_add_f32 v[12:13], v[12:13], 1.0 op_sel_hi:[1,0]
	v_pk_mul_f32 v[10:11], v[102:103], v[10:11]
	v_rcp_f32_e32 v12, v12
	v_rcp_f32_e32 v13, v13
	v_pk_mul_f32 v[14:15], v[106:107], v[14:15]
	v_med3_f32 v16, v10, s48, v193
	v_pk_mul_f32 v[14:15], v[98:99], v[14:15]
	v_med3_f32 v11, v11, s48, v193
	v_mov_b32_e32 v10, 0
	v_cvt_pk_fp8_f32 v10, v16, v11
	v_med3_f32 v14, v14, s48, v193
	v_med3_f32 v15, v15, s48, v193
	v_mov_b32_e32 v11, 0
	v_pk_mul_f32 v[8:9], v[112:113], v[8:9]
	v_cvt_pk_fp8_f32 v11, v14, v15
	v_pk_mul_f32 v[8:9], v[104:105], v[8:9]
	v_pk_mul_f32 v[12:13], v[108:109], v[12:13]
	v_med3_f32 v8, v8, s48, v193
	v_pk_mul_f32 v[12:13], v[100:101], v[12:13]
	v_med3_f32 v9, v9, s48, v193
	v_cvt_pk_fp8_f32 v10, v8, v9 op_sel:[0,0,1]
	v_med3_f32 v8, v12, s48, v193
	v_med3_f32 v9, v13, s48, v193
	v_cvt_pk_fp8_f32 v11, v8, v9 op_sel:[0,0,1]
	v_or_b32_e32 v7, 48, v6
	v_mad_i64_i32 v[8:9], s[26:27], v7, s47, v[4:5]
	v_lshl_add_u64 v[8:9], v[8:9], 0, v[2:3]
	global_store_dwordx2 v[8:9], v[10:11], off
	v_pk_mul_f32 v[10:11], v[94:95], s[12:13] op_sel_hi:[1,0]
	v_pk_mul_f32 v[8:9], v[96:97], s[12:13] op_sel_hi:[1,0]
	v_exp_f32_e32 v10, v10
	v_exp_f32_e32 v11, v11
	v_pk_mul_f32 v[16:17], v[90:91], s[12:13] op_sel_hi:[1,0]
	v_exp_f32_e32 v8, v8
	v_exp_f32_e32 v9, v9
	v_exp_f32_e32 v16, v16
	v_exp_f32_e32 v17, v17
	v_pk_add_f32 v[10:11], v[10:11], 1.0 op_sel_hi:[1,0]
	v_pk_mul_f32 v[14:15], v[92:93], s[12:13] op_sel_hi:[1,0]
	v_pk_add_f32 v[8:9], v[8:9], 1.0 op_sel_hi:[1,0]
	v_rcp_f32_e32 v10, v10
	v_rcp_f32_e32 v11, v11
	v_exp_f32_e32 v14, v14
	v_exp_f32_e32 v15, v15
	v_pk_add_f32 v[16:17], v[16:17], 1.0 op_sel_hi:[1,0]
	v_rcp_f32_e32 v8, v8
	v_rcp_f32_e32 v9, v9
	v_rcp_f32_e32 v16, v16
	v_rcp_f32_e32 v17, v17
	v_pk_mul_f32 v[10:11], v[94:95], v[10:11]
	v_pk_add_f32 v[14:15], v[14:15], 1.0 op_sel_hi:[1,0]
	v_add_u32_e32 v7, 0x80, v6
	v_pk_mul_f32 v[8:9], v[96:97], v[8:9]
	v_rcp_f32_e32 v14, v14
	v_rcp_f32_e32 v15, v15
	v_pk_mul_f32 v[10:11], v[86:87], v[10:11]
	v_pk_mul_f32 v[16:17], v[90:91], v[16:17]
	v_mad_i64_i32 v[12:13], s[26:27], v7, s47, v[4:5]
	v_pk_mul_f32 v[8:9], v[88:89], v[8:9]
	v_pk_mul_f32 v[16:17], v[82:83], v[16:17]
	v_med3_f32 v7, v10, s48, v193
	v_med3_f32 v11, v11, s48, v193
	v_mov_b32_e32 v10, 0
	v_cvt_pk_fp8_f32 v10, v7, v11
	v_med3_f32 v7, v8, s48, v193
	v_med3_f32 v8, v9, s48, v193
	v_med3_f32 v9, v16, s48, v193
	v_med3_f32 v16, v17, s48, v193
	v_mov_b32_e32 v11, 0
	v_cvt_pk_fp8_f32 v11, v9, v16
	v_pk_mul_f32 v[14:15], v[92:93], v[14:15]
	v_cvt_pk_fp8_f32 v10, v7, v8 op_sel:[0,0,1]
	v_pk_mul_f32 v[14:15], v[84:85], v[14:15]
	v_lshl_add_u64 v[12:13], v[12:13], 0, v[2:3]
	v_med3_f32 v7, v14, s48, v193
	v_med3_f32 v8, v15, s48, v193
	v_pk_mul_f32 v[14:15], v[78:79], s[12:13] op_sel_hi:[1,0]
	v_cvt_pk_fp8_f32 v11, v7, v8 op_sel:[0,0,1]
	v_exp_f32_e32 v14, v14
	v_exp_f32_e32 v15, v15
	v_pk_mul_f32 v[8:9], v[80:81], s[12:13] op_sel_hi:[1,0]
	global_store_dwordx2 v[12:13], v[10:11], off
	v_exp_f32_e32 v8, v8
	v_pk_add_f32 v[10:11], v[14:15], 1.0 op_sel_hi:[1,0]
	v_pk_mul_f32 v[14:15], v[74:75], s[12:13] op_sel_hi:[1,0]
	v_exp_f32_e32 v9, v9
	v_exp_f32_e32 v14, v14
	v_exp_f32_e32 v15, v15
	v_pk_mul_f32 v[12:13], v[76:77], s[12:13] op_sel_hi:[1,0]
	v_rcp_f32_e32 v10, v10
	v_rcp_f32_e32 v11, v11
	v_exp_f32_e32 v12, v12
	v_exp_f32_e32 v13, v13
	v_pk_add_f32 v[14:15], v[14:15], 1.0 op_sel_hi:[1,0]
	v_pk_add_f32 v[8:9], v[8:9], 1.0 op_sel_hi:[1,0]
	v_rcp_f32_e32 v14, v14
	v_rcp_f32_e32 v15, v15
	v_rcp_f32_e32 v8, v8
	v_rcp_f32_e32 v9, v9
	v_pk_mul_f32 v[10:11], v[78:79], v[10:11]
	v_pk_add_f32 v[12:13], v[12:13], 1.0 op_sel_hi:[1,0]
	v_pk_mul_f32 v[10:11], v[70:71], v[10:11]
; __device__ __forceinline__ float fast_silu(float g) { return g * __builtin_amdgcn_rcpf(1.0f + __expf(-g)); }
; __device__ __forceinline__ float clamp448(float x) { return __builtin_amdgcn_fmed3f(x, -448.f, 448.f); }
; __device__ __forceinline__ unsigned pk4_fp8(float a, float b, float c, float d) { int w = 0; w = __builtin_amdgcn_cvt_pk_fp8_f32(clamp448(a), clamp448(b), w, false); w = __builtin_amdgcn_cvt_pk_fp8_f32(clamp448(c), clamp448(d), w, true); return (unsigned)w; }
; #define PG8_BAR __builtin_amdgcn_s_barrier()
;     __device__ __forceinline__ void operator()(const f32x4 (&acc)[2][2][4][2], const Unit& u, int wr, int wc, int fr, int fq) const {
;     ...
;         for (int ai = 0; ai < 2; ++ai)
; #pragma unroll
;             for (int m = 0; m < 4; ++m) { unsigned char* rowp = O + (size_t)(row0 + ai * HALF + m * 16) * ldc + col0;
;                 f32x4 g0 = acc[ai][0][m][0], g1 = acc[ai][0][m][1], u0 = acc[ai][1][m][0], u1 = acc[ai][1][m][1];
;                 if (PROBE_REPEAT == 300) {
; #pragma unroll
;                     for (int q = 0; q < 4; ++q) { float t0 = fast_silu(g0[q] + 1.0f) * u0[q], t1 = fast_silu(g1[q] + 1.0f) * u1[q]; asm volatile("" : "+v"(t0), "+v"(t1)); u0[q] += 0.0f * clamp448(t0); u1[q] += 0.0f * clamp448(t1); } }
;                 const f32x4 h0 = silu_mul4(g0, u0), h1 = silu_mul4(g1, u1);
;                 u32x2 w; w.x = pk4_fp8(h0[0], h0[1], h0[2], h0[3]); w.y = pk4_fp8(h1[0], h1[1], h1[2], h1[3]);
;                 *(u32x2*)(rowp) = w; }
; template <class Epi, class Sched, bool ALIGN_EPI = false, bool SP2 = false>
; __device__ __forceinline__ void gemm_phase(PG8_LAS unsigned char* lds, const Gemm g, const Sched& S, const Epi& E) {
;     ...
;         if (!has_next) break;
; #pragma unroll
;         for (int a = 0; a < 2; ++a)
; #pragma unroll
;             for (int b = 0; b < 2; ++b)
; #pragma unroll
;                 for (int m = 0; m < 4; ++m)
; #pragma unroll
;                     for (int n = 0; n < 2; ++n) acc[a][b][m][n] = (f32x4){0.f, 0.f, 0.f, 0.f};
;         cur = nxt; cA = nA; cB = nB; ++ui;
;         if constexpr (ALIGN_EPI) { if (wr == 1) PG8_BAR; }
	v_rcp_f32_e32 v12, v12
	v_rcp_f32_e32 v13, v13
	v_pk_mul_f32 v[14:15], v[74:75], v[14:15]
	v_med3_f32 v16, v10, s48, v193
	v_pk_mul_f32 v[14:15], v[66:67], v[14:15]
	v_med3_f32 v11, v11, s48, v193
	v_mov_b32_e32 v10, 0
	v_cvt_pk_fp8_f32 v10, v16, v11
	v_med3_f32 v14, v14, s48, v193
	v_med3_f32 v15, v15, s48, v193
	v_mov_b32_e32 v11, 0
	v_pk_mul_f32 v[8:9], v[80:81], v[8:9]
	v_cvt_pk_fp8_f32 v11, v14, v15
	v_pk_mul_f32 v[8:9], v[72:73], v[8:9]
	v_pk_mul_f32 v[12:13], v[76:77], v[12:13]
	v_med3_f32 v8, v8, s48, v193
	v_pk_mul_f32 v[12:13], v[68:69], v[12:13]
	v_med3_f32 v9, v9, s48, v193
	v_cvt_pk_fp8_f32 v10, v8, v9 op_sel:[0,0,1]
	v_med3_f32 v8, v12, s48, v193
	v_med3_f32 v9, v13, s48, v193
	v_cvt_pk_fp8_f32 v11, v8, v9 op_sel:[0,0,1]
	v_add_u32_e32 v7, 0x90, v6
	v_mad_i64_i32 v[8:9], s[26:27], v7, s47, v[4:5]
	v_lshl_add_u64 v[8:9], v[8:9], 0, v[2:3]
	global_store_dwordx2 v[8:9], v[10:11], off
	v_pk_mul_f32 v[10:11], v[62:63], s[12:13] op_sel_hi:[1,0]
	v_pk_mul_f32 v[8:9], v[64:65], s[12:13] op_sel_hi:[1,0]
	v_exp_f32_e32 v10, v10
	v_exp_f32_e32 v11, v11
	v_pk_mul_f32 v[16:17], v[58:59], s[12:13] op_sel_hi:[1,0]
	v_exp_f32_e32 v8, v8
	v_exp_f32_e32 v9, v9
	v_exp_f32_e32 v16, v16
	v_exp_f32_e32 v17, v17
	v_pk_add_f32 v[10:11], v[10:11], 1.0 op_sel_hi:[1,0]
	v_pk_mul_f32 v[14:15], v[60:61], s[12:13] op_sel_hi:[1,0]
	v_pk_add_f32 v[8:9], v[8:9], 1.0 op_sel_hi:[1,0]
	v_rcp_f32_e32 v10, v10
	v_rcp_f32_e32 v11, v11
	v_exp_f32_e32 v14, v14
	v_exp_f32_e32 v15, v15
	v_pk_add_f32 v[16:17], v[16:17], 1.0 op_sel_hi:[1,0]
	v_rcp_f32_e32 v8, v8
	v_rcp_f32_e32 v9, v9
	v_rcp_f32_e32 v16, v16
	v_rcp_f32_e32 v17, v17
	v_pk_mul_f32 v[10:11], v[62:63], v[10:11]
	v_pk_add_f32 v[14:15], v[14:15], 1.0 op_sel_hi:[1,0]
	v_add_u32_e32 v7, 0xa0, v6
	v_pk_mul_f32 v[8:9], v[64:65], v[8:9]
	v_rcp_f32_e32 v14, v14
	v_rcp_f32_e32 v15, v15
	v_pk_mul_f32 v[10:11], v[54:55], v[10:11]
	v_pk_mul_f32 v[16:17], v[58:59], v[16:17]
	v_mad_i64_i32 v[12:13], s[26:27], v7, s47, v[4:5]
	v_pk_mul_f32 v[8:9], v[56:57], v[8:9]
	v_pk_mul_f32 v[16:17], v[50:51], v[16:17]
	v_med3_f32 v7, v10, s48, v193
	v_med3_f32 v11, v11, s48, v193
	v_mov_b32_e32 v10, 0
	v_cvt_pk_fp8_f32 v10, v7, v11
	v_med3_f32 v7, v8, s48, v193
	v_med3_f32 v8, v9, s48, v193
	v_med3_f32 v9, v16, s48, v193
	v_med3_f32 v16, v17, s48, v193
	v_mov_b32_e32 v11, 0
	v_cvt_pk_fp8_f32 v11, v9, v16
	v_pk_mul_f32 v[14:15], v[60:61], v[14:15]
	v_cvt_pk_fp8_f32 v10, v7, v8 op_sel:[0,0,1]
	v_pk_mul_f32 v[14:15], v[52:53], v[14:15]
	v_lshl_add_u64 v[12:13], v[12:13], 0, v[2:3]
	v_med3_f32 v7, v14, s48, v193
	v_med3_f32 v8, v15, s48, v193
	v_cvt_pk_fp8_f32 v11, v7, v8 op_sel:[0,0,1]
	v_pk_mul_f32 v[8:9], v[48:49], s[12:13] op_sel_hi:[1,0]
	v_pk_mul_f32 v[14:15], v[46:47], s[12:13] op_sel_hi:[1,0]
	v_exp_f32_e32 v8, v8
	v_exp_f32_e32 v14, v14
	v_exp_f32_e32 v9, v9
	v_exp_f32_e32 v15, v15
	global_store_dwordx2 v[12:13], v[10:11], off
	v_pk_mul_f32 v[12:13], v[42:43], s[12:13] op_sel_hi:[1,0]
	v_add_u32_e32 v16, 0xb0, v6
	v_exp_f32_e32 v12, v12
	v_exp_f32_e32 v13, v13
	v_pk_add_f32 v[6:7], v[8:9], 1.0 op_sel_hi:[1,0]
	v_pk_add_f32 v[8:9], v[14:15], 1.0 op_sel_hi:[1,0]
	v_pk_mul_f32 v[10:11], v[44:45], s[12:13] op_sel_hi:[1,0]
	v_rcp_f32_e32 v8, v8
	v_rcp_f32_e32 v9, v9
	v_exp_f32_e32 v10, v10
	v_exp_f32_e32 v11, v11
	v_pk_add_f32 v[12:13], v[12:13], 1.0 op_sel_hi:[1,0]
	v_rcp_f32_e32 v6, v6
	v_rcp_f32_e32 v12, v12
	v_rcp_f32_e32 v13, v13
	v_rcp_f32_e32 v7, v7
	v_pk_mul_f32 v[8:9], v[46:47], v[8:9]
	v_pk_add_f32 v[10:11], v[10:11], 1.0 op_sel_hi:[1,0]
	v_pk_mul_f32 v[8:9], v[38:39], v[8:9]
	v_rcp_f32_e32 v10, v10
	v_rcp_f32_e32 v11, v11
	v_pk_mul_f32 v[12:13], v[42:43], v[12:13]
	v_med3_f32 v14, v8, s48, v193
	v_pk_mul_f32 v[12:13], v[34:35], v[12:13]
	v_med3_f32 v9, v9, s48, v193
	v_mov_b32_e32 v8, 0
	v_cvt_pk_fp8_f32 v8, v14, v9
	v_med3_f32 v12, v12, s48, v193
	v_med3_f32 v13, v13, s48, v193
	v_mov_b32_e32 v9, 0
	v_pk_mul_f32 v[6:7], v[48:49], v[6:7]
	v_cvt_pk_fp8_f32 v9, v12, v13
	v_pk_mul_f32 v[6:7], v[40:41], v[6:7]
	v_pk_mul_f32 v[10:11], v[44:45], v[10:11]
	v_med3_f32 v6, v6, s48, v193
	v_pk_mul_f32 v[10:11], v[36:37], v[10:11]
	v_med3_f32 v7, v7, s48, v193
	v_cvt_pk_fp8_f32 v8, v6, v7 op_sel:[0,0,1]
	v_med3_f32 v6, v10, s48, v193
	v_med3_f32 v7, v11, s48, v193
	v_cvt_pk_fp8_f32 v9, v6, v7 op_sel:[0,0,1]
	v_mad_i64_i32 v[4:5], s[26:27], v16, s47, v[4:5]
	v_lshl_add_u64 v[2:3], v[4:5], 0, v[2:3]
	s_andn2_b64 vcc, exec, s[0:1]
	s_mov_b64 s[0:1], -1
	global_store_dwordx2 v[2:3], v[8:9], off
	s_cbranch_vccnz .LBB0_1879
	s_andn2_b64 vcc, exec, s[2:3]
	s_cbranch_vccnz .LBB0_1878
	s_barrier
	s_branch .LBB0_1878

; #define PG8_STAGE(bufoff, gbase, voff) do { _Pragma("unroll") for (int _i = 0; _i < 2; ++_i) \
;         __builtin_amdgcn_global_load_lds((const unsigned*)((const char*)(gbase) + (voff)[_i]), (PG8_LAS unsigned*)(lds + (bufoff) + ldsw + _i * 8192), 16, 0, 0); } while (0)
; #define PG8_LDA(dst, b, h) do { _Pragma("unroll") for (int m = 0; m < 4; ++m) _Pragma("unroll") for (int k = 0; k < 2; ++k) dst[m][k] = *(const PG8_LAS bf16x8*)(lds + PG8_SA(b, h) + aoff + m * 2048 + k * 1024); } while (0)
; #define PG8_LDB(dst, b, h) do { _Pragma("unroll") for (int n = 0; n < 2; ++n) _Pragma("unroll") for (int k = 0; k < 2; ++k) dst[n][k] = *(const PG8_LAS bf16x8*)(lds + PG8_SB(b, h) + boff + n * 2048 + k * 1024); } while (0)
; #define PG8_WAIT_V(n) asm volatile("s_waitcnt vmcnt(" #n ")" ::: "memory")
; #define PG8_WAIT_L(n) asm volatile("s_waitcnt lgkmcnt(" #n ")" ::: "memory")
; #define PG8_BAR __builtin_amdgcn_s_barrier()
; #define PG8_SCHED __builtin_amdgcn_sched_barrier(0)
; template <class Epi, class Sched, bool ALIGN_EPI = false, bool SP2 = false>
; __device__ __forceinline__ void gemm_phase(PG8_LAS unsigned char* lds, const Gemm g, const Sched& S, const Epi& E) {
;     ...
;             const bool last = (t == nt - 2);
;             const char* a1 = cA + (size_t)(t + 1) * kstep;
;             const char* a2 = last ? nA : cA + (size_t)(t + 2) * kstep; const char* b2 = last ? nB : cB + (size_t)(t + 2) * kstep;
;             const char* a3 = a2 + kstep; const char* b3 = b2 + kstep;
;             if (last && has_next) S.a_ready(nxt);
;             if constexpr (SP2) {
;             PG8_LDB(B0, 0, 0); PG8_LDB(B1, 0, 1); PG8_SCHED; PG8_LDA(At, 0, 0); PG8_STAGE(PG8_SA(1, 1), a1 + hstep, voffA);
;             PG8_WAIT_V(8); PG8_WAIT_L(0); PG8_BAR; PG8_MMA(0, 0, At, B0); PG8_MMA(0, 1, At, B1); PG8_BAR; PG8_SCHED;
;             PG8_LDA(At, 0, 1); PG8_STAGE(PG8_SB(0, 0), b2, voffB); PG8_STAGE(PG8_SB(0, 1), b2 + hstep, voffB); PG8_STAGE(PG8_SA(0, 0), a2, voffA);
;             PG8_WAIT_V(8); PG8_WAIT_L(0); PG8_BAR; PG8_MMA(1, 0, At, B0); PG8_MMA(1, 1, At, B1); PG8_BAR; PG8_SCHED;
.LBB0_2054:
	ds_read_b128 v[26:29], v197
	ds_read_b128 v[30:33], v197 offset:1024
	ds_read_b128 v[18:21], v197 offset:2048
	ds_read_b128 v[22:25], v197 offset:3072
	ds_read_b128 v[10:13], v198
	ds_read_b128 v[14:17], v198 offset:1024
	ds_read_b128 v[2:5], v198 offset:2048
	ds_read_b128 v[6:9], v198 offset:3072
	s_add_u32 s28, s26, 0xfff20080
	s_addc_u32 s29, s27, -1
	s_cmp_eq_u32 s60, 52
	s_cselect_b32 s31, s5, s29
	s_cselect_b32 s30, s4, s28
	s_cselect_b32 s29, s25, s59
	s_cselect_b32 s28, s24, s58
	s_add_i32 m0, s36, 0xc000
	ds_read_b128 v[176:179], v199
	ds_read_b128 v[180:183], v199 offset:1024
	ds_read_b128 v[200:203], v199 offset:2048
	ds_read_b128 v[204:207], v199 offset:3072
	ds_read_b128 v[214:217], v199 offset:4096
	ds_read_b128 v[218:221], v199 offset:5120
	ds_read_b128 v[222:225], v199 offset:6144
	ds_read_b128 v[226:229], v199 offset:7168
	global_load_lds_dwordx4 v170, s[26:27]
	s_add_i32 m0, s36, 0xe000
	s_nop 0
	global_load_lds_dwordx4 v172, s[26:27]
	s_waitcnt vmcnt(8)
	s_waitcnt lgkmcnt(0)
	s_barrier
	s_setprio 1
	s_waitcnt lgkmcnt(0)
	v_mfma_scale_f32_16x16x128_f8f6f4 v[158:161], v[26:33], v[176:183], v[158:161], v192, v193 op_sel_hi:[0,0,0]
	v_mfma_scale_f32_16x16x128_f8f6f4 v[154:157], v[18:25], v[176:183], v[154:157], v192, v193 op_sel_hi:[0,0,0]
	v_mfma_scale_f32_16x16x128_f8f6f4 v[150:153], v[26:33], v[200:207], v[150:153], v192, v193 op_sel_hi:[0,0,0]
	v_mfma_scale_f32_16x16x128_f8f6f4 v[142:145], v[18:25], v[200:207], v[142:145], v192, v193 op_sel_hi:[0,0,0]
	v_mfma_scale_f32_16x16x128_f8f6f4 v[134:137], v[26:33], v[214:221], v[134:137], v192, v193 op_sel_hi:[0,0,0]
	v_mfma_scale_f32_16x16x128_f8f6f4 v[126:129], v[18:25], v[214:221], v[126:129], v192, v193 op_sel_hi:[0,0,0]
	v_mfma_scale_f32_16x16x128_f8f6f4 v[118:121], v[26:33], v[222:229], v[118:121], v192, v193 op_sel_hi:[0,0,0]
	v_mfma_scale_f32_16x16x128_f8f6f4 v[110:113], v[18:25], v[222:229], v[110:113], v192, v193 op_sel_hi:[0,0,0]
	s_setprio 0
	s_setprio 1
	v_mfma_scale_f32_16x16x128_f8f6f4 v[146:149], v[10:17], v[176:183], v[146:149], v192, v193 op_sel_hi:[0,0,0]
	v_mfma_scale_f32_16x16x128_f8f6f4 v[138:141], v[2:9], v[176:183], v[138:141], v192, v193 op_sel_hi:[0,0,0]
	v_mfma_scale_f32_16x16x128_f8f6f4 v[130:133], v[10:17], v[200:207], v[130:133], v192, v193 op_sel_hi:[0,0,0]
	v_mfma_scale_f32_16x16x128_f8f6f4 v[122:125], v[2:9], v[200:207], v[122:125], v192, v193 op_sel_hi:[0,0,0]
	v_mfma_scale_f32_16x16x128_f8f6f4 v[114:117], v[10:17], v[214:221], v[114:117], v192, v193 op_sel_hi:[0,0,0]
	v_mfma_scale_f32_16x16x128_f8f6f4 v[106:109], v[2:9], v[214:221], v[106:109], v192, v193 op_sel_hi:[0,0,0]
	v_mfma_scale_f32_16x16x128_f8f6f4 v[102:105], v[10:17], v[222:229], v[102:105], v192, v193 op_sel_hi:[0,0,0]
	v_mfma_scale_f32_16x16x128_f8f6f4 v[98:101], v[2:9], v[222:229], v[98:101], v192, v193 op_sel_hi:[0,0,0]
	s_setprio 0
	s_barrier
	s_add_i32 s61, s44, s34
	s_mov_b32 m0, s61
	ds_read_b128 v[200:203], v199 offset:16384
	ds_read_b128 v[204:207], v199 offset:17408
	ds_read_b128 v[214:217], v199 offset:18432
	ds_read_b128 v[218:221], v199 offset:19456
	ds_read_b128 v[222:225], v199 offset:20480
	ds_read_b128 v[226:229], v199 offset:21504
	ds_read_b128 v[230:233], v199 offset:22528
	ds_read_b128 v[234:237], v199 offset:23552
	global_load_lds_dwordx4 v164, s[28:29]
	s_add_i32 m0, s61, 0x2000
	s_add_u32 s62, s28, 0xe0000
	s_addc_u32 s63, s29, 0
	s_add_i32 s61, s45, s34
	global_load_lds_dwordx4 v168, s[28:29]
	s_mov_b32 m0, s61
	s_nop 0
	global_load_lds_dwordx4 v164, s[62:63]
	s_add_i32 m0, s61, 0x2000
	s_nop 0
	global_load_lds_dwordx4 v168, s[62:63]
	s_mov_b32 m0, s36
	s_nop 0
	global_load_lds_dwordx4 v162, s[30:31]
	s_mov_b32 m0, s37
	s_nop 0
	global_load_lds_dwordx4 v166, s[30:31]
	s_waitcnt vmcnt(8)
	s_waitcnt lgkmcnt(0)
	s_barrier
	s_setprio 1
	s_waitcnt lgkmcnt(0)
	v_mfma_scale_f32_16x16x128_f8f6f4 v[94:97], v[26:33], v[200:207], v[94:97], v192, v193 op_sel_hi:[0,0,0]
	v_mfma_scale_f32_16x16x128_f8f6f4 v[90:93], v[18:25], v[200:207], v[90:93], v192, v193 op_sel_hi:[0,0,0]
	v_mfma_scale_f32_16x16x128_f8f6f4 v[86:89], v[26:33], v[214:221], v[86:89], v192, v193 op_sel_hi:[0,0,0]
	v_mfma_scale_f32_16x16x128_f8f6f4 v[78:81], v[18:25], v[214:221], v[78:81], v192, v193 op_sel_hi:[0,0,0]
	v_mfma_scale_f32_16x16x128_f8f6f4 v[70:73], v[26:33], v[222:229], v[70:73], v192, v193 op_sel_hi:[0,0,0]
	v_mfma_scale_f32_16x16x128_f8f6f4 v[62:65], v[18:25], v[222:229], v[62:65], v192, v193 op_sel_hi:[0,0,0]
	v_mfma_scale_f32_16x16x128_f8f6f4 v[54:57], v[26:33], v[230:237], v[54:57], v192, v193 op_sel_hi:[0,0,0]
	v_mfma_scale_f32_16x16x128_f8f6f4 v[46:49], v[18:25], v[230:237], v[46:49], v192, v193 op_sel_hi:[0,0,0]
	s_setprio 0
	s_setprio 1
	v_mfma_scale_f32_16x16x128_f8f6f4 v[82:85], v[10:17], v[200:207], v[82:85], v192, v193 op_sel_hi:[0,0,0]
	v_mfma_scale_f32_16x16x128_f8f6f4 v[74:77], v[2:9], v[200:207], v[74:77], v192, v193 op_sel_hi:[0,0,0]
	v_mfma_scale_f32_16x16x128_f8f6f4 v[66:69], v[10:17], v[214:221], v[66:69], v192, v193 op_sel_hi:[0,0,0]
	v_mfma_scale_f32_16x16x128_f8f6f4 v[58:61], v[2:9], v[214:221], v[58:61], v192, v193 op_sel_hi:[0,0,0]
	v_mfma_scale_f32_16x16x128_f8f6f4 v[50:53], v[10:17], v[222:229], v[50:53], v192, v193 op_sel_hi:[0,0,0]
	v_mfma_scale_f32_16x16x128_f8f6f4 v[42:45], v[2:9], v[222:229], v[42:45], v192, v193 op_sel_hi:[0,0,0]
	v_mfma_scale_f32_16x16x128_f8f6f4 v[38:41], v[10:17], v[230:237], v[38:41], v192, v193 op_sel_hi:[0,0,0]
	v_mfma_scale_f32_16x16x128_f8f6f4 v[34:37], v[2:9], v[230:237], v[34:37], v192, v193 op_sel_hi:[0,0,0]
	s_setprio 0
	s_barrier
; #define PG8_STAGE(bufoff, gbase, voff) do { _Pragma("unroll") for (int _i = 0; _i < 2; ++_i) \
;         __builtin_amdgcn_global_load_lds((const unsigned*)((const char*)(gbase) + (voff)[_i]), (PG8_LAS unsigned*)(lds + (bufoff) + ldsw + _i * 8192), 16, 0, 0); } while (0)
; #define PG8_LDA(dst, b, h) do { _Pragma("unroll") for (int m = 0; m < 4; ++m) _Pragma("unroll") for (int k = 0; k < 2; ++k) dst[m][k] = *(const PG8_LAS bf16x8*)(lds + PG8_SA(b, h) + aoff + m * 2048 + k * 1024); } while (0)
; #define PG8_LDB(dst, b, h) do { _Pragma("unroll") for (int n = 0; n < 2; ++n) _Pragma("unroll") for (int k = 0; k < 2; ++k) dst[n][k] = *(const PG8_LAS bf16x8*)(lds + PG8_SB(b, h) + boff + n * 2048 + k * 1024); } while (0)
; #define PG8_WAIT_V(n) asm volatile("s_waitcnt vmcnt(" #n ")" ::: "memory")
; #define PG8_WAIT_L(n) asm volatile("s_waitcnt lgkmcnt(" #n ")" ::: "memory")
; #define PG8_BAR __builtin_amdgcn_s_barrier()
; #define PG8_SCHED __builtin_amdgcn_sched_barrier(0)
; template <class Epi, class Sched, bool ALIGN_EPI = false, bool SP2 = false>
; __device__ __forceinline__ void gemm_phase(PG8_LAS unsigned char* lds, const Gemm g, const Sched& S, const Epi& E) {
;     ...
;             PG8_LDB(B0, 1, 0); PG8_LDB(B1, 1, 1); PG8_SCHED; PG8_LDA(At, 1, 0); PG8_STAGE(PG8_SA(0, 1), a2 + hstep, voffA);
;             PG8_WAIT_V(8); PG8_WAIT_L(0); PG8_BAR; PG8_MMA(0, 0, At, B0); PG8_MMA(0, 1, At, B1); PG8_BAR; PG8_SCHED;
;             PG8_LDA(At, 1, 1); PG8_STAGE(PG8_SB(1, 0), b3, voffB); PG8_STAGE(PG8_SB(1, 1), b3 + hstep, voffB); PG8_STAGE(PG8_SA(1, 0), a3, voffA);
;             PG8_WAIT_V(8); PG8_WAIT_L(0); PG8_BAR; PG8_MMA(1, 0, At, B0); PG8_MMA(1, 1, At, B1); PG8_BAR; PG8_SCHED;
	s_add_i32 s61, 0, 0x18000
	s_add_i32 s62, 0, 0x1c000
	ds_read_b128 v[2:5], v248
	ds_read_b128 v[6:9], v248 offset:1024
	ds_read_b128 v[10:13], v248 offset:2048
	ds_read_b128 v[14:17], v248 offset:3072
	ds_read_b128 v[18:21], v249
	ds_read_b128 v[22:25], v249 offset:1024
	ds_read_b128 v[26:29], v249 offset:2048
	ds_read_b128 v[30:33], v249 offset:3072
	s_add_u32 s30, s30, 0xe0000
	s_addc_u32 s31, s31, 0
	s_mov_b32 m0, s38
	ds_read_b128 v[200:203], v199 offset:32768
	ds_read_b128 v[204:207], v199 offset:33792
	ds_read_b128 v[214:217], v199 offset:34816
	ds_read_b128 v[218:221], v199 offset:35840
	ds_read_b128 v[222:225], v199 offset:36864
	ds_read_b128 v[226:229], v199 offset:37888
	ds_read_b128 v[230:233], v199 offset:38912
	ds_read_b128 v[234:237], v199 offset:39936
	global_load_lds_dwordx4 v162, s[30:31]
	s_mov_b32 m0, s39
	s_nop 0
	global_load_lds_dwordx4 v166, s[30:31]
	s_waitcnt vmcnt(8)
	s_waitcnt lgkmcnt(0)
	s_barrier
	s_setprio 1
	s_waitcnt lgkmcnt(0)
	v_mfma_scale_f32_16x16x128_f8f6f4 v[158:161], v[2:9], v[200:207], v[158:161], v192, v193 op_sel_hi:[0,0,0]
	v_mfma_scale_f32_16x16x128_f8f6f4 v[154:157], v[10:17], v[200:207], v[154:157], v192, v193 op_sel_hi:[0,0,0]
	v_mfma_scale_f32_16x16x128_f8f6f4 v[150:153], v[2:9], v[214:221], v[150:153], v192, v193 op_sel_hi:[0,0,0]
	v_mfma_scale_f32_16x16x128_f8f6f4 v[142:145], v[10:17], v[214:221], v[142:145], v192, v193 op_sel_hi:[0,0,0]
	v_mfma_scale_f32_16x16x128_f8f6f4 v[134:137], v[2:9], v[222:229], v[134:137], v192, v193 op_sel_hi:[0,0,0]
	v_mfma_scale_f32_16x16x128_f8f6f4 v[126:129], v[10:17], v[222:229], v[126:129], v192, v193 op_sel_hi:[0,0,0]
	v_mfma_scale_f32_16x16x128_f8f6f4 v[118:121], v[2:9], v[230:237], v[118:121], v192, v193 op_sel_hi:[0,0,0]
	v_mfma_scale_f32_16x16x128_f8f6f4 v[110:113], v[10:17], v[230:237], v[110:113], v192, v193 op_sel_hi:[0,0,0]
	s_setprio 0
	s_setprio 1
	v_mfma_scale_f32_16x16x128_f8f6f4 v[146:149], v[18:25], v[200:207], v[146:149], v192, v193 op_sel_hi:[0,0,0]
	v_mfma_scale_f32_16x16x128_f8f6f4 v[138:141], v[26:33], v[200:207], v[138:141], v192, v193 op_sel_hi:[0,0,0]
	v_mfma_scale_f32_16x16x128_f8f6f4 v[130:133], v[18:25], v[214:221], v[130:133], v192, v193 op_sel_hi:[0,0,0]
	v_mfma_scale_f32_16x16x128_f8f6f4 v[122:125], v[26:33], v[214:221], v[122:125], v192, v193 op_sel_hi:[0,0,0]
	v_mfma_scale_f32_16x16x128_f8f6f4 v[114:117], v[18:25], v[222:229], v[114:117], v192, v193 op_sel_hi:[0,0,0]
	v_mfma_scale_f32_16x16x128_f8f6f4 v[106:109], v[26:33], v[222:229], v[106:109], v192, v193 op_sel_hi:[0,0,0]
	v_mfma_scale_f32_16x16x128_f8f6f4 v[102:105], v[18:25], v[230:237], v[102:105], v192, v193 op_sel_hi:[0,0,0]
	v_mfma_scale_f32_16x16x128_f8f6f4 v[98:101], v[26:33], v[230:237], v[98:101], v192, v193 op_sel_hi:[0,0,0]
	s_setprio 0
	s_barrier
	s_add_u32 s98, s28, 0x80
	s_addc_u32 s99, s29, 0
	s_add_u32 s100, s30, 0xfff20080
	s_addc_u32 s101, s31, -1
	s_add_i32 s30, s61, s34
	s_mov_b32 m0, s30
	ds_read_b128 v[200:203], v199 offset:49152
	ds_read_b128 v[204:207], v199 offset:50176
	ds_read_b128 v[214:217], v199 offset:51200
	ds_read_b128 v[218:221], v199 offset:52224
	ds_read_b128 v[222:225], v199 offset:53248
	ds_read_b128 v[226:229], v199 offset:54272
	ds_read_b128 v[230:233], v199 offset:55296
	ds_read_b128 v[234:237], v199 offset:56320
	global_load_lds_dwordx4 v164, s[98:99]
	s_add_i32 m0, s30, 0x2000
	s_add_u32 s28, s28, 0xe0080
	s_addc_u32 s29, s29, 0
	s_add_i32 s30, s62, s34
	global_load_lds_dwordx4 v168, s[98:99]
	s_mov_b32 m0, s30
	s_nop 0
	global_load_lds_dwordx4 v164, s[28:29]
	s_add_i32 m0, s30, 0x2000
	s_nop 0
	global_load_lds_dwordx4 v168, s[28:29]
	s_mov_b32 m0, s41
	s_nop 0
	global_load_lds_dwordx4 v162, s[100:101]
	s_mov_b32 m0, s42
	s_nop 0
	global_load_lds_dwordx4 v166, s[100:101]
	s_waitcnt vmcnt(8)
	s_waitcnt lgkmcnt(0)
	s_barrier
	s_setprio 1
	s_waitcnt lgkmcnt(0)
	v_mfma_scale_f32_16x16x128_f8f6f4 v[94:97], v[2:9], v[200:207], v[94:97], v192, v193 op_sel_hi:[0,0,0]
	v_mfma_scale_f32_16x16x128_f8f6f4 v[90:93], v[10:17], v[200:207], v[90:93], v192, v193 op_sel_hi:[0,0,0]
	v_mfma_scale_f32_16x16x128_f8f6f4 v[86:89], v[2:9], v[214:221], v[86:89], v192, v193 op_sel_hi:[0,0,0]
	v_mfma_scale_f32_16x16x128_f8f6f4 v[78:81], v[10:17], v[214:221], v[78:81], v192, v193 op_sel_hi:[0,0,0]
	v_mfma_scale_f32_16x16x128_f8f6f4 v[70:73], v[2:9], v[222:229], v[70:73], v192, v193 op_sel_hi:[0,0,0]
	v_mfma_scale_f32_16x16x128_f8f6f4 v[62:65], v[10:17], v[222:229], v[62:65], v192, v193 op_sel_hi:[0,0,0]
	v_mfma_scale_f32_16x16x128_f8f6f4 v[54:57], v[2:9], v[230:237], v[54:57], v192, v193 op_sel_hi:[0,0,0]
	v_mfma_scale_f32_16x16x128_f8f6f4 v[46:49], v[10:17], v[230:237], v[46:49], v192, v193 op_sel_hi:[0,0,0]
	s_setprio 0
	s_setprio 1
	v_mfma_scale_f32_16x16x128_f8f6f4 v[82:85], v[18:25], v[200:207], v[82:85], v192, v193 op_sel_hi:[0,0,0]
	v_mfma_scale_f32_16x16x128_f8f6f4 v[74:77], v[26:33], v[200:207], v[74:77], v192, v193 op_sel_hi:[0,0,0]
	v_mfma_scale_f32_16x16x128_f8f6f4 v[66:69], v[18:25], v[214:221], v[66:69], v192, v193 op_sel_hi:[0,0,0]
	v_mfma_scale_f32_16x16x128_f8f6f4 v[58:61], v[26:33], v[214:221], v[58:61], v192, v193 op_sel_hi:[0,0,0]
	v_mfma_scale_f32_16x16x128_f8f6f4 v[50:53], v[18:25], v[222:229], v[50:53], v192, v193 op_sel_hi:[0,0,0]
	v_mfma_scale_f32_16x16x128_f8f6f4 v[42:45], v[26:33], v[222:229], v[42:45], v192, v193 op_sel_hi:[0,0,0]
	v_mfma_scale_f32_16x16x128_f8f6f4 v[38:41], v[18:25], v[230:237], v[38:41], v192, v193 op_sel_hi:[0,0,0]
	v_mfma_scale_f32_16x16x128_f8f6f4 v[34:37], v[26:33], v[230:237], v[34:37], v192, v193 op_sel_hi:[0,0,0]
	s_setprio 0
	s_barrier
; #define PG8_LAS __attribute__((address_space(3)))
; __device__ __forceinline__ unsigned cvt_pk_bf16(float lo, float hi) { unsigned r; asm volatile("v_cvt_pk_bf16_f32 %0, %1, %2" : "=v"(r) : "v"(lo), "v"(hi)); return r; }
; #define PG8_BAR __builtin_amdgcn_s_barrier()
;     __device__ __forceinline__ void operator()(const f32x4 (&acc)[2][2][4][2], const Unit& u, int wr, int wc, int fr, int fq) const {
;         const int row0 = u.pm * BM + wr * 64 + fr, col0 = (u.pn % nN) * BM + wc * 32 + 8 * fq;
; #pragma unroll
;         for (int ai = 0; ai < 2; ++ai)
; #pragma unroll
;             for (int m = 0; m < 4; ++m) { bf16_t* rowp = O + (size_t)(row0 + ai * HALF + m * 16) * ldc + col0;
; #pragma unroll
;                 for (int bj = 0; bj < 2; ++bj) { const f32x4 v0 = acc[ai][bj][m][0], v1 = acc[ai][bj][m][1];
;                     u32x4 w; w.x = cvt_pk_bf16(v0[0], v0[1]); w.y = cvt_pk_bf16(v0[2], v0[3]); w.z = cvt_pk_bf16(v1[0], v1[1]); w.w = cvt_pk_bf16(v1[2], v1[3]);
;                     *(u32x4*)(rowp + bj * HALF) = w; } }
; template <class Epi, class Sched, bool ALIGN_EPI = false, bool SP2 = false>
; __device__ __forceinline__ void gemm_phase(PG8_LAS unsigned char* lds, const Gemm g, const Sched& S, const Epi& E) {
;     ...
;         if constexpr (ALIGN_EPI) { if (wr == 0) PG8_BAR; }
;         if constexpr (!Epi::AFTER_DRAIN) { E(acc, cur, wr, wc, fr, fq); S.done(cur); }
;         if (PROBE_EPI) { asm volatile("s_waitcnt vmcnt(0)" ::: "memory"); if (tid == 0) *(PG8_LAS unsigned long long*)(lds + 131072 + 8192) += __builtin_amdgcn_s_memrealtime() - pr_e0; }
;         if (!has_next) break;
; #pragma unroll
;         for (int a = 0; a < 2; ++a)
; #pragma unroll
;             for (int b = 0; b < 2; ++b)
; #pragma unroll
;                 for (int m = 0; m < 4; ++m)
; #pragma unroll
;                     for (int n = 0; n < 2; ++n) acc[a][b][m][n] = (f32x4){0.f, 0.f, 0.f, 0.f};
;         cur = nxt; cA = nA; cB = nB; ++ui;
;         if constexpr (ALIGN_EPI) { if (wr == 1) PG8_BAR; }
	s_add_i32 s60, s60, 2
	s_add_u32 s26, s26, 0x100
	s_addc_u32 s27, s27, 0
	s_add_u32 s58, s58, 0x100
	s_addc_u32 s59, s59, 0
	s_cmp_gt_u32 s60, 53
	s_cbranch_scc0 .LBB0_2054
	s_ashr_i32 s26, s57, 31
	s_lshr_b32 s26, s26, 29
	s_add_i32 s26, s57, s26
	s_and_b32 s26, s26, 0xfffff8
	v_lshl_add_u32 v8, s56, 8, v194
	s_sub_i32 s26, s57, s26
	v_lshl_or_b32 v2, s26, 8, v196
	v_ashrrev_i32_e32 v9, 31, v8
	v_ashrrev_i32_e32 v3, 31, v2
	v_lshlrev_b64 v[4:5], 12, v[8:9]
	v_lshl_add_u64 v[4:5], s[8:9], 0, v[4:5]
	v_lshlrev_b64 v[10:11], 1, v[2:3]
	v_lshl_add_u64 v[2:3], v[4:5], 0, v[10:11]
	v_cvt_pk_bf16_f32 v4, v158, v159
	v_cvt_pk_bf16_f32 v5, v160, v161
	v_cvt_pk_bf16_f32 v6, v154, v155
	v_cvt_pk_bf16_f32 v7, v156, v157
	global_store_dwordx4 v[2:3], v[4:7], off
	s_nop 1
	v_cvt_pk_bf16_f32 v4, v146, v147
	v_cvt_pk_bf16_f32 v5, v148, v149
	v_cvt_pk_bf16_f32 v6, v138, v139
	v_cvt_pk_bf16_f32 v7, v140, v141
	global_store_dwordx4 v[2:3], v[4:7], off offset:256
	s_nop 1
	v_or_b32_e32 v4, 16, v8
	v_ashrrev_i32_e32 v5, 31, v4
	v_lshlrev_b64 v[4:5], 12, v[4:5]
	v_lshl_add_u64 v[4:5], s[8:9], 0, v[4:5]
	v_lshl_add_u64 v[12:13], v[4:5], 0, v[10:11]
	v_cvt_pk_bf16_f32 v4, v150, v151
	v_cvt_pk_bf16_f32 v5, v152, v153
	v_cvt_pk_bf16_f32 v6, v142, v143
	v_cvt_pk_bf16_f32 v7, v144, v145
	global_store_dwordx4 v[12:13], v[4:7], off
	s_nop 1
	v_cvt_pk_bf16_f32 v4, v130, v131
	v_cvt_pk_bf16_f32 v5, v132, v133
	v_cvt_pk_bf16_f32 v6, v122, v123
	v_cvt_pk_bf16_f32 v7, v124, v125
	global_store_dwordx4 v[12:13], v[4:7], off offset:256
	s_nop 1
	v_or_b32_e32 v4, 32, v8
	v_ashrrev_i32_e32 v5, 31, v4
	v_lshlrev_b64 v[4:5], 12, v[4:5]
	v_lshl_add_u64 v[4:5], s[8:9], 0, v[4:5]
	v_lshl_add_u64 v[12:13], v[4:5], 0, v[10:11]
	v_cvt_pk_bf16_f32 v4, v134, v135
	v_cvt_pk_bf16_f32 v5, v136, v137
	v_cvt_pk_bf16_f32 v6, v126, v127
	v_cvt_pk_bf16_f32 v7, v128, v129
	global_store_dwordx4 v[12:13], v[4:7], off
	s_nop 1
	v_cvt_pk_bf16_f32 v4, v114, v115
	v_cvt_pk_bf16_f32 v5, v116, v117
	v_cvt_pk_bf16_f32 v6, v106, v107
	v_cvt_pk_bf16_f32 v7, v108, v109
	global_store_dwordx4 v[12:13], v[4:7], off offset:256
	s_nop 1
	v_or_b32_e32 v4, 48, v8
	v_ashrrev_i32_e32 v5, 31, v4
	v_lshlrev_b64 v[4:5], 12, v[4:5]
	v_lshl_add_u64 v[4:5], s[8:9], 0, v[4:5]
	v_lshl_add_u64 v[8:9], v[4:5], 0, v[10:11]
	v_cvt_pk_bf16_f32 v4, v118, v119
	v_cvt_pk_bf16_f32 v5, v120, v121
	v_cvt_pk_bf16_f32 v6, v110, v111
	v_cvt_pk_bf16_f32 v7, v112, v113
	global_store_dwordx4 v[8:9], v[4:7], off
	v_add_co_u32_e32 v10, vcc, s46, v2
	s_nop 0
	v_cvt_pk_bf16_f32 v4, v102, v103
	v_cvt_pk_bf16_f32 v5, v104, v105
	v_cvt_pk_bf16_f32 v6, v98, v99
	v_cvt_pk_bf16_f32 v7, v100, v101
	global_store_dwordx4 v[8:9], v[4:7], off offset:256
	v_addc_co_u32_e32 v11, vcc, 0, v3, vcc
	s_and_b64 vcc, exec, s[14:15]
	s_cbranch_vccz .LBB0_2057
	s_barrier
.LBB0_2057:
	s_nop 0
	v_cvt_pk_bf16_f32 v4, v94, v95
	v_cvt_pk_bf16_f32 v5, v96, v97
	v_cvt_pk_bf16_f32 v6, v90, v91
	v_cvt_pk_bf16_f32 v7, v92, v93
	v_lshl_add_u64 v[8:9], v[2:3], 0, s[16:17]
	global_store_dwordx4 v[10:11], v[4:7], off
	v_add_co_u32_e32 v10, vcc, s47, v2
	s_nop 0
	v_cvt_pk_bf16_f32 v4, v82, v83
	v_cvt_pk_bf16_f32 v5, v84, v85
	v_cvt_pk_bf16_f32 v6, v74, v75
	v_cvt_pk_bf16_f32 v7, v76, v77
	global_store_dwordx4 v[8:9], v[4:7], off offset:256
	v_addc_co_u32_e32 v11, vcc, 0, v3, vcc
	s_nop 0
	v_cvt_pk_bf16_f32 v4, v86, v87
	v_cvt_pk_bf16_f32 v5, v88, v89
	v_cvt_pk_bf16_f32 v6, v78, v79
	v_cvt_pk_bf16_f32 v7, v80, v81
	v_lshl_add_u64 v[8:9], v[2:3], 0, s[18:19]
	global_store_dwordx4 v[10:11], v[4:7], off
	v_add_co_u32_e32 v10, vcc, s52, v2
	s_nop 0
	v_cvt_pk_bf16_f32 v4, v66, v67
	v_cvt_pk_bf16_f32 v5, v68, v69
	v_cvt_pk_bf16_f32 v6, v58, v59
	v_cvt_pk_bf16_f32 v7, v60, v61
	global_store_dwordx4 v[8:9], v[4:7], off offset:256
	v_lshl_add_u64 v[8:9], v[2:3], 0, s[20:21]
	v_addc_co_u32_e32 v11, vcc, 0, v3, vcc
	v_cvt_pk_bf16_f32 v4, v70, v71
	v_cvt_pk_bf16_f32 v5, v72, v73
	v_cvt_pk_bf16_f32 v6, v62, v63
	v_cvt_pk_bf16_f32 v7, v64, v65
	global_store_dwordx4 v[10:11], v[4:7], off
	s_nop 1
	v_cvt_pk_bf16_f32 v4, v50, v51
	v_cvt_pk_bf16_f32 v5, v52, v53
	v_cvt_pk_bf16_f32 v6, v42, v43
	v_cvt_pk_bf16_f32 v7, v44, v45
	global_store_dwordx4 v[8:9], v[4:7], off offset:256
	v_lshl_add_u64 v[8:9], v[2:3], 0, s[22:23]
	v_add_co_u32_e32 v2, vcc, s53, v2
	v_cvt_pk_bf16_f32 v4, v54, v55
	v_cvt_pk_bf16_f32 v5, v56, v57
	v_cvt_pk_bf16_f32 v6, v46, v47
	v_cvt_pk_bf16_f32 v7, v48, v49
	s_nop 1
	v_addc_co_u32_e32 v3, vcc, 0, v3, vcc
	s_and_b64 vcc, exec, s[2:3]
	s_mov_b64 s[2:3], -1
	global_store_dwordx4 v[2:3], v[4:7], off
	v_cvt_pk_bf16_f32 v2, v38, v39
	v_cvt_pk_bf16_f32 v3, v40, v41
	s_nop 1
	v_cvt_pk_bf16_f32 v4, v34, v35
	v_cvt_pk_bf16_f32 v5, v36, v37
	global_store_dwordx4 v[8:9], v[2:5], off offset:256
	s_cbranch_vccnz .LBB0_2046
	s_andn2_b64 vcc, exec, s[6:7]
	s_cbranch_vccnz .LBB0_2045
	s_barrier
	s_branch .LBB0_2045

; #define PG8_STAGE(bufoff, gbase, voff) do { _Pragma("unroll") for (int _i = 0; _i < 2; ++_i) \
;         __builtin_amdgcn_global_load_lds((const unsigned*)((const char*)(gbase) + (voff)[_i]), (PG8_LAS unsigned*)(lds + (bufoff) + ldsw + _i * 8192), 16, 0, 0); } while (0)
; #define PG8_LDA(dst, b, h) do { _Pragma("unroll") for (int m = 0; m < 4; ++m) _Pragma("unroll") for (int k = 0; k < 2; ++k) dst[m][k] = *(const PG8_LAS bf16x8*)(lds + PG8_SA(b, h) + aoff + m * 2048 + k * 1024); } while (0)
; #define PG8_LDB(dst, b, h) do { _Pragma("unroll") for (int n = 0; n < 2; ++n) _Pragma("unroll") for (int k = 0; k < 2; ++k) dst[n][k] = *(const PG8_LAS bf16x8*)(lds + PG8_SB(b, h) + boff + n * 2048 + k * 1024); } while (0)
; #define PG8_WAIT_V(n) asm volatile("s_waitcnt vmcnt(" #n ")" ::: "memory")
; #define PG8_WAIT_L(n) asm volatile("s_waitcnt lgkmcnt(" #n ")" ::: "memory")
; #define PG8_BAR __builtin_amdgcn_s_barrier()
; #define PG8_SCHED __builtin_amdgcn_sched_barrier(0)
; template <class Epi, class Sched, bool ALIGN_EPI = false, bool SP2 = false>
; __device__ __forceinline__ void gemm_phase(PG8_LAS unsigned char* lds, const Gemm g, const Sched& S, const Epi& E) {
;     ...
;             const bool last = (t == nt - 2);
;             const char* a1 = cA + (size_t)(t + 1) * kstep;
;             const char* a2 = last ? nA : cA + (size_t)(t + 2) * kstep; const char* b2 = last ? nB : cB + (size_t)(t + 2) * kstep;
;             const char* a3 = a2 + kstep; const char* b3 = b2 + kstep;
;             if (last && has_next) S.a_ready(nxt);
;             if constexpr (SP2) {
;             PG8_LDB(B0, 0, 0); PG8_LDB(B1, 0, 1); PG8_SCHED; PG8_LDA(At, 0, 0); PG8_STAGE(PG8_SA(1, 1), a1 + hstep, voffA);
;             PG8_WAIT_V(8); PG8_WAIT_L(0); PG8_BAR; PG8_MMA(0, 0, At, B0); PG8_MMA(0, 1, At, B1); PG8_BAR; PG8_SCHED;
;             PG8_LDA(At, 0, 1); PG8_STAGE(PG8_SB(0, 0), b2, voffB); PG8_STAGE(PG8_SB(0, 1), b2 + hstep, voffB); PG8_STAGE(PG8_SA(0, 0), a2, voffA);
;             PG8_WAIT_V(8); PG8_WAIT_L(0); PG8_BAR; PG8_MMA(1, 0, At, B0); PG8_MMA(1, 1, At, B1); PG8_BAR; PG8_SCHED;
.LBB0_2133:
	ds_read_b128 v[26:29], v1
	ds_read_b128 v[30:33], v1 offset:1024
	ds_read_b128 v[18:21], v1 offset:2048
	ds_read_b128 v[22:25], v1 offset:3072
	ds_read_b128 v[10:13], v184
	ds_read_b128 v[14:17], v184 offset:1024
	ds_read_b128 v[2:5], v184 offset:2048
	ds_read_b128 v[6:9], v184 offset:3072
	s_add_u32 s26, s24, 0xfff20080
	s_addc_u32 s27, s25, -1
	s_cmp_eq_u32 s58, 52
	s_cselect_b32 s29, s3, s27
	s_cselect_b32 s28, s2, s26
	s_cselect_b32 s27, s23, s57
	s_cselect_b32 s26, s22, s56
	s_add_i32 m0, s34, 0xc000
	ds_read_b128 v[176:179], v188
	ds_read_b128 v[180:183], v188 offset:1024
	ds_read_b128 v[194:197], v188 offset:2048
	ds_read_b128 v[198:201], v188 offset:3072
	ds_read_b128 v[202:205], v188 offset:4096
	ds_read_b128 v[206:209], v188 offset:5120
	ds_read_b128 v[210:213], v188 offset:6144
	ds_read_b128 v[214:217], v188 offset:7168
	global_load_lds_dwordx4 v170, s[24:25]
	s_add_i32 m0, s34, 0xe000
	s_nop 0
	global_load_lds_dwordx4 v172, s[24:25]
	s_waitcnt vmcnt(8)
	s_waitcnt lgkmcnt(0)
	s_barrier
	s_setprio 1
	s_waitcnt lgkmcnt(0)
	v_mfma_scale_f32_16x16x128_f8f6f4 v[158:161], v[26:33], v[176:183], v[158:161], v187, v192 op_sel_hi:[0,0,0]
	v_mfma_scale_f32_16x16x128_f8f6f4 v[154:157], v[18:25], v[176:183], v[154:157], v187, v192 op_sel_hi:[0,0,0]
	v_mfma_scale_f32_16x16x128_f8f6f4 v[150:153], v[26:33], v[194:201], v[150:153], v187, v192 op_sel_hi:[0,0,0]
	v_mfma_scale_f32_16x16x128_f8f6f4 v[142:145], v[18:25], v[194:201], v[142:145], v187, v192 op_sel_hi:[0,0,0]
	v_mfma_scale_f32_16x16x128_f8f6f4 v[134:137], v[26:33], v[202:209], v[134:137], v187, v192 op_sel_hi:[0,0,0]
	v_mfma_scale_f32_16x16x128_f8f6f4 v[126:129], v[18:25], v[202:209], v[126:129], v187, v192 op_sel_hi:[0,0,0]
	v_mfma_scale_f32_16x16x128_f8f6f4 v[118:121], v[26:33], v[210:217], v[118:121], v187, v192 op_sel_hi:[0,0,0]
	v_mfma_scale_f32_16x16x128_f8f6f4 v[110:113], v[18:25], v[210:217], v[110:113], v187, v192 op_sel_hi:[0,0,0]
	s_setprio 0
	s_setprio 1
	v_mfma_scale_f32_16x16x128_f8f6f4 v[146:149], v[10:17], v[176:183], v[146:149], v187, v192 op_sel_hi:[0,0,0]
	v_mfma_scale_f32_16x16x128_f8f6f4 v[138:141], v[2:9], v[176:183], v[138:141], v187, v192 op_sel_hi:[0,0,0]
	v_mfma_scale_f32_16x16x128_f8f6f4 v[130:133], v[10:17], v[194:201], v[130:133], v187, v192 op_sel_hi:[0,0,0]
	v_mfma_scale_f32_16x16x128_f8f6f4 v[122:125], v[2:9], v[194:201], v[122:125], v187, v192 op_sel_hi:[0,0,0]
	v_mfma_scale_f32_16x16x128_f8f6f4 v[114:117], v[10:17], v[202:209], v[114:117], v187, v192 op_sel_hi:[0,0,0]
	v_mfma_scale_f32_16x16x128_f8f6f4 v[106:109], v[2:9], v[202:209], v[106:109], v187, v192 op_sel_hi:[0,0,0]
	v_mfma_scale_f32_16x16x128_f8f6f4 v[102:105], v[10:17], v[210:217], v[102:105], v187, v192 op_sel_hi:[0,0,0]
	v_mfma_scale_f32_16x16x128_f8f6f4 v[98:101], v[2:9], v[210:217], v[98:101], v187, v192 op_sel_hi:[0,0,0]
	s_setprio 0
	s_barrier
	s_add_i32 s59, s42, s31
	s_mov_b32 m0, s59
	ds_read_b128 v[194:197], v188 offset:16384
	ds_read_b128 v[198:201], v188 offset:17408
	ds_read_b128 v[202:205], v188 offset:18432
	ds_read_b128 v[206:209], v188 offset:19456
	ds_read_b128 v[210:213], v188 offset:20480
	ds_read_b128 v[214:217], v188 offset:21504
	ds_read_b128 v[218:221], v188 offset:22528
	ds_read_b128 v[222:225], v188 offset:23552
	global_load_lds_dwordx4 v164, s[26:27]
	s_add_i32 m0, s59, 0x2000
	s_add_u32 s60, s26, 0xe0000
	s_addc_u32 s61, s27, 0
	s_add_i32 s59, s43, s31
	global_load_lds_dwordx4 v168, s[26:27]
	s_mov_b32 m0, s59
	s_nop 0
	global_load_lds_dwordx4 v164, s[60:61]
	s_add_i32 m0, s59, 0x2000
	s_nop 0
	global_load_lds_dwordx4 v168, s[60:61]
	s_mov_b32 m0, s34
	s_nop 0
	global_load_lds_dwordx4 v162, s[28:29]
	s_mov_b32 m0, s35
	s_nop 0
	global_load_lds_dwordx4 v166, s[28:29]
	s_waitcnt vmcnt(8)
	s_waitcnt lgkmcnt(0)
	s_barrier
	s_setprio 1
	s_waitcnt lgkmcnt(0)
	v_mfma_scale_f32_16x16x128_f8f6f4 v[94:97], v[26:33], v[194:201], v[94:97], v187, v192 op_sel_hi:[0,0,0]
	v_mfma_scale_f32_16x16x128_f8f6f4 v[90:93], v[18:25], v[194:201], v[90:93], v187, v192 op_sel_hi:[0,0,0]
	v_mfma_scale_f32_16x16x128_f8f6f4 v[86:89], v[26:33], v[202:209], v[86:89], v187, v192 op_sel_hi:[0,0,0]
	v_mfma_scale_f32_16x16x128_f8f6f4 v[78:81], v[18:25], v[202:209], v[78:81], v187, v192 op_sel_hi:[0,0,0]
	v_mfma_scale_f32_16x16x128_f8f6f4 v[70:73], v[26:33], v[210:217], v[70:73], v187, v192 op_sel_hi:[0,0,0]
	v_mfma_scale_f32_16x16x128_f8f6f4 v[62:65], v[18:25], v[210:217], v[62:65], v187, v192 op_sel_hi:[0,0,0]
	v_mfma_scale_f32_16x16x128_f8f6f4 v[54:57], v[26:33], v[218:225], v[54:57], v187, v192 op_sel_hi:[0,0,0]
	v_mfma_scale_f32_16x16x128_f8f6f4 v[46:49], v[18:25], v[218:225], v[46:49], v187, v192 op_sel_hi:[0,0,0]
	s_setprio 0
	s_setprio 1
	v_mfma_scale_f32_16x16x128_f8f6f4 v[82:85], v[10:17], v[194:201], v[82:85], v187, v192 op_sel_hi:[0,0,0]
	v_mfma_scale_f32_16x16x128_f8f6f4 v[74:77], v[2:9], v[194:201], v[74:77], v187, v192 op_sel_hi:[0,0,0]
	v_mfma_scale_f32_16x16x128_f8f6f4 v[66:69], v[10:17], v[202:209], v[66:69], v187, v192 op_sel_hi:[0,0,0]
	v_mfma_scale_f32_16x16x128_f8f6f4 v[58:61], v[2:9], v[202:209], v[58:61], v187, v192 op_sel_hi:[0,0,0]
	v_mfma_scale_f32_16x16x128_f8f6f4 v[50:53], v[10:17], v[210:217], v[50:53], v187, v192 op_sel_hi:[0,0,0]
	v_mfma_scale_f32_16x16x128_f8f6f4 v[42:45], v[2:9], v[210:217], v[42:45], v187, v192 op_sel_hi:[0,0,0]
	v_mfma_scale_f32_16x16x128_f8f6f4 v[38:41], v[10:17], v[218:225], v[38:41], v187, v192 op_sel_hi:[0,0,0]
	v_mfma_scale_f32_16x16x128_f8f6f4 v[34:37], v[2:9], v[218:225], v[34:37], v187, v192 op_sel_hi:[0,0,0]
	s_setprio 0
	s_barrier
; #define PG8_STAGE(bufoff, gbase, voff) do { _Pragma("unroll") for (int _i = 0; _i < 2; ++_i) \
;         __builtin_amdgcn_global_load_lds((const unsigned*)((const char*)(gbase) + (voff)[_i]), (PG8_LAS unsigned*)(lds + (bufoff) + ldsw + _i * 8192), 16, 0, 0); } while (0)
; #define PG8_LDA(dst, b, h) do { _Pragma("unroll") for (int m = 0; m < 4; ++m) _Pragma("unroll") for (int k = 0; k < 2; ++k) dst[m][k] = *(const PG8_LAS bf16x8*)(lds + PG8_SA(b, h) + aoff + m * 2048 + k * 1024); } while (0)
; #define PG8_LDB(dst, b, h) do { _Pragma("unroll") for (int n = 0; n < 2; ++n) _Pragma("unroll") for (int k = 0; k < 2; ++k) dst[n][k] = *(const PG8_LAS bf16x8*)(lds + PG8_SB(b, h) + boff + n * 2048 + k * 1024); } while (0)
; #define PG8_WAIT_V(n) asm volatile("s_waitcnt vmcnt(" #n ")" ::: "memory")
; #define PG8_WAIT_L(n) asm volatile("s_waitcnt lgkmcnt(" #n ")" ::: "memory")
; #define PG8_BAR __builtin_amdgcn_s_barrier()
; #define PG8_SCHED __builtin_amdgcn_sched_barrier(0)
; template <class Epi, class Sched, bool ALIGN_EPI = false, bool SP2 = false>
; __device__ __forceinline__ void gemm_phase(PG8_LAS unsigned char* lds, const Gemm g, const Sched& S, const Epi& E) {
;     ...
;             PG8_LDB(B0, 1, 0); PG8_LDB(B1, 1, 1); PG8_SCHED; PG8_LDA(At, 1, 0); PG8_STAGE(PG8_SA(0, 1), a2 + hstep, voffA);
;             PG8_WAIT_V(8); PG8_WAIT_L(0); PG8_BAR; PG8_MMA(0, 0, At, B0); PG8_MMA(0, 1, At, B1); PG8_BAR; PG8_SCHED;
;             PG8_LDA(At, 1, 1); PG8_STAGE(PG8_SB(1, 0), b3, voffB); PG8_STAGE(PG8_SB(1, 1), b3 + hstep, voffB); PG8_STAGE(PG8_SA(1, 0), a3, voffA);
;             PG8_WAIT_V(8); PG8_WAIT_L(0); PG8_BAR; PG8_MMA(1, 0, At, B0); PG8_MMA(1, 1, At, B1); PG8_BAR; PG8_SCHED;
	s_add_i32 s59, 0, 0x18000
	s_add_i32 s60, 0, 0x1c000
	ds_read_b128 v[2:5], v248
	ds_read_b128 v[6:9], v248 offset:1024
	ds_read_b128 v[10:13], v248 offset:2048
	ds_read_b128 v[14:17], v248 offset:3072
	ds_read_b128 v[18:21], v249
	ds_read_b128 v[22:25], v249 offset:1024
	ds_read_b128 v[26:29], v249 offset:2048
	ds_read_b128 v[30:33], v249 offset:3072
	s_add_u32 s28, s28, 0xe0000
	s_addc_u32 s29, s29, 0
	s_mov_b32 m0, s36
	ds_read_b128 v[194:197], v188 offset:32768
	ds_read_b128 v[198:201], v188 offset:33792
	ds_read_b128 v[202:205], v188 offset:34816
	ds_read_b128 v[206:209], v188 offset:35840
	ds_read_b128 v[210:213], v188 offset:36864
	ds_read_b128 v[214:217], v188 offset:37888
	ds_read_b128 v[218:221], v188 offset:38912
	ds_read_b128 v[222:225], v188 offset:39936
	global_load_lds_dwordx4 v162, s[28:29]
	s_mov_b32 m0, s37
	s_nop 0
	global_load_lds_dwordx4 v166, s[28:29]
	s_waitcnt vmcnt(8)
	s_waitcnt lgkmcnt(0)
	s_barrier
	s_setprio 1
	s_waitcnt lgkmcnt(0)
	v_mfma_scale_f32_16x16x128_f8f6f4 v[158:161], v[2:9], v[194:201], v[158:161], v187, v192 op_sel_hi:[0,0,0]
	v_mfma_scale_f32_16x16x128_f8f6f4 v[154:157], v[10:17], v[194:201], v[154:157], v187, v192 op_sel_hi:[0,0,0]
	v_mfma_scale_f32_16x16x128_f8f6f4 v[150:153], v[2:9], v[202:209], v[150:153], v187, v192 op_sel_hi:[0,0,0]
	v_mfma_scale_f32_16x16x128_f8f6f4 v[142:145], v[10:17], v[202:209], v[142:145], v187, v192 op_sel_hi:[0,0,0]
	v_mfma_scale_f32_16x16x128_f8f6f4 v[134:137], v[2:9], v[210:217], v[134:137], v187, v192 op_sel_hi:[0,0,0]
	v_mfma_scale_f32_16x16x128_f8f6f4 v[126:129], v[10:17], v[210:217], v[126:129], v187, v192 op_sel_hi:[0,0,0]
	v_mfma_scale_f32_16x16x128_f8f6f4 v[118:121], v[2:9], v[218:225], v[118:121], v187, v192 op_sel_hi:[0,0,0]
	v_mfma_scale_f32_16x16x128_f8f6f4 v[110:113], v[10:17], v[218:225], v[110:113], v187, v192 op_sel_hi:[0,0,0]
	s_setprio 0
	s_setprio 1
	v_mfma_scale_f32_16x16x128_f8f6f4 v[146:149], v[18:25], v[194:201], v[146:149], v187, v192 op_sel_hi:[0,0,0]
	v_mfma_scale_f32_16x16x128_f8f6f4 v[138:141], v[26:33], v[194:201], v[138:141], v187, v192 op_sel_hi:[0,0,0]
	v_mfma_scale_f32_16x16x128_f8f6f4 v[130:133], v[18:25], v[202:209], v[130:133], v187, v192 op_sel_hi:[0,0,0]
	v_mfma_scale_f32_16x16x128_f8f6f4 v[122:125], v[26:33], v[202:209], v[122:125], v187, v192 op_sel_hi:[0,0,0]
	v_mfma_scale_f32_16x16x128_f8f6f4 v[114:117], v[18:25], v[210:217], v[114:117], v187, v192 op_sel_hi:[0,0,0]
	v_mfma_scale_f32_16x16x128_f8f6f4 v[106:109], v[26:33], v[210:217], v[106:109], v187, v192 op_sel_hi:[0,0,0]
	v_mfma_scale_f32_16x16x128_f8f6f4 v[102:105], v[18:25], v[218:225], v[102:105], v187, v192 op_sel_hi:[0,0,0]
	v_mfma_scale_f32_16x16x128_f8f6f4 v[98:101], v[26:33], v[218:225], v[98:101], v187, v192 op_sel_hi:[0,0,0]
	s_setprio 0
	s_barrier
	s_add_u32 s98, s26, 0x80
	s_addc_u32 s99, s27, 0
	s_add_u32 s100, s28, 0xfff20080
	s_addc_u32 s101, s29, -1
	s_add_i32 s28, s59, s31
	s_mov_b32 m0, s28
	ds_read_b128 v[194:197], v188 offset:49152
	ds_read_b128 v[198:201], v188 offset:50176
	ds_read_b128 v[202:205], v188 offset:51200
	ds_read_b128 v[206:209], v188 offset:52224
	ds_read_b128 v[210:213], v188 offset:53248
	ds_read_b128 v[214:217], v188 offset:54272
	ds_read_b128 v[218:221], v188 offset:55296
	ds_read_b128 v[222:225], v188 offset:56320
	global_load_lds_dwordx4 v164, s[98:99]
	s_add_i32 m0, s28, 0x2000
	s_add_u32 s26, s26, 0xe0080
	s_addc_u32 s27, s27, 0
	s_add_i32 s28, s60, s31
	global_load_lds_dwordx4 v168, s[98:99]
	s_mov_b32 m0, s28
	s_nop 0
	global_load_lds_dwordx4 v164, s[26:27]
	s_add_i32 m0, s28, 0x2000
	s_nop 0
	global_load_lds_dwordx4 v168, s[26:27]
	s_mov_b32 m0, s39
	s_nop 0
	global_load_lds_dwordx4 v162, s[100:101]
	s_mov_b32 m0, s40
	s_nop 0
	global_load_lds_dwordx4 v166, s[100:101]
	s_waitcnt vmcnt(8)
	s_waitcnt lgkmcnt(0)
	s_barrier
	s_setprio 1
	s_waitcnt lgkmcnt(0)
	v_mfma_scale_f32_16x16x128_f8f6f4 v[94:97], v[2:9], v[194:201], v[94:97], v187, v192 op_sel_hi:[0,0,0]
	v_mfma_scale_f32_16x16x128_f8f6f4 v[90:93], v[10:17], v[194:201], v[90:93], v187, v192 op_sel_hi:[0,0,0]
	v_mfma_scale_f32_16x16x128_f8f6f4 v[86:89], v[2:9], v[202:209], v[86:89], v187, v192 op_sel_hi:[0,0,0]
	v_mfma_scale_f32_16x16x128_f8f6f4 v[78:81], v[10:17], v[202:209], v[78:81], v187, v192 op_sel_hi:[0,0,0]
	v_mfma_scale_f32_16x16x128_f8f6f4 v[70:73], v[2:9], v[210:217], v[70:73], v187, v192 op_sel_hi:[0,0,0]
	v_mfma_scale_f32_16x16x128_f8f6f4 v[62:65], v[10:17], v[210:217], v[62:65], v187, v192 op_sel_hi:[0,0,0]
	v_mfma_scale_f32_16x16x128_f8f6f4 v[54:57], v[2:9], v[218:225], v[54:57], v187, v192 op_sel_hi:[0,0,0]
	v_mfma_scale_f32_16x16x128_f8f6f4 v[46:49], v[10:17], v[218:225], v[46:49], v187, v192 op_sel_hi:[0,0,0]
	s_setprio 0
	s_setprio 1
	v_mfma_scale_f32_16x16x128_f8f6f4 v[82:85], v[18:25], v[194:201], v[82:85], v187, v192 op_sel_hi:[0,0,0]
	v_mfma_scale_f32_16x16x128_f8f6f4 v[74:77], v[26:33], v[194:201], v[74:77], v187, v192 op_sel_hi:[0,0,0]
	v_mfma_scale_f32_16x16x128_f8f6f4 v[66:69], v[18:25], v[202:209], v[66:69], v187, v192 op_sel_hi:[0,0,0]
	v_mfma_scale_f32_16x16x128_f8f6f4 v[58:61], v[26:33], v[202:209], v[58:61], v187, v192 op_sel_hi:[0,0,0]
	v_mfma_scale_f32_16x16x128_f8f6f4 v[50:53], v[18:25], v[210:217], v[50:53], v187, v192 op_sel_hi:[0,0,0]
	v_mfma_scale_f32_16x16x128_f8f6f4 v[42:45], v[26:33], v[210:217], v[42:45], v187, v192 op_sel_hi:[0,0,0]
	v_mfma_scale_f32_16x16x128_f8f6f4 v[38:41], v[18:25], v[218:225], v[38:41], v187, v192 op_sel_hi:[0,0,0]
	v_mfma_scale_f32_16x16x128_f8f6f4 v[34:37], v[26:33], v[218:225], v[34:37], v187, v192 op_sel_hi:[0,0,0]
	s_setprio 0
	s_barrier
; #define PG8_LAS __attribute__((address_space(3)))
; __device__ __forceinline__ unsigned cvt_pk_bf16(float lo, float hi) { unsigned r; asm volatile("v_cvt_pk_bf16_f32 %0, %1, %2" : "=v"(r) : "v"(lo), "v"(hi)); return r; }
; #define PG8_BAR __builtin_amdgcn_s_barrier()
;     __device__ __forceinline__ void operator()(const f32x4 (&acc)[2][2][4][2], const Unit& u, int wr, int wc, int fr, int fq) const {
;         const int row0 = u.pm * BM + wr * 64 + fr, col0 = (u.pn % nN) * BM + wc * 32 + 8 * fq;
; #pragma unroll
;         for (int ai = 0; ai < 2; ++ai)
; #pragma unroll
;             for (int m = 0; m < 4; ++m) { bf16_t* rowp = O + (size_t)(row0 + ai * HALF + m * 16) * ldc + col0;
; #pragma unroll
;                 for (int bj = 0; bj < 2; ++bj) { const f32x4 v0 = acc[ai][bj][m][0], v1 = acc[ai][bj][m][1];
;                     u32x4 w; w.x = cvt_pk_bf16(v0[0], v0[1]); w.y = cvt_pk_bf16(v0[2], v0[3]); w.z = cvt_pk_bf16(v1[0], v1[1]); w.w = cvt_pk_bf16(v1[2], v1[3]);
;                     *(u32x4*)(rowp + bj * HALF) = w; } }
; template <class Epi, class Sched, bool ALIGN_EPI = false, bool SP2 = false>
; __device__ __forceinline__ void gemm_phase(PG8_LAS unsigned char* lds, const Gemm g, const Sched& S, const Epi& E) {
;     ...
;         if constexpr (ALIGN_EPI) { if (wr == 0) PG8_BAR; }
;         if constexpr (!Epi::AFTER_DRAIN) { E(acc, cur, wr, wc, fr, fq); S.done(cur); }
;         if (PROBE_EPI) { asm volatile("s_waitcnt vmcnt(0)" ::: "memory"); if (tid == 0) *(PG8_LAS unsigned long long*)(lds + 131072 + 8192) += __builtin_amdgcn_s_memrealtime() - pr_e0; }
;         if (!has_next) break;
; #pragma unroll
;         for (int a = 0; a < 2; ++a)
; #pragma unroll
;             for (int b = 0; b < 2; ++b)
; #pragma unroll
;                 for (int m = 0; m < 4; ++m)
; #pragma unroll
;                     for (int n = 0; n < 2; ++n) acc[a][b][m][n] = (f32x4){0.f, 0.f, 0.f, 0.f};
;         cur = nxt; cA = nA; cB = nB; ++ui;
;         if constexpr (ALIGN_EPI) { if (wr == 1) PG8_BAR; }
	s_add_i32 s58, s58, 2
	s_add_u32 s24, s24, 0x100
	s_addc_u32 s25, s25, 0
	s_add_u32 s56, s56, 0x100
	s_addc_u32 s57, s57, 0
	s_cmp_gt_u32 s58, 53
	s_cbranch_scc0 .LBB0_2133
	s_ashr_i32 s24, s55, 31
	s_lshr_b32 s24, s24, 29
	s_add_i32 s24, s55, s24
	s_and_b32 s24, s24, 0xfffff8
	v_lshl_add_u32 v8, s54, 8, v193
	s_sub_i32 s24, s55, s24
	v_lshl_or_b32 v2, s24, 8, v185
	v_ashrrev_i32_e32 v9, 31, v8
	v_ashrrev_i32_e32 v3, 31, v2
	v_lshlrev_b64 v[4:5], 12, v[8:9]
	v_lshl_add_u64 v[4:5], s[8:9], 0, v[4:5]
	v_lshlrev_b64 v[10:11], 1, v[2:3]
	v_lshl_add_u64 v[2:3], v[4:5], 0, v[10:11]
	v_cvt_pk_bf16_f32 v4, v158, v159
	v_cvt_pk_bf16_f32 v5, v160, v161
	v_cvt_pk_bf16_f32 v6, v154, v155
	v_cvt_pk_bf16_f32 v7, v156, v157
	global_store_dwordx4 v[2:3], v[4:7], off
	s_nop 1
	v_cvt_pk_bf16_f32 v4, v146, v147
	v_cvt_pk_bf16_f32 v5, v148, v149
	v_cvt_pk_bf16_f32 v6, v138, v139
	v_cvt_pk_bf16_f32 v7, v140, v141
	global_store_dwordx4 v[2:3], v[4:7], off offset:256
	s_nop 1
	v_or_b32_e32 v4, 16, v8
	v_ashrrev_i32_e32 v5, 31, v4
	v_lshlrev_b64 v[4:5], 12, v[4:5]
	v_lshl_add_u64 v[4:5], s[8:9], 0, v[4:5]
	v_lshl_add_u64 v[12:13], v[4:5], 0, v[10:11]
	v_cvt_pk_bf16_f32 v4, v150, v151
	v_cvt_pk_bf16_f32 v5, v152, v153
	v_cvt_pk_bf16_f32 v6, v142, v143
	v_cvt_pk_bf16_f32 v7, v144, v145
	global_store_dwordx4 v[12:13], v[4:7], off
	s_nop 1
	v_cvt_pk_bf16_f32 v4, v130, v131
	v_cvt_pk_bf16_f32 v5, v132, v133
	v_cvt_pk_bf16_f32 v6, v122, v123
	v_cvt_pk_bf16_f32 v7, v124, v125
	global_store_dwordx4 v[12:13], v[4:7], off offset:256
	s_nop 1
	v_or_b32_e32 v4, 32, v8
	v_ashrrev_i32_e32 v5, 31, v4
	v_lshlrev_b64 v[4:5], 12, v[4:5]
	v_lshl_add_u64 v[4:5], s[8:9], 0, v[4:5]
	v_lshl_add_u64 v[12:13], v[4:5], 0, v[10:11]
	v_cvt_pk_bf16_f32 v4, v134, v135
	v_cvt_pk_bf16_f32 v5, v136, v137
	v_cvt_pk_bf16_f32 v6, v126, v127
	v_cvt_pk_bf16_f32 v7, v128, v129
	global_store_dwordx4 v[12:13], v[4:7], off
	s_nop 1
	v_cvt_pk_bf16_f32 v4, v114, v115
	v_cvt_pk_bf16_f32 v5, v116, v117
	v_cvt_pk_bf16_f32 v6, v106, v107
	v_cvt_pk_bf16_f32 v7, v108, v109
	global_store_dwordx4 v[12:13], v[4:7], off offset:256
	s_nop 1
	v_or_b32_e32 v4, 48, v8
	v_ashrrev_i32_e32 v5, 31, v4
	v_lshlrev_b64 v[4:5], 12, v[4:5]
	v_lshl_add_u64 v[4:5], s[8:9], 0, v[4:5]
	v_lshl_add_u64 v[8:9], v[4:5], 0, v[10:11]
	v_cvt_pk_bf16_f32 v4, v118, v119
	v_cvt_pk_bf16_f32 v5, v120, v121
	v_cvt_pk_bf16_f32 v6, v110, v111
	v_cvt_pk_bf16_f32 v7, v112, v113
	global_store_dwordx4 v[8:9], v[4:7], off
	v_add_co_u32_e32 v10, vcc, s44, v2
	s_nop 0
	v_cvt_pk_bf16_f32 v4, v102, v103
	v_cvt_pk_bf16_f32 v5, v104, v105
	v_cvt_pk_bf16_f32 v6, v98, v99
	v_cvt_pk_bf16_f32 v7, v100, v101
	global_store_dwordx4 v[8:9], v[4:7], off offset:256
	v_addc_co_u32_e32 v11, vcc, 0, v3, vcc
	s_and_b64 vcc, exec, s[12:13]
	s_cbranch_vccz .LBB0_2136
	s_barrier
.LBB0_2136:
	s_nop 0
	v_cvt_pk_bf16_f32 v4, v94, v95
	v_cvt_pk_bf16_f32 v5, v96, v97
	v_cvt_pk_bf16_f32 v6, v90, v91
	v_cvt_pk_bf16_f32 v7, v92, v93
	v_lshl_add_u64 v[8:9], v[2:3], 0, s[14:15]
	global_store_dwordx4 v[10:11], v[4:7], off
	v_add_co_u32_e32 v10, vcc, s45, v2
	s_nop 0
	v_cvt_pk_bf16_f32 v4, v82, v83
	v_cvt_pk_bf16_f32 v5, v84, v85
	v_cvt_pk_bf16_f32 v6, v74, v75
	v_cvt_pk_bf16_f32 v7, v76, v77
	global_store_dwordx4 v[8:9], v[4:7], off offset:256
	v_addc_co_u32_e32 v11, vcc, 0, v3, vcc
	s_nop 0
	v_cvt_pk_bf16_f32 v4, v86, v87
	v_cvt_pk_bf16_f32 v5, v88, v89
	v_cvt_pk_bf16_f32 v6, v78, v79
	v_cvt_pk_bf16_f32 v7, v80, v81
	v_lshl_add_u64 v[8:9], v[2:3], 0, s[16:17]
	global_store_dwordx4 v[10:11], v[4:7], off
	v_add_co_u32_e32 v10, vcc, s46, v2
	s_nop 0
	v_cvt_pk_bf16_f32 v4, v66, v67
	v_cvt_pk_bf16_f32 v5, v68, v69
	v_cvt_pk_bf16_f32 v6, v58, v59
	v_cvt_pk_bf16_f32 v7, v60, v61
	global_store_dwordx4 v[8:9], v[4:7], off offset:256
	v_lshl_add_u64 v[8:9], v[2:3], 0, s[18:19]
	v_addc_co_u32_e32 v11, vcc, 0, v3, vcc
	v_cvt_pk_bf16_f32 v4, v70, v71
	v_cvt_pk_bf16_f32 v5, v72, v73
	v_cvt_pk_bf16_f32 v6, v62, v63
	v_cvt_pk_bf16_f32 v7, v64, v65
	global_store_dwordx4 v[10:11], v[4:7], off
	s_nop 1
	v_cvt_pk_bf16_f32 v4, v50, v51
	v_cvt_pk_bf16_f32 v5, v52, v53
	v_cvt_pk_bf16_f32 v6, v42, v43
	v_cvt_pk_bf16_f32 v7, v44, v45
	global_store_dwordx4 v[8:9], v[4:7], off offset:256
	v_lshl_add_u64 v[8:9], v[2:3], 0, s[20:21]
	v_add_co_u32_e32 v2, vcc, s47, v2
	v_cvt_pk_bf16_f32 v4, v54, v55
	v_cvt_pk_bf16_f32 v5, v56, v57
	v_cvt_pk_bf16_f32 v6, v46, v47
	v_cvt_pk_bf16_f32 v7, v48, v49
	s_nop 1
	v_addc_co_u32_e32 v3, vcc, 0, v3, vcc
	s_and_b64 vcc, exec, s[0:1]
	s_mov_b64 s[0:1], -1
	global_store_dwordx4 v[2:3], v[4:7], off
	v_cvt_pk_bf16_f32 v2, v38, v39
	v_cvt_pk_bf16_f32 v3, v40, v41
	s_nop 1
	v_cvt_pk_bf16_f32 v4, v34, v35
	v_cvt_pk_bf16_f32 v5, v36, v37
	global_store_dwordx4 v[8:9], v[2:5], off offset:256
	s_cbranch_vccnz .LBB0_2125
	s_andn2_b64 vcc, exec, s[4:5]
	s_cbranch_vccnz .LBB0_2124
	s_barrier
	s_branch .LBB0_2124
